# H rows (GEMM A operands written by the norm phases 1, 5, 13) stored write-through
# speedup vs baseline: 1.0080x; 1.0049x over previous
; #define LAS __attribute__((address_space(3)))
; template <int R, bool RT = false>
; __device__ __forceinline__ void norm_phase(const NormArgs& a, LAS unsigned char* lds, bool ctx_rows, const float* ctx_src, const float* ctx_shift, const float* ctx_scale) {
;     ...
;             for (int q = 0; q < R; ++q) { const int row = row0 + rr + q;
;                 if (a.src16) { const f16* xr = a.src16 + (size_t)row * DM;
; #pragma unroll
;                     for (int j = 0; j < 4; ++j) { const f16x4 t = *(const f16x4*)(xr + 4 * lane + 256 * j); v[q][j] = (f32x4){(float)t[0], (float)t[1], (float)t[2], (float)t[3]};
;                         if constexpr (RT) { if (j == 0) *(LAS u32x2*)(hs + (rr + q) * 528 + 8 * lane) = __builtin_bit_cast(u32x2, t);
;                             else xp[rr / 4][q][j - 1] = __builtin_bit_cast(u32x2, t); } } }
;                 else { const float* xr = a.src + (size_t)row * DM;
; #pragma unroll
;                     for (int j = 0; j < 4; ++j) v[q][j] = *(const f32x4*)(xr + 4 * lane + 256 * j); } }
;     ...
;             for (int q = 0; q < R; ++q) { float ss = 0.f;
; #pragma unroll
;                 for (int j = 0; j < 4; ++j) ss += (v[q][j][0] * v[q][j][0] + v[q][j][1] * v[q][j][1]) + (v[q][j][2] * v[q][j][2] + v[q][j][3] * v[q][j][3]);
;                 rstd[q] = __builtin_amdgcn_rsqf(wave_sum(ss) * (1.f / DM) + EPS);
.LBB0_308:
	v_lshl_add_u64 v[18:19], s[16:17], 0, v[30:31]
	v_lshl_add_u64 v[20:21], s[22:23], 0, v[30:31]
	v_lshl_add_u64 v[48:49], s[28:29], 0, v[30:31]
	v_lshl_add_u64 v[50:51], s[20:21], 0, v[30:31]
	global_load_dwordx4 v[68:71], v[18:19], off nt
	global_load_dwordx4 v[72:75], v[18:19], off offset:1024 nt
	global_load_dwordx4 v[76:79], v[18:19], off offset:3072 nt
	global_load_dwordx4 v[80:83], v[18:19], off offset:2048 nt
	global_load_dwordx4 v[84:87], v[20:21], off nt
	global_load_dwordx4 v[88:91], v[20:21], off offset:1024 nt
	global_load_dwordx4 v[92:95], v[20:21], off offset:3072 nt
	global_load_dwordx4 v[96:99], v[20:21], off offset:2048 nt
	global_load_dwordx4 v[100:103], v[48:49], off nt
	global_load_dwordx4 v[104:107], v[48:49], off offset:1024 nt
	global_load_dwordx4 v[108:111], v[48:49], off offset:3072 nt
	global_load_dwordx4 v[112:115], v[48:49], off offset:2048 nt
	global_load_dwordx4 v[116:119], v[50:51], off nt
	global_load_dwordx4 v[120:123], v[50:51], off offset:1024 nt
	global_load_dwordx4 v[18:21], v[50:51], off offset:3072 nt
	global_load_dwordx4 v[124:127], v[50:51], off offset:2048 nt
	v_lshl_add_u64 v[52:53], s[14:15], 0, v[22:23]
	v_add_co_u32_e32 v54, vcc, s7, v52
	v_lshl_add_u64 v[128:129], s[18:19], 0, v[22:23]
	s_nop 0
	v_addc_co_u32_e32 v55, vcc, 0, v53, vcc
	v_add_co_u32_e32 v52, vcc, s7, v128
	v_lshl_add_u64 v[130:131], s[24:25], 0, v[22:23]
	s_nop 0
	v_addc_co_u32_e32 v53, vcc, 0, v129, vcc
	v_add_co_u32_e32 v50, vcc, s7, v130
	v_lshl_add_u64 v[132:133], s[26:27], 0, v[22:23]
	s_nop 0
	v_addc_co_u32_e32 v51, vcc, 0, v131, vcc
	v_add_co_u32_e32 v48, vcc, s7, v132
	s_add_u32 s14, s14, 0x2000
	s_nop 0
	v_addc_co_u32_e32 v49, vcc, 0, v133, vcc
	s_addc_u32 s15, s15, 0
	s_add_i32 s3, s3, 4
	s_add_u32 s16, s16, 0x4000
	v_mov_b32_e32 v61, 0
	s_addc_u32 s17, s17, 0
	v_mov_b32_e32 v63, 0
	v_mov_b32_e32 v65, 0
	v_mov_b32_e32 v67, 0
	s_add_u32 s18, s18, 0x2000
	v_mov_b32_e32 v60, 0
	s_addc_u32 s19, s19, 0
	v_mov_b32_e32 v62, 0
	v_mov_b32_e32 v64, 0
	v_mov_b32_e32 v66, 0
	s_add_u32 s20, s20, 0x4000
	s_addc_u32 s21, s21, 0
	s_add_u32 s22, s22, 0x4000
	s_addc_u32 s23, s23, 0
	s_add_u32 s24, s24, 0x2000
	s_addc_u32 s25, s25, 0
	s_add_u32 s26, s26, 0x2000
	s_addc_u32 s27, s27, 0
	s_add_u32 s28, s28, 0x4000
	s_addc_u32 s29, s29, 0
	s_cmp_gt_u32 s3, 11
	s_waitcnt vmcnt(15)
	v_pk_mul_f32 v[128:129], v[70:71], v[70:71]
	v_pk_mul_f32 v[130:131], v[68:69], v[68:69]
	s_waitcnt vmcnt(14)
	v_pk_mul_f32 v[132:133], v[74:75], v[74:75]
	v_pk_mul_f32 v[134:135], v[72:73], v[72:73]
	s_waitcnt vmcnt(12)
	v_mul_f32_e32 v136, v81, v81
	v_mul_f32_e32 v138, v83, v83
	s_waitcnt vmcnt(11)
	v_pk_mul_f32 v[140:141], v[86:87], v[86:87]
	v_pk_mul_f32 v[142:143], v[84:85], v[84:85]
	s_waitcnt vmcnt(10)
	v_pk_mul_f32 v[144:145], v[90:91], v[90:91]
	v_pk_mul_f32 v[146:147], v[88:89], v[88:89]
	s_waitcnt vmcnt(8)
	v_mul_f32_e32 v148, v97, v97
	v_mul_f32_e32 v150, v99, v99
	s_waitcnt vmcnt(7)
	v_pk_mul_f32 v[152:153], v[102:103], v[102:103]
	v_pk_mul_f32 v[154:155], v[100:101], v[100:101]
	s_waitcnt vmcnt(6)
	v_pk_mul_f32 v[156:157], v[106:107], v[106:107]
	v_pk_mul_f32 v[158:159], v[104:105], v[104:105]
	s_waitcnt vmcnt(4)
	v_mul_f32_e32 v160, v113, v113
	v_mul_f32_e32 v162, v115, v115
	s_waitcnt vmcnt(3)
	v_pk_mul_f32 v[164:165], v[118:119], v[118:119]
	v_pk_mul_f32 v[166:167], v[116:117], v[116:117]
	s_waitcnt vmcnt(2)
	v_pk_mul_f32 v[168:169], v[122:123], v[122:123]
	v_pk_mul_f32 v[170:171], v[120:121], v[120:121]
	v_pk_mov_b32 v[176:177], v[130:131], v[128:129] op_sel:[1,0]
	v_mov_b32_e32 v131, v129
	v_pk_mov_b32 v[128:129], v[134:135], v[132:133] op_sel:[1,0]
	v_mov_b32_e32 v135, v133
	v_mul_f32_e32 v179, v78, v78
	v_mul_f32_e32 v180, v79, v79
	v_mul_f32_e32 v183, v94, v94
	v_mul_f32_e32 v184, v95, v95
	v_pk_fma_f32 v[132:133], v[80:81], v[80:81], v[136:137] op_sel_hi:[1,1,0]
	v_pk_fma_f32 v[136:137], v[82:83], v[82:83], v[138:139] op_sel_hi:[1,1,0]
	v_pk_mov_b32 v[138:139], v[142:143], v[140:141] op_sel:[1,0]
	v_mov_b32_e32 v143, v141
	v_pk_mov_b32 v[140:141], v[146:147], v[144:145] op_sel:[1,0]
	v_mov_b32_e32 v147, v145
	v_pk_fma_f32 v[144:145], v[96:97], v[96:97], v[148:149] op_sel_hi:[1,1,0]
	v_pk_fma_f32 v[148:149], v[98:99], v[98:99], v[150:151] op_sel_hi:[1,1,0]
	v_pk_mov_b32 v[150:151], v[154:155], v[152:153] op_sel:[1,0]
	v_mov_b32_e32 v155, v153
	v_pk_mov_b32 v[152:153], v[158:159], v[156:157] op_sel:[1,0]
	v_mov_b32_e32 v159, v157
	v_pk_fma_f32 v[156:157], v[112:113], v[112:113], v[160:161] op_sel_hi:[1,1,0]
	v_pk_fma_f32 v[160:161], v[114:115], v[114:115], v[162:163] op_sel_hi:[1,1,0]
	v_pk_mov_b32 v[162:163], v[166:167], v[164:165] op_sel:[1,0]
	v_mov_b32_e32 v167, v165
	v_pk_mov_b32 v[164:165], v[170:171], v[168:169] op_sel:[1,0]
	v_mov_b32_e32 v171, v169
	v_pk_add_f32 v[130:131], v[176:177], v[130:131]
	v_pk_add_f32 v[128:129], v[128:129], v[134:135]
	v_mul_f32_e32 v175, v76, v76
	v_mul_f32_e32 v178, v77, v77
	s_waitcnt vmcnt(0)
; #define WS_DPP(x, ctrl, rmask) __builtin_bit_cast(float, __builtin_amdgcn_update_dpp(0, __builtin_bit_cast(int, x), ctrl, rmask, 0xF, false))
; __device__ __forceinline__ float wave_sum(float v) {
;     ...
;     v += WS_DPP(v, 0xB1, 0xF);
;     v += WS_DPP(v, 0x4E, 0xF);
;     v += WS_DPP(v, 0x141, 0xF);
;     v += WS_DPP(v, 0x140, 0xF);
;     v += WS_DPP(v, 0x142, 0xA);
;     v += WS_DPP(v, 0x143, 0xC);
;     ...
;     return __builtin_bit_cast(float, __builtin_amdgcn_readlane(__builtin_bit_cast(int, v), 63));
; template <int R, bool RT = false>
; __device__ __forceinline__ void norm_phase(const NormArgs& a, LAS unsigned char* lds, bool ctx_rows, const float* ctx_src, const float* ctx_shift, const float* ctx_scale) {
;     ...
;             for (int q = 0; q < R; ++q) { float ss = 0.f;
; #pragma unroll
;                 for (int j = 0; j < 4; ++j) ss += (v[q][j][0] * v[q][j][0] + v[q][j][1] * v[q][j][1]) + (v[q][j][2] * v[q][j][2] + v[q][j][3] * v[q][j][3]);
;                 rstd[q] = __builtin_amdgcn_rsqf(wave_sum(ss) * (1.f / DM) + EPS);
;                 if constexpr (RT) rsel[q] = ((lane >> 4) == rr / 4) ? rstd[q] : rsel[q]; }
; #pragma unroll
;             for (int q = 0; q < R; ++q) { const int row = row0 + rr + q;
; #pragma unroll
;                 for (int j = 0; j < 4; ++j) v[q][j] = (v[q][j] * rstd[q]) * A[j] + Sh[j];
	v_mul_f32_e32 v172, v125, v125
	v_mul_f32_e32 v174, v127, v127
	v_mov_b32_e32 v133, v179
	v_mov_b32_e32 v137, v180
	v_pk_add_f32 v[134:135], v[138:139], v[142:143]
	v_pk_add_f32 v[138:139], v[140:141], v[146:147]
	v_mov_b32_e32 v145, v183
	v_mov_b32_e32 v149, v184
	v_pk_add_f32 v[140:141], v[150:151], v[154:155]
	v_pk_add_f32 v[142:143], v[152:153], v[158:159]
	v_pk_add_f32 v[146:147], v[162:163], v[166:167]
	v_pk_add_f32 v[150:151], v[164:165], v[170:171]
	v_pk_add_f32 v[130:131], v[130:131], v[130:131] op_sel:[0,1] op_sel_hi:[1,0]
	v_pk_add_f32 v[128:129], v[128:129], v[128:129] op_sel:[0,1] op_sel_hi:[1,0]
	v_mul_f32_e32 v181, v92, v92
	v_mul_f32_e32 v182, v93, v93
	v_mul_f32_e32 v185, v108, v108
	v_mul_f32_e32 v186, v109, v109
	v_mul_f32_e32 v187, v110, v110
	v_mul_f32_e32 v188, v111, v111
	v_mul_f32_e32 v189, v18, v18
	v_mul_f32_e32 v190, v19, v19
	v_mul_f32_e32 v191, v20, v20
	v_mul_f32_e32 v192, v21, v21
	v_pk_fma_f32 v[168:169], v[124:125], v[124:125], v[172:173] op_sel_hi:[1,1,0]
	v_pk_fma_f32 v[172:173], v[126:127], v[126:127], v[174:175] op_sel_hi:[1,1,0]
	v_pk_add_f32 v[132:133], v[132:133], v[136:137]
	v_pk_add_f32 v[134:135], v[134:135], v[134:135] op_sel:[0,1] op_sel_hi:[1,0]
	v_pk_add_f32 v[136:137], v[138:139], v[138:139] op_sel:[0,1] op_sel_hi:[1,0]
	v_pk_add_f32 v[138:139], v[144:145], v[148:149]
	v_pk_add_f32 v[140:141], v[140:141], v[140:141] op_sel:[0,1] op_sel_hi:[1,0]
	v_pk_add_f32 v[142:143], v[142:143], v[142:143] op_sel:[0,1] op_sel_hi:[1,0]
	v_pk_add_f32 v[146:147], v[146:147], v[146:147] op_sel:[0,1] op_sel_hi:[1,0]
	v_pk_add_f32 v[148:149], v[150:151], v[150:151] op_sel:[0,1] op_sel_hi:[1,0]
	v_mov_b32_e32 v131, v175
	v_mov_b32_e32 v129, v178
	v_mov_b32_e32 v157, v187
	v_mov_b32_e32 v161, v188
	v_mov_b32_e32 v169, v191
	v_mov_b32_e32 v173, v192
	v_mov_b32_e32 v135, v181
	v_mov_b32_e32 v137, v182
	v_mov_b32_e32 v141, v185
	v_mov_b32_e32 v143, v186
	v_mov_b32_e32 v147, v189
	v_mov_b32_e32 v149, v190
	v_pk_add_f32 v[128:129], v[130:131], v[128:129]
	v_pk_add_f32 v[144:145], v[156:157], v[160:161]
	v_pk_add_f32 v[150:151], v[168:169], v[172:173]
	v_pk_add_f32 v[130:131], v[134:135], v[136:137]
	v_pk_add_f32 v[134:135], v[140:141], v[142:143]
	v_pk_add_f32 v[136:137], v[146:147], v[148:149]
	v_pk_add_f32 v[128:129], v[128:129], v[132:133]
	v_pk_add_f32 v[130:131], v[130:131], v[138:139]
	v_pk_add_f32 v[132:133], v[134:135], v[144:145]
	v_pk_add_f32 v[134:135], v[136:137], v[150:151]
	v_add_f32_e32 v128, v128, v129
	v_add_f32_e32 v129, v130, v131
	v_add_f32_e32 v130, v132, v133
	v_add_f32_e32 v131, v134, v135
	v_add_f32_dpp v128, v128, v128 quad_perm:[1,0,3,2] row_mask:0xf bank_mask:0xf bound_ctrl:1
	v_add_f32_dpp v129, v129, v129 quad_perm:[1,0,3,2] row_mask:0xf bank_mask:0xf bound_ctrl:1
	v_add_f32_dpp v130, v130, v130 quad_perm:[1,0,3,2] row_mask:0xf bank_mask:0xf bound_ctrl:1
	v_add_f32_dpp v131, v131, v131 quad_perm:[1,0,3,2] row_mask:0xf bank_mask:0xf bound_ctrl:1
	v_add_f32_dpp v128, v128, v128 quad_perm:[2,3,0,1] row_mask:0xf bank_mask:0xf bound_ctrl:1
	v_add_f32_dpp v129, v129, v129 quad_perm:[2,3,0,1] row_mask:0xf bank_mask:0xf bound_ctrl:1
	v_add_f32_dpp v130, v130, v130 quad_perm:[2,3,0,1] row_mask:0xf bank_mask:0xf bound_ctrl:1
	v_add_f32_dpp v131, v131, v131 quad_perm:[2,3,0,1] row_mask:0xf bank_mask:0xf bound_ctrl:1
	v_add_f32_dpp v128, v128, v128 row_half_mirror row_mask:0xf bank_mask:0xf bound_ctrl:1
	v_add_f32_dpp v129, v129, v129 row_half_mirror row_mask:0xf bank_mask:0xf bound_ctrl:1
	v_add_f32_dpp v130, v130, v130 row_half_mirror row_mask:0xf bank_mask:0xf bound_ctrl:1
	v_add_f32_dpp v131, v131, v131 row_half_mirror row_mask:0xf bank_mask:0xf bound_ctrl:1
	v_add_f32_dpp v128, v128, v128 row_mirror row_mask:0xf bank_mask:0xf bound_ctrl:1
	v_add_f32_dpp v129, v129, v129 row_mirror row_mask:0xf bank_mask:0xf bound_ctrl:1
	v_add_f32_dpp v130, v130, v130 row_mirror row_mask:0xf bank_mask:0xf bound_ctrl:1
	v_add_f32_dpp v131, v131, v131 row_mirror row_mask:0xf bank_mask:0xf bound_ctrl:1
	v_mov_b32_dpp v61, v128 row_bcast:15 row_mask:0xa bank_mask:0xf
	v_mov_b32_dpp v63, v129 row_bcast:15 row_mask:0xa bank_mask:0xf
	v_mov_b32_dpp v65, v130 row_bcast:15 row_mask:0xa bank_mask:0xf
	v_mov_b32_dpp v67, v131 row_bcast:15 row_mask:0xa bank_mask:0xf
	v_add_f32_e32 v61, v128, v61
	v_add_f32_e32 v63, v129, v63
	v_add_f32_e32 v65, v130, v65
	v_add_f32_e32 v67, v131, v67
	v_mov_b32_dpp v60, v61 row_bcast:31 row_mask:0xc bank_mask:0xf
	v_mov_b32_dpp v62, v63 row_bcast:31 row_mask:0xc bank_mask:0xf
	v_mov_b32_dpp v64, v65 row_bcast:31 row_mask:0xc bank_mask:0xf
	v_mov_b32_dpp v66, v67 row_bcast:31 row_mask:0xc bank_mask:0xf
	v_add_f32_e32 v60, v61, v60
	v_add_f32_e32 v61, v63, v62
	v_add_f32_e32 v62, v65, v64
	v_add_f32_e32 v63, v67, v66
	v_readlane_b32 s9, v60, 63
	v_readlane_b32 s11, v61, 63
	v_readlane_b32 s13, v62, 63
	v_readlane_b32 s31, v63, 63
	v_fma_f32 v60, s9, v59, v58
	v_fma_f32 v61, s11, v59, v58
	v_fma_f32 v63, s13, v59, v58
	v_fma_f32 v65, s31, v59, v58
	v_rsq_f32_e32 v60, v60
	v_rsq_f32_e32 v62, v61
	v_rsq_f32_e32 v64, v63
	v_rsq_f32_e32 v66, v65
	v_pk_mul_f32 v[68:69], v[68:69], v[60:61] op_sel_hi:[1,0]
	v_pk_mul_f32 v[70:71], v[70:71], v[60:61] op_sel_hi:[1,0]
	v_pk_mul_f32 v[72:73], v[72:73], v[60:61] op_sel_hi:[1,0]
	v_pk_mul_f32 v[74:75], v[74:75], v[60:61] op_sel_hi:[1,0]
	v_pk_mul_f32 v[80:81], v[80:81], v[60:61] op_sel_hi:[1,0]
	v_pk_mul_f32 v[82:83], v[82:83], v[60:61] op_sel_hi:[1,0]
	v_pk_mul_f32 v[76:77], v[76:77], v[60:61] op_sel_hi:[1,0]
; __device__ __forceinline__ unsigned pkb(float lo, float hi) { f32x2 v = {lo, hi}; bf16x2_t b = __builtin_convertvector(v, bf16x2_t); return __builtin_bit_cast(unsigned, b); }
; template <int R, bool RT = false>
; __device__ __forceinline__ void norm_phase(const NormArgs& a, LAS unsigned char* lds, bool ctx_rows, const float* ctx_src, const float* ctx_shift, const float* ctx_scale) {
;     ...
;             for (int q = 0; q < R; ++q) { const int row = row0 + rr + q;
; #pragma unroll
;                 for (int j = 0; j < 4; ++j) v[q][j] = (v[q][j] * rstd[q]) * A[j] + Sh[j];
;                 if (a.fout) {
; #pragma unroll
;                     for (int j = 0; j < 4; ++j) *(f32x4*)(a.fout + (size_t)row * DM + 4 * lane + 256 * j) = v[q][j];
;                 }
;                 if (a.hout) {
; #pragma unroll
;                     for (int j = 0; j < 4; ++j) { u32x2 w; if (a.hbf) { w.x = pkb(v[q][j][0], v[q][j][1]); w.y = pkb(v[q][j][2], v[q][j][3]); } else { w.x = pkh(v[q][j][0], v[q][j][1]); w.y = pkh(v[q][j][2], v[q][j][3]); } *(u32x2*)(a.hout + (size_t)row * DM + 4 * lane + 256 * j) = w; }
;                 }
	v_pk_mul_f32 v[60:61], v[78:79], v[60:61] op_sel_hi:[1,0]
	v_pk_mul_f32 v[78:79], v[84:85], v[62:63] op_sel_hi:[1,0]
	v_pk_mul_f32 v[84:85], v[86:87], v[62:63] op_sel_hi:[1,0]
	v_pk_mul_f32 v[86:87], v[88:89], v[62:63] op_sel_hi:[1,0]
	v_pk_mul_f32 v[88:89], v[90:91], v[62:63] op_sel_hi:[1,0]
	v_pk_mul_f32 v[90:91], v[96:97], v[62:63] op_sel_hi:[1,0]
	v_pk_mul_f32 v[96:97], v[98:99], v[62:63] op_sel_hi:[1,0]
	v_pk_mul_f32 v[92:93], v[92:93], v[62:63] op_sel_hi:[1,0]
	v_pk_mul_f32 v[62:63], v[94:95], v[62:63] op_sel_hi:[1,0]
	v_pk_mul_f32 v[94:95], v[100:101], v[64:65] op_sel_hi:[1,0]
	v_pk_mul_f32 v[98:99], v[102:103], v[64:65] op_sel_hi:[1,0]
	v_pk_mul_f32 v[100:101], v[104:105], v[64:65] op_sel_hi:[1,0]
	v_pk_mul_f32 v[102:103], v[106:107], v[64:65] op_sel_hi:[1,0]
	v_pk_mul_f32 v[104:105], v[112:113], v[64:65] op_sel_hi:[1,0]
	v_pk_mul_f32 v[106:107], v[114:115], v[64:65] op_sel_hi:[1,0]
	v_pk_mul_f32 v[108:109], v[108:109], v[64:65] op_sel_hi:[1,0]
	v_pk_mul_f32 v[64:65], v[110:111], v[64:65] op_sel_hi:[1,0]
	v_pk_mul_f32 v[110:111], v[116:117], v[66:67] op_sel_hi:[1,0]
	v_pk_mul_f32 v[112:113], v[118:119], v[66:67] op_sel_hi:[1,0]
	v_pk_mul_f32 v[114:115], v[120:121], v[66:67] op_sel_hi:[1,0]
	v_pk_mul_f32 v[116:117], v[122:123], v[66:67] op_sel_hi:[1,0]
	v_pk_mul_f32 v[118:119], v[124:125], v[66:67] op_sel_hi:[1,0]
	v_pk_mul_f32 v[120:121], v[126:127], v[66:67] op_sel_hi:[1,0]
	v_pk_mul_f32 v[18:19], v[18:19], v[66:67] op_sel_hi:[1,0]
	v_pk_mul_f32 v[20:21], v[20:21], v[66:67] op_sel_hi:[1,0]
	v_pk_fma_f32 v[66:67], v[32:33], v[70:71], v[4:5]
	v_pk_fma_f32 v[68:69], v[34:35], v[68:69], v[2:3]
	v_pk_fma_f32 v[70:71], v[36:37], v[74:75], v[8:9]
	v_pk_fma_f32 v[72:73], v[38:39], v[72:73], v[6:7]
	v_pk_fma_f32 v[74:75], v[40:41], v[82:83], v[12:13]
	v_pk_fma_f32 v[80:81], v[42:43], v[80:81], v[10:11]
	v_pk_fma_f32 v[60:61], v[44:45], v[60:61], v[16:17]
	v_pk_fma_f32 v[76:77], v[46:47], v[76:77], v[14:15]
	v_pk_fma_f32 v[82:83], v[32:33], v[84:85], v[4:5]
	v_pk_fma_f32 v[78:79], v[34:35], v[78:79], v[2:3]
	v_pk_fma_f32 v[84:85], v[36:37], v[88:89], v[8:9]
	v_pk_fma_f32 v[86:87], v[38:39], v[86:87], v[6:7]
	v_pk_fma_f32 v[88:89], v[40:41], v[96:97], v[12:13]
	v_pk_fma_f32 v[90:91], v[42:43], v[90:91], v[10:11]
	v_pk_fma_f32 v[62:63], v[44:45], v[62:63], v[16:17]
	v_pk_fma_f32 v[92:93], v[46:47], v[92:93], v[14:15]
	v_pk_fma_f32 v[96:97], v[32:33], v[98:99], v[4:5]
	v_pk_fma_f32 v[94:95], v[34:35], v[94:95], v[2:3]
	v_pk_fma_f32 v[98:99], v[36:37], v[102:103], v[8:9]
	v_pk_fma_f32 v[100:101], v[38:39], v[100:101], v[6:7]
	v_pk_fma_f32 v[102:103], v[40:41], v[106:107], v[12:13]
	v_pk_fma_f32 v[104:105], v[42:43], v[104:105], v[10:11]
	v_pk_fma_f32 v[64:65], v[44:45], v[64:65], v[16:17]
	v_pk_fma_f32 v[106:107], v[46:47], v[108:109], v[14:15]
	v_pk_fma_f32 v[108:109], v[32:33], v[112:113], v[4:5]
	v_pk_fma_f32 v[110:111], v[34:35], v[110:111], v[2:3]
	v_pk_fma_f32 v[112:113], v[36:37], v[116:117], v[8:9]
	v_pk_fma_f32 v[114:115], v[38:39], v[114:115], v[6:7]
	v_pk_fma_f32 v[116:117], v[40:41], v[120:121], v[12:13]
	v_pk_fma_f32 v[118:119], v[42:43], v[118:119], v[10:11]
	v_pk_fma_f32 v[20:21], v[44:45], v[20:21], v[16:17]
	v_pk_fma_f32 v[18:19], v[46:47], v[18:19], v[14:15]
	v_cvt_pk_f16_f32 v68, v68, v69
	v_cvt_pk_f16_f32 v69, v66, v67
	v_cvt_pk_f16_f32 v66, v72, v73
	v_cvt_pk_f16_f32 v67, v70, v71
	v_cvt_pk_f16_f32 v70, v80, v81
	v_cvt_pk_f16_f32 v71, v74, v75
	v_cvt_pk_f16_f32 v72, v76, v77
	v_cvt_pk_f16_f32 v73, v60, v61
	v_cvt_pk_f16_f32 v60, v78, v79
	v_cvt_pk_f16_f32 v61, v82, v83
	v_cvt_pk_f16_f32 v74, v86, v87
	v_cvt_pk_f16_f32 v75, v84, v85
	v_cvt_pk_f16_f32 v76, v90, v91
	v_cvt_pk_f16_f32 v77, v88, v89
	v_cvt_pk_f16_f32 v78, v92, v93
	v_cvt_pk_f16_f32 v79, v62, v63
	v_cvt_pk_f16_f32 v62, v94, v95
	v_cvt_pk_f16_f32 v63, v96, v97
	v_cvt_pk_f16_f32 v80, v100, v101
	v_cvt_pk_f16_f32 v81, v98, v99
	v_cvt_pk_f16_f32 v82, v104, v105
	v_cvt_pk_f16_f32 v83, v102, v103
	v_cvt_pk_f16_f32 v84, v106, v107
	v_cvt_pk_f16_f32 v85, v64, v65
	v_cvt_pk_f16_f32 v64, v110, v111
	v_cvt_pk_f16_f32 v65, v108, v109
	v_cvt_pk_f16_f32 v86, v114, v115
	v_cvt_pk_f16_f32 v87, v112, v113
	v_cvt_pk_f16_f32 v88, v118, v119
	v_cvt_pk_f16_f32 v89, v116, v117
	v_cvt_pk_f16_f32 v18, v18, v19
	v_cvt_pk_f16_f32 v19, v20, v21
	global_store_dwordx2 v[54:55], v[68:69], off sc0 sc1
	global_store_dwordx2 v[54:55], v[66:67], off offset:512 sc0 sc1
	global_store_dwordx2 v[54:55], v[70:71], off offset:1024 sc0 sc1
	global_store_dwordx2 v[54:55], v[72:73], off offset:1536 sc0 sc1
	global_store_dwordx2 v[52:53], v[60:61], off sc0 sc1
	global_store_dwordx2 v[52:53], v[74:75], off offset:512 sc0 sc1
	global_store_dwordx2 v[52:53], v[76:77], off offset:1024 sc0 sc1
	global_store_dwordx2 v[52:53], v[78:79], off offset:1536 sc0 sc1
	global_store_dwordx2 v[50:51], v[62:63], off sc0 sc1
	global_store_dwordx2 v[50:51], v[80:81], off offset:512 sc0 sc1
	global_store_dwordx2 v[50:51], v[82:83], off offset:1024 sc0 sc1
	global_store_dwordx2 v[50:51], v[84:85], off offset:1536 sc0 sc1
	global_store_dwordx2 v[48:49], v[64:65], off sc0 sc1
	global_store_dwordx2 v[48:49], v[86:87], off offset:512 sc0 sc1
	global_store_dwordx2 v[48:49], v[88:89], off offset:1024 sc0 sc1
	global_store_dwordx2 v[48:49], v[18:19], off offset:1536 sc0 sc1
	s_cbranch_scc0 .LBB0_308
	s_add_i32 s30, s30, s6
	s_add_i32 s2, s2, s5
	s_add_i32 s8, s8, s5
	s_add_i32 s10, s10, s5
	s_add_i32 s12, s12, s5
	s_cmpk_gt_i32 s30, 0x7ff
	s_cbranch_scc0 .LBB0_307

; template <int R, bool RT = false>
; __device__ __forceinline__ void norm_phase(const NormArgs& a, LAS unsigned char* lds, bool ctx_rows, const float* ctx_src, const float* ctx_shift, const float* ctx_scale) {
;     ...
;         for (int row = gw; row < NCTX; row += NGW) {
;             f32x4 v[4]; float ss = 0.f;
; #pragma unroll
;             for (int j = 0; j < 4; ++j) { v[j] = *(const f32x4*)(ctx_src + (size_t)row * DM + 4 * lane + 256 * j); ss += (v[j][0] * v[j][0] + v[j][1] * v[j][1]) + (v[j][2] * v[j][2] + v[j][3] * v[j][3]); }
;             const float rstd = __builtin_amdgcn_rsqf(wave_sum(ss) * (1.f / DM) + EPS);
; #pragma unroll
;             for (int j = 0; j < 4; ++j) { const f32x4 h = (v[j] * rstd) * A[j] + Sh[j]; u32x2 w; w.x = pkh(h[0], h[1]); w.y = pkh(h[2], h[3]); *(u32x2*)(a.hout + (size_t)(NTOK + row) * DM + 4 * lane + 256 * j) = w; }
;         }
.LBB0_312:
	global_load_dwordx4 v[40:43], v[20:21], off
	global_load_dwordx4 v[44:47], v[20:21], off offset:1024
	global_load_dwordx4 v[48:51], v[20:21], off offset:2048
	global_load_dwordx4 v[52:55], v[20:21], off offset:3072
	v_mov_b32_e32 v69, 0
	v_mov_b32_e32 v39, 0
	s_add_i32 s8, s4, 0x8000
	s_ashr_i32 s9, s8, 31
	s_add_i32 s4, s4, s6
	s_lshl_b64 s[8:9], s[8:9], 11
	v_lshl_add_u64 v[20:21], v[20:21], 0, s[2:3]
	v_lshl_add_u64 v[56:57], v[18:19], 0, s[8:9]
	s_cmpk_lt_i32 s4, 0x1000
	s_waitcnt vmcnt(3)
	v_pk_mul_f32 v[58:59], v[42:43], v[42:43]
	v_pk_mul_f32 v[60:61], v[40:41], v[40:41]
	s_waitcnt vmcnt(2)
	v_pk_mul_f32 v[62:63], v[46:47], v[46:47]
	v_pk_mul_f32 v[64:65], v[44:45], v[44:45]
	v_pk_mov_b32 v[70:71], v[60:61], v[58:59] op_sel:[1,0]
	v_mov_b32_e32 v61, v59
	v_pk_mov_b32 v[58:59], v[64:65], v[62:63] op_sel:[1,0]
	v_mov_b32_e32 v65, v63
	s_waitcnt vmcnt(1)
	v_mul_f32_e32 v66, v49, v49
	v_mul_f32_e32 v68, v51, v51
	v_pk_add_f32 v[60:61], v[70:71], v[60:61]
	v_pk_add_f32 v[58:59], v[58:59], v[64:65]
	s_waitcnt vmcnt(0)
	v_mul_f32_e32 v72, v52, v52
	v_mul_f32_e32 v73, v53, v53
	v_mul_f32_e32 v74, v54, v54
	v_mul_f32_e32 v75, v55, v55
	v_pk_fma_f32 v[62:63], v[48:49], v[48:49], v[66:67] op_sel_hi:[1,1,0]
	v_pk_fma_f32 v[66:67], v[50:51], v[50:51], v[68:69] op_sel_hi:[1,1,0]
	v_pk_add_f32 v[60:61], v[60:61], v[60:61] op_sel:[0,1] op_sel_hi:[1,0]
	v_pk_add_f32 v[58:59], v[58:59], v[58:59] op_sel:[0,1] op_sel_hi:[1,0]
	v_mov_b32_e32 v63, v74
	v_mov_b32_e32 v67, v75
	v_mov_b32_e32 v61, v72
	v_mov_b32_e32 v59, v73
	v_pk_add_f32 v[62:63], v[62:63], v[66:67]
	v_pk_add_f32 v[58:59], v[60:61], v[58:59]
	s_nop 0
	v_pk_add_f32 v[58:59], v[58:59], v[62:63]
	s_nop 0
	v_add_f32_e32 v58, v58, v59
	s_nop 1
	v_add_f32_dpp v58, v58, v58 quad_perm:[1,0,3,2] row_mask:0xf bank_mask:0xf bound_ctrl:1
	s_nop 1
	v_add_f32_dpp v58, v58, v58 quad_perm:[2,3,0,1] row_mask:0xf bank_mask:0xf bound_ctrl:1
	s_nop 1
	v_add_f32_dpp v58, v58, v58 row_half_mirror row_mask:0xf bank_mask:0xf bound_ctrl:1
	s_nop 1
	v_add_f32_dpp v58, v58, v58 row_mirror row_mask:0xf bank_mask:0xf bound_ctrl:1
	s_nop 1
	v_mov_b32_dpp v39, v58 row_bcast:15 row_mask:0xa bank_mask:0xf
	v_add_f32_e32 v39, v58, v39
	s_nop 1
	v_mov_b32_dpp v69, v39 row_bcast:31 row_mask:0xc bank_mask:0xf
	v_add_f32_e32 v39, v39, v69
	s_nop 0
	v_readlane_b32 s5, v39, 63
	s_nop 1
	v_fma_f32 v39, s5, v38, v1
	v_rsq_f32_e32 v58, v39
	s_nop 0
	v_pk_mul_f32 v[40:41], v[40:41], v[58:59] op_sel_hi:[1,0]
	v_pk_mul_f32 v[42:43], v[42:43], v[58:59] op_sel_hi:[1,0]
	v_pk_mul_f32 v[44:45], v[44:45], v[58:59] op_sel_hi:[1,0]
	v_pk_mul_f32 v[46:47], v[46:47], v[58:59] op_sel_hi:[1,0]
	v_pk_mul_f32 v[48:49], v[48:49], v[58:59] op_sel_hi:[1,0]
	v_pk_mul_f32 v[50:51], v[50:51], v[58:59] op_sel_hi:[1,0]
	v_pk_mul_f32 v[52:53], v[52:53], v[58:59] op_sel_hi:[1,0]
	v_pk_mul_f32 v[54:55], v[54:55], v[58:59] op_sel_hi:[1,0]
	v_pk_fma_f32 v[42:43], v[22:23], v[42:43], v[4:5]
	v_pk_fma_f32 v[40:41], v[24:25], v[40:41], v[2:3]
	v_pk_fma_f32 v[46:47], v[26:27], v[46:47], v[8:9]
	v_pk_fma_f32 v[44:45], v[28:29], v[44:45], v[6:7]
	v_pk_fma_f32 v[50:51], v[30:31], v[50:51], v[12:13]
	v_pk_fma_f32 v[48:49], v[32:33], v[48:49], v[10:11]
	v_pk_fma_f32 v[54:55], v[34:35], v[54:55], v[16:17]
	v_pk_fma_f32 v[52:53], v[36:37], v[52:53], v[14:15]
	v_cvt_pk_f16_f32 v40, v40, v41
	v_cvt_pk_f16_f32 v41, v42, v43
	v_cvt_pk_f16_f32 v42, v44, v45
	v_cvt_pk_f16_f32 v43, v46, v47
	v_cvt_pk_f16_f32 v44, v48, v49
	v_cvt_pk_f16_f32 v45, v50, v51
	v_cvt_pk_f16_f32 v46, v52, v53
	v_cvt_pk_f16_f32 v47, v54, v55
	global_store_dwordx2 v[56:57], v[40:41], off sc0 sc1
	global_store_dwordx2 v[56:57], v[42:43], off offset:512 sc0 sc1
	global_store_dwordx2 v[56:57], v[44:45], off offset:1024 sc0 sc1
	global_store_dwordx2 v[56:57], v[46:47], off offset:1536 sc0 sc1
	s_cbranch_scc1 .LBB0_312

; #define LAS __attribute__((address_space(3)))
; template <int R, bool RT = false>
; __device__ __forceinline__ void norm_phase(const NormArgs& a, LAS unsigned char* lds, bool ctx_rows, const float* ctx_src, const float* ctx_shift, const float* ctx_scale) {
;     ...
;         f32x4 A[4], Sh[4], G2[4];
; #pragma unroll
;         for (int j = 0; j < 4; ++j) { const int c = 4 * lane + 256 * j; const f32x4 g = *(const f32x4*)(a.gain + c);
;             if (a.shift) { const f32x4 sc = *(const f32x4*)(a.scale + (size_t)b * a.mstride + c); A[j] = g * (sc + 1.f); Sh[j] = *(const f32x4*)(a.shift + (size_t)b * a.mstride + c); }
;             else { A[j] = g; Sh[j] = (f32x4){0.f, 0.f, 0.f, 0.f}; }
;             if (a.y2) G2[j] = *(const f32x4*)(a.gate2 + (size_t)b * 6144 + c); else G2[j] = (f32x4){0.f, 0.f, 0.f, 0.f}; }
;         int ipk[4] = {-1, -1, -1, -1};
;         if (a.y2) {
; #pragma unroll
;             for (int i = 0; i < 4; ++i) ipk[i] = a.inv[((size_t)b * NE + (lane & 15)) * SEQ + ((row0 + 4 * i + (lane >> 4)) & (SEQ - 1))]; }
;         u32x2 xp[RT ? 4 : 1][4][3]; float rsel[4] = {0.f, 0.f, 0.f, 0.f};
;         LAS unsigned char* hs = wave < 7 ? lds + 65536 + wave * 8448 : lds + 132608;
; #pragma unroll (RT ? 4 : 1)
;         for (int rr = 0; rr < 16; rr += R) {
;             if constexpr (RT) asm volatile("" ::: "memory");
;             f32x4 v[R][4];
;             int sl[R];
; #pragma unroll
;             for (int q = 0; q < R; ++q) { sl[q] = -1; if (a.y2) { const int r = rr + q; const int pk = r < 4 ? ipk[0] : (r < 8 ? ipk[1] : (r < 12 ? ipk[2] : ipk[3]));
;                     const int got = __shfl(pk, (lane & 15) + 16 * (r & 3)); sl[q] = lane < 16 ? got : -1; } }
; #pragma unroll
;             for (int q = 0; q < R; ++q) { const int row = row0 + rr + q;
;                 if (a.src16) { const f16* xr = a.src16 + (size_t)row * DM;
; #pragma unroll
;                     for (int j = 0; j < 4; ++j) { const f16x4 t = *(const f16x4*)(xr + 4 * lane + 256 * j); v[q][j] = (f32x4){(float)t[0], (float)t[1], (float)t[2], (float)t[3]};
;                         if constexpr (RT) { if (j == 0) *(LAS u32x2*)(hs + (rr + q) * 528 + 8 * lane) = __builtin_bit_cast(u32x2, t);
;                             else xp[rr / 4][q][j - 1] = __builtin_bit_cast(u32x2, t); } } }
;                 else { const float* xr = a.src + (size_t)row * DM;
; #pragma unroll
.LBB0_808:
	s_ashr_i32 s0, s34, 31
	s_lshr_b32 s0, s0, 25
	s_add_i32 s0, s34, s0
	s_ashr_i32 s22, s0, 7
	v_mad_i64_i32 v[32:33], s[2:3], s22, v209, v[28:29]
	global_load_dwordx4 v[6:9], v[32:33], off
	global_load_dwordx4 v[2:5], v[20:21], off
	v_mad_i64_i32 v[38:39], s[2:3], s22, v209, v[30:31]
	s_add_i32 s24, s14, 1
	s_ashr_i32 s15, s14, 31
	s_ashr_i32 s25, s24, 31
	s_lshl_b64 s[2:3], s[14:15], 11
	s_lshl_b64 s[24:25], s[24:25], 11
	v_lshl_add_u64 v[60:61], v[22:23], 0, s[24:25]
	s_add_i32 s28, s14, 3
	s_add_i32 s26, s14, 2
	s_ashr_i32 s29, s28, 31
	s_ashr_i32 s27, s26, 31
	s_lshl_b64 s[28:29], s[28:29], 11
	s_lshl_b64 s[26:27], s[26:27], 11
	v_lshl_add_u64 v[130:131], v[22:23], 0, s[28:29]
	v_cmp_lt_i32_e32 vcc, v222, v221
	s_ashr_i32 s23, s22, 31
	s_waitcnt vmcnt(0)
	v_pk_add_f32 v[8:9], v[8:9], 1.0 op_sel_hi:[1,0]
	v_pk_add_f32 v[6:7], v[6:7], 1.0 op_sel_hi:[1,0]
	v_pk_mul_f32 v[34:35], v[4:5], v[8:9]
	v_pk_mul_f32 v[36:37], v[2:3], v[6:7]
	global_load_dwordx4 v[2:5], v[38:39], off
	global_load_dwordx4 v[6:9], v[20:21], off offset:1024
	global_load_dwordx4 v[10:13], v[32:33], off offset:1024
	s_waitcnt vmcnt(0)
	v_pk_add_f32 v[12:13], v[12:13], 1.0 op_sel_hi:[1,0]
	v_pk_add_f32 v[10:11], v[10:11], 1.0 op_sel_hi:[1,0]
	v_pk_mul_f32 v[40:41], v[8:9], v[12:13]
	v_pk_mul_f32 v[42:43], v[6:7], v[10:11]
	global_load_dwordx4 v[6:9], v[38:39], off offset:1024
	global_load_dwordx4 v[10:13], v[20:21], off offset:2048
	global_load_dwordx4 v[14:17], v[32:33], off offset:2048
	s_waitcnt vmcnt(0)
	v_pk_add_f32 v[16:17], v[16:17], 1.0 op_sel_hi:[1,0]
	v_pk_add_f32 v[14:15], v[14:15], 1.0 op_sel_hi:[1,0]
	v_pk_mul_f32 v[44:45], v[12:13], v[16:17]
	v_pk_mul_f32 v[46:47], v[10:11], v[14:15]
	global_load_dwordx4 v[10:13], v[38:39], off offset:2048
	global_load_dwordx4 v[14:17], v[20:21], off offset:3072
	global_load_dwordx4 v[48:51], v[32:33], off offset:3072
	s_waitcnt vmcnt(0)
	v_pk_add_f32 v[32:33], v[50:51], 1.0 op_sel_hi:[1,0]
	v_pk_add_f32 v[48:49], v[48:49], 1.0 op_sel_hi:[1,0]
	v_pk_mul_f32 v[52:53], v[16:17], v[32:33]
	v_pk_mul_f32 v[54:55], v[14:15], v[48:49]
	global_load_dwordx4 v[14:17], v[38:39], off offset:3072
	v_lshl_add_u64 v[32:33], v[22:23], 0, s[2:3]
	global_load_dwordx2 v[50:51], v[32:33], off nt
	global_load_dwordx2 v[48:49], v[32:33], off offset:512 nt
	global_load_dwordx2 v[38:39], v[32:33], off offset:1024 nt
	global_load_dwordx2 v[56:57], v[60:61], off nt
	global_load_dwordx2 v[58:59], v[60:61], off offset:512 nt
	global_load_dwordx2 v[68:69], v[130:131], off nt
	global_load_dwordx2 v[70:71], v[130:131], off offset:512 nt
	s_waitcnt vmcnt(6)
	v_cvt_f32_f16_e32 v72, v50
	v_cvt_f32_f16_sdwa v73, v50 dst_sel:DWORD dst_unused:UNUSED_PAD src0_sel:WORD_1
	v_cvt_f32_f16_e32 v76, v51
	v_cvt_f32_f16_sdwa v77, v51 dst_sel:DWORD dst_unused:UNUSED_PAD src0_sel:WORD_1
	s_waitcnt vmcnt(3)
	v_cvt_f32_f16_e32 v88, v56
	v_cvt_f32_f16_sdwa v89, v56 dst_sel:DWORD dst_unused:UNUSED_PAD src0_sel:WORD_1
	v_cvt_f32_f16_e32 v90, v57
	v_cvt_f32_f16_sdwa v91, v57 dst_sel:DWORD dst_unused:UNUSED_PAD src0_sel:WORD_1
	ds_write2_b64 v211, v[50:51], v[56:57] offset1:66
	global_load_dwordx2 v[56:57], v[60:61], off offset:1024 nt
	global_load_dwordx2 v[50:51], v[60:61], off offset:1536 nt
	v_lshl_add_u64 v[60:61], v[22:23], 0, s[26:27]
	global_load_dwordx2 v[32:33], v[32:33], off offset:1536 nt
	v_cvt_f32_f16_e32 v74, v48
	global_load_dwordx2 v[66:67], v[60:61], off nt
	global_load_dwordx2 v[64:65], v[60:61], off offset:512 nt
	global_load_dwordx2 v[62:63], v[60:61], off offset:1024 nt
	v_cvt_f32_f16_sdwa v75, v48 dst_sel:DWORD dst_unused:UNUSED_PAD src0_sel:WORD_1
	global_load_dwordx2 v[60:61], v[60:61], off offset:1536 nt
	v_cvt_f32_f16_e32 v80, v49
	v_cvt_f32_f16_sdwa v81, v49 dst_sel:DWORD dst_unused:UNUSED_PAD src0_sel:WORD_1
	v_cvt_f32_f16_e32 v78, v38
	v_cvt_f32_f16_sdwa v79, v38 dst_sel:DWORD dst_unused:UNUSED_PAD src0_sel:WORD_1
	v_cvt_f32_f16_e32 v84, v39
	v_cvt_f32_f16_sdwa v85, v39 dst_sel:DWORD dst_unused:UNUSED_PAD src0_sel:WORD_1
	v_pk_mul_f32 v[136:137], v[72:73], v[72:73]
	v_pk_mul_f32 v[138:139], v[76:77], v[76:77]
	v_pk_mul_f32 v[140:141], v[74:75], v[74:75]
	v_pk_mul_f32 v[142:143], v[80:81], v[80:81]
	v_pk_mul_f32 v[144:145], v[78:79], v[78:79]
	v_pk_mul_f32 v[146:147], v[84:85], v[84:85]
	v_add_f32_e32 v142, v142, v143
	v_add_f32_e32 v140, v140, v141
	v_add_f32_e32 v138, v138, v139
	v_add_f32_e32 v136, v136, v137
	v_add_f32_e32 v140, v140, v142
	v_add_f32_e32 v136, v136, v138
	v_add_f32_e32 v137, v146, v147
	v_add_f32_e32 v138, v144, v145
	v_add_f32_e32 v136, v136, v140
	v_add_f32_e32 v137, v138, v137
	v_add_f32_e32 v136, v136, v137
	s_waitcnt vmcnt(9)
	v_cvt_f32_f16_e32 v92, v58
	v_cvt_f32_f16_sdwa v93, v58 dst_sel:DWORD dst_unused:UNUSED_PAD src0_sel:WORD_1
	v_cvt_f32_f16_e32 v96, v59
	v_cvt_f32_f16_sdwa v97, v59 dst_sel:DWORD dst_unused:UNUSED_PAD src0_sel:WORD_1
	v_pk_mul_f32 v[140:141], v[90:91], v[90:91]
	v_pk_mul_f32 v[142:143], v[92:93], v[92:93]
	v_add_f32_e32 v140, v140, v141
	v_pk_mul_f32 v[144:145], v[96:97], v[96:97]
	v_add_f32_e32 v142, v142, v143
	s_waitcnt vmcnt(8)
	v_cvt_f32_f16_e32 v120, v68
	v_cvt_f32_f16_sdwa v121, v68 dst_sel:DWORD dst_unused:UNUSED_PAD src0_sel:WORD_1
	v_cvt_f32_f16_e32 v122, v69
	v_cvt_f32_f16_sdwa v123, v69 dst_sel:DWORD dst_unused:UNUSED_PAD src0_sel:WORD_1
	s_waitcnt vmcnt(6)
	v_cvt_f32_f16_e32 v94, v56
	v_cvt_f32_f16_sdwa v95, v56 dst_sel:DWORD dst_unused:UNUSED_PAD src0_sel:WORD_1
	v_cvt_f32_f16_e32 v100, v57
	s_waitcnt vmcnt(4)
	v_cvt_f32_f16_e32 v82, v32
	v_cvt_f32_f16_sdwa v83, v32 dst_sel:DWORD dst_unused:UNUSED_PAD src0_sel:WORD_1
	s_waitcnt vmcnt(3)
; #define LAS __attribute__((address_space(3)))
; template <int R, bool RT = false>
; __device__ __forceinline__ void norm_phase(const NormArgs& a, LAS unsigned char* lds, bool ctx_rows, const float* ctx_src, const float* ctx_shift, const float* ctx_scale) {
;     ...
;             for (int q = 0; q < R; ++q) { const int row = row0 + rr + q;
;                 if (a.src16) { const f16* xr = a.src16 + (size_t)row * DM;
; #pragma unroll
;                     for (int j = 0; j < 4; ++j) { const f16x4 t = *(const f16x4*)(xr + 4 * lane + 256 * j); v[q][j] = (f32x4){(float)t[0], (float)t[1], (float)t[2], (float)t[3]};
;                         if constexpr (RT) { if (j == 0) *(LAS u32x2*)(hs + (rr + q) * 528 + 8 * lane) = __builtin_bit_cast(u32x2, t);
;                             else xp[rr / 4][q][j - 1] = __builtin_bit_cast(u32x2, t); } } }
;     ...
;             for (int q = 0; q < R; ++q) { float ss = 0.f;
; #pragma unroll
;                 for (int j = 0; j < 4; ++j) ss += (v[q][j][0] * v[q][j][0] + v[q][j][1] * v[q][j][1]) + (v[q][j][2] * v[q][j][2] + v[q][j][3] * v[q][j][3]);
;                 rstd[q] = __builtin_amdgcn_rsqf(wave_sum(ss) * (1.f / DM) + EPS);
	ds_write2_b64 v211, v[66:67], v[68:69] offset0:132 offset1:198
	global_load_dwordx2 v[68:69], v[130:131], off offset:1024 nt
	v_cvt_f32_f16_e32 v104, v66
	v_cvt_f32_f16_sdwa v105, v66 dst_sel:DWORD dst_unused:UNUSED_PAD src0_sel:WORD_1
	v_cvt_f32_f16_e32 v108, v67
	v_cvt_f32_f16_sdwa v109, v67 dst_sel:DWORD dst_unused:UNUSED_PAD src0_sel:WORD_1
	global_load_dwordx2 v[66:67], v[130:131], off offset:1536 nt
	v_cvt_f32_f16_e32 v86, v33
	v_cvt_f32_f16_sdwa v87, v33 dst_sel:DWORD dst_unused:UNUSED_PAD src0_sel:WORD_1
	v_pk_mul_f32 v[148:149], v[82:83], v[82:83]
	v_cvt_f32_f16_sdwa v101, v57 dst_sel:DWORD dst_unused:UNUSED_PAD src0_sel:WORD_1
	v_add_f32_e32 v138, v148, v149
	v_pk_mul_f32 v[150:151], v[86:87], v[86:87]
	v_cvt_f32_f16_e32 v98, v50
	v_add_f32_e32 v137, v150, v151
	v_add_f32_e32 v137, v138, v137
	v_add_f32_e32 v136, v136, v137
	v_mov_b32_e32 v137, 0
	v_cvt_f32_f16_sdwa v99, v50 dst_sel:DWORD dst_unused:UNUSED_PAD src0_sel:WORD_1
	v_add_f32_dpp v136, v136, v136 quad_perm:[1,0,3,2] row_mask:0xf bank_mask:0xf bound_ctrl:1
	v_cvt_f32_f16_e32 v102, v51
	v_cvt_f32_f16_sdwa v103, v51 dst_sel:DWORD dst_unused:UNUSED_PAD src0_sel:WORD_1
	v_add_f32_dpp v136, v136, v136 quad_perm:[2,3,0,1] row_mask:0xf bank_mask:0xf bound_ctrl:1
	v_pk_mul_f32 v[138:139], v[88:89], v[88:89]
	v_pk_mul_f32 v[146:147], v[94:95], v[94:95]
	v_add_f32_dpp v136, v136, v136 row_half_mirror row_mask:0xf bank_mask:0xf bound_ctrl:1
	v_add_f32_e32 v138, v138, v139
	v_pk_mul_f32 v[148:149], v[100:101], v[100:101]
	v_add_f32_dpp v136, v136, v136 row_mirror row_mask:0xf bank_mask:0xf bound_ctrl:1
	v_add_f32_e32 v138, v138, v140
	v_add_f32_e32 v139, v146, v147
	v_mov_b32_dpp v137, v136 row_bcast:15 row_mask:0xa bank_mask:0xf
	v_add_f32_e32 v136, v136, v137
	v_mov_b32_e32 v137, 0
	v_pk_mul_f32 v[150:151], v[98:99], v[98:99]
	v_pk_mul_f32 v[152:153], v[102:103], v[102:103]
	v_mov_b32_dpp v137, v136 row_bcast:31 row_mask:0xc bank_mask:0xf
	v_add_f32_e32 v136, v136, v137
	v_add_f32_e32 v137, v144, v145
	v_add_f32_e32 v137, v142, v137
	v_add_f32_e32 v137, v138, v137
	v_add_f32_e32 v138, v148, v149
	v_add_f32_e32 v138, v139, v138
	v_add_f32_e32 v137, v137, v138
	v_add_f32_e32 v138, v152, v153
	v_add_f32_e32 v139, v150, v151
	v_add_f32_e32 v138, v139, v138
	v_add_f32_e32 v137, v137, v138
	v_mov_b32_e32 v138, 0
	s_waitcnt vmcnt(4)
	v_cvt_f32_f16_e32 v106, v64
	v_add_f32_dpp v137, v137, v137 quad_perm:[1,0,3,2] row_mask:0xf bank_mask:0xf bound_ctrl:1
	v_cvt_f32_f16_sdwa v107, v64 dst_sel:DWORD dst_unused:UNUSED_PAD src0_sel:WORD_1
	v_cvt_f32_f16_e32 v112, v65
	v_add_f32_dpp v137, v137, v137 quad_perm:[2,3,0,1] row_mask:0xf bank_mask:0xf bound_ctrl:1
	v_cvt_f32_f16_sdwa v113, v65 dst_sel:DWORD dst_unused:UNUSED_PAD src0_sel:WORD_1
	v_readlane_b32 s0, v136, 63
	v_add_f32_dpp v137, v137, v137 row_half_mirror row_mask:0xf bank_mask:0xf bound_ctrl:1
	s_waitcnt vmcnt(3)
	v_cvt_f32_f16_e32 v110, v62
	v_cvt_f32_f16_sdwa v111, v62 dst_sel:DWORD dst_unused:UNUSED_PAD src0_sel:WORD_1
	v_add_f32_dpp v137, v137, v137 row_mirror row_mask:0xf bank_mask:0xf bound_ctrl:1
	v_cvt_f32_f16_e32 v116, v63
	v_cvt_f32_f16_sdwa v117, v63 dst_sel:DWORD dst_unused:UNUSED_PAD src0_sel:WORD_1
	v_mov_b32_dpp v138, v137 row_bcast:15 row_mask:0xa bank_mask:0xf
	v_add_f32_e32 v137, v137, v138
	v_mov_b32_e32 v138, 0
	v_fma_f32 v136, s0, v214, v213
	v_pk_mul_f32 v[144:145], v[106:107], v[106:107]
	v_mov_b32_dpp v138, v137 row_bcast:31 row_mask:0xc bank_mask:0xf
	v_add_f32_e32 v137, v137, v138
	v_pk_mul_f32 v[146:147], v[112:113], v[112:113]
	v_readlane_b32 s0, v137, 63
	s_waitcnt vmcnt(2)
	v_cvt_f32_f16_e32 v114, v60
	v_cvt_f32_f16_sdwa v115, v60 dst_sel:DWORD dst_unused:UNUSED_PAD src0_sel:WORD_1
	v_fma_f32 v137, s0, v214, v213
	v_cvt_f32_f16_e32 v118, v61
	v_cvt_f32_f16_sdwa v119, v61 dst_sel:DWORD dst_unused:UNUSED_PAD src0_sel:WORD_1
	v_rsq_f32_e32 v138, v137
	v_pk_mul_f32 v[140:141], v[104:105], v[104:105]
	v_pk_mul_f32 v[142:143], v[108:109], v[108:109]
	v_add_f32_e32 v137, v146, v147
	v_add_f32_e32 v139, v144, v145
	v_add_f32_e32 v137, v139, v137
	v_add_f32_e32 v139, v142, v143
	v_add_f32_e32 v140, v140, v141
	v_pk_mul_f32 v[148:149], v[110:111], v[110:111]
	v_pk_mul_f32 v[150:151], v[116:117], v[116:117]
	v_add_f32_e32 v139, v140, v139
	v_add_f32_e32 v137, v139, v137
	v_add_f32_e32 v139, v150, v151
	v_add_f32_e32 v140, v148, v149
	v_pk_mul_f32 v[152:153], v[114:115], v[114:115]
	v_pk_mul_f32 v[154:155], v[118:119], v[118:119]
	v_add_f32_e32 v139, v140, v139
	v_add_f32_e32 v137, v137, v139
	v_add_f32_e32 v139, v154, v155
	v_add_f32_e32 v140, v152, v153
	v_add_f32_e32 v139, v140, v139
	v_add_f32_e32 v137, v137, v139
	v_mov_b32_e32 v139, 0
	v_cvt_f32_f16_e32 v124, v70
	v_add_f32_dpp v137, v137, v137 quad_perm:[1,0,3,2] row_mask:0xf bank_mask:0xf bound_ctrl:1
	v_cvt_f32_f16_sdwa v125, v70 dst_sel:DWORD dst_unused:UNUSED_PAD src0_sel:WORD_1
	v_cvt_f32_f16_e32 v128, v71
	v_add_f32_dpp v137, v137, v137 quad_perm:[2,3,0,1] row_mask:0xf bank_mask:0xf bound_ctrl:1
	v_cvt_f32_f16_sdwa v129, v71 dst_sel:DWORD dst_unused:UNUSED_PAD src0_sel:WORD_1
	s_waitcnt vmcnt(1)
	v_cvt_f32_f16_e32 v126, v68
	v_add_f32_dpp v137, v137, v137 row_half_mirror row_mask:0xf bank_mask:0xf bound_ctrl:1
	v_cvt_f32_f16_sdwa v127, v68 dst_sel:DWORD dst_unused:UNUSED_PAD src0_sel:WORD_1
	v_cvt_f32_f16_e32 v132, v69
	v_add_f32_dpp v137, v137, v137 row_mirror row_mask:0xf bank_mask:0xf bound_ctrl:1
	v_cvt_f32_f16_sdwa v133, v69 dst_sel:DWORD dst_unused:UNUSED_PAD src0_sel:WORD_1
	v_pk_mul_f32 v[142:143], v[120:121], v[120:121]
	v_mov_b32_dpp v139, v137 row_bcast:15 row_mask:0xa bank_mask:0xf
	v_add_f32_e32 v137, v137, v139
	v_mov_b32_e32 v139, 0
	v_pk_mul_f32 v[144:145], v[122:123], v[122:123]
	s_waitcnt vmcnt(0)
; __device__ __forceinline__ unsigned pkb(float lo, float hi) { f32x2 v = {lo, hi}; bf16x2_t b = __builtin_convertvector(v, bf16x2_t); return __builtin_bit_cast(unsigned, b); }
; template <int R, bool RT = false>
; __device__ __forceinline__ void norm_phase(const NormArgs& a, LAS unsigned char* lds, bool ctx_rows, const float* ctx_src, const float* ctx_shift, const float* ctx_scale) {
;     ...
;             for (int q = 0; q < R; ++q) { float ss = 0.f;
; #pragma unroll
;                 for (int j = 0; j < 4; ++j) ss += (v[q][j][0] * v[q][j][0] + v[q][j][1] * v[q][j][1]) + (v[q][j][2] * v[q][j][2] + v[q][j][3] * v[q][j][3]);
;                 rstd[q] = __builtin_amdgcn_rsqf(wave_sum(ss) * (1.f / DM) + EPS);
;                 if constexpr (RT) rsel[q] = ((lane >> 4) == rr / 4) ? rstd[q] : rsel[q]; }
; #pragma unroll
;             for (int q = 0; q < R; ++q) { const int row = row0 + rr + q;
; #pragma unroll
;                 for (int j = 0; j < 4; ++j) v[q][j] = (v[q][j] * rstd[q]) * A[j] + Sh[j];
;                 if (a.fout) {
; #pragma unroll
;                     for (int j = 0; j < 4; ++j) *(f32x4*)(a.fout + (size_t)row * DM + 4 * lane + 256 * j) = v[q][j];
;                 }
;                 if (a.hout) {
; #pragma unroll
;                     for (int j = 0; j < 4; ++j) { u32x2 w; if (a.hbf) { w.x = pkb(v[q][j][0], v[q][j][1]); w.y = pkb(v[q][j][2], v[q][j][3]); } else { w.x = pkh(v[q][j][0], v[q][j][1]); w.y = pkh(v[q][j][2], v[q][j][3]); } *(u32x2*)(a.hout + (size_t)row * DM + 4 * lane + 256 * j) = w; }
;                 }
	v_cvt_f32_f16_e32 v130, v66
	v_mov_b32_dpp v139, v137 row_bcast:31 row_mask:0xc bank_mask:0xf
	v_add_f32_e32 v137, v137, v139
	v_cvt_f32_f16_sdwa v131, v66 dst_sel:DWORD dst_unused:UNUSED_PAD src0_sel:WORD_1
	v_readlane_b32 s0, v137, 63
	v_cvt_f32_f16_e32 v134, v67
	v_cvt_f32_f16_sdwa v135, v67 dst_sel:DWORD dst_unused:UNUSED_PAD src0_sel:WORD_1
	v_fma_f32 v137, s0, v214, v213
	v_rsq_f32_e32 v140, v137
	v_pk_mul_f32 v[146:147], v[124:125], v[124:125]
	v_pk_mul_f32 v[148:149], v[128:129], v[128:129]
	v_add_f32_e32 v137, v144, v145
	v_add_f32_e32 v139, v142, v143
	v_add_f32_e32 v137, v139, v137
	v_add_f32_e32 v139, v148, v149
	v_add_f32_e32 v141, v146, v147
	v_pk_mul_f32 v[150:151], v[126:127], v[126:127]
	v_pk_mul_f32 v[152:153], v[132:133], v[132:133]
	v_add_f32_e32 v139, v141, v139
	v_add_f32_e32 v137, v137, v139
	v_add_f32_e32 v139, v152, v153
	v_add_f32_e32 v141, v150, v151
	v_pk_mul_f32 v[154:155], v[130:131], v[130:131]
	v_pk_mul_f32 v[156:157], v[134:135], v[134:135]
	v_add_f32_e32 v139, v141, v139
	v_add_f32_e32 v137, v137, v139
	v_add_f32_e32 v139, v156, v157
	v_add_f32_e32 v141, v154, v155
	v_add_f32_e32 v139, v141, v139
	v_add_f32_e32 v137, v137, v139
	v_mov_b32_e32 v139, 0
	v_rsq_f32_e32 v136, v136
	v_add_f32_dpp v137, v137, v137 quad_perm:[1,0,3,2] row_mask:0xf bank_mask:0xf bound_ctrl:1
	v_cndmask_b32_e64 v164, 0, v140, s[4:5]
	v_cndmask_b32_e64 v163, 0, v138, s[4:5]
	v_add_f32_dpp v137, v137, v137 quad_perm:[2,3,0,1] row_mask:0xf bank_mask:0xf bound_ctrl:1
	v_cndmask_b32_e64 v161, 0, v136, s[4:5]
	s_nop 0
	v_add_f32_dpp v137, v137, v137 row_half_mirror row_mask:0xf bank_mask:0xf bound_ctrl:1
	s_nop 1
	v_add_f32_dpp v137, v137, v137 row_mirror row_mask:0xf bank_mask:0xf bound_ctrl:1
	s_nop 1
	v_mov_b32_dpp v139, v137 row_bcast:15 row_mask:0xa bank_mask:0xf
	v_add_f32_e32 v137, v137, v139
	v_mov_b32_e32 v139, 0
	s_nop 1
	v_mov_b32_dpp v139, v137 row_bcast:31 row_mask:0xc bank_mask:0xf
	v_add_f32_e32 v137, v137, v139
	s_nop 0
	v_readlane_b32 s0, v137, 63
	s_nop 1
	v_fma_f32 v137, s0, v214, v213
	v_pk_mul_f32 v[72:73], v[72:73], v[136:137] op_sel_hi:[1,0]
	v_pk_mul_f32 v[76:77], v[76:77], v[136:137] op_sel_hi:[1,0]
	v_pk_fma_f32 v[72:73], v[36:37], v[72:73], v[2:3]
	v_pk_fma_f32 v[76:77], v[34:35], v[76:77], v[4:5]
	v_pk_mul_f32 v[74:75], v[74:75], v[136:137] op_sel_hi:[1,0]
	v_pk_mul_f32 v[80:81], v[80:81], v[136:137] op_sel_hi:[1,0]
	v_pk_fma_f32 v[74:75], v[42:43], v[74:75], v[6:7]
	v_pk_fma_f32 v[80:81], v[40:41], v[80:81], v[8:9]
	v_pk_mul_f32 v[78:79], v[78:79], v[136:137] op_sel_hi:[1,0]
	v_pk_mul_f32 v[84:85], v[84:85], v[136:137] op_sel_hi:[1,0]
	v_cvt_pk_bf16_f32 v72, v72, v73
	v_cvt_pk_bf16_f32 v73, v76, v77
	v_lshl_add_u64 v[76:77], v[24:25], 0, s[2:3]
	v_pk_fma_f32 v[84:85], v[44:45], v[84:85], v[12:13]
	v_pk_fma_f32 v[78:79], v[46:47], v[78:79], v[10:11]
	v_pk_mul_f32 v[82:83], v[82:83], v[136:137] op_sel_hi:[1,0]
	v_pk_mul_f32 v[86:87], v[86:87], v[136:137] op_sel_hi:[1,0]
	global_store_dwordx2 v[76:77], v[72:73], off sc0 sc1
	v_cvt_pk_bf16_f32 v72, v74, v75
	v_cvt_pk_bf16_f32 v73, v80, v81
	v_pk_fma_f32 v[86:87], v[52:53], v[86:87], v[16:17]
	v_pk_fma_f32 v[82:83], v[54:55], v[82:83], v[14:15]
	global_store_dwordx2 v[76:77], v[72:73], off offset:512 sc0 sc1
	v_cvt_pk_bf16_f32 v72, v78, v79
	v_cvt_pk_bf16_f32 v73, v84, v85
	global_store_dwordx2 v[76:77], v[72:73], off offset:1024 sc0 sc1
	v_cvt_pk_bf16_f32 v72, v82, v83
	v_cvt_pk_bf16_f32 v73, v86, v87
	global_store_dwordx2 v[76:77], v[72:73], off offset:1536 sc0 sc1
	v_pk_mul_f32 v[72:73], v[88:89], v[138:139] op_sel_hi:[1,0]
	v_pk_mul_f32 v[74:75], v[90:91], v[138:139] op_sel_hi:[1,0]
	v_pk_fma_f32 v[72:73], v[36:37], v[72:73], v[2:3]
	v_pk_fma_f32 v[74:75], v[34:35], v[74:75], v[4:5]
	v_pk_mul_f32 v[76:77], v[92:93], v[138:139] op_sel_hi:[1,0]
	v_pk_mul_f32 v[78:79], v[96:97], v[138:139] op_sel_hi:[1,0]
	v_pk_fma_f32 v[76:77], v[42:43], v[76:77], v[6:7]
	v_pk_fma_f32 v[78:79], v[40:41], v[78:79], v[8:9]
	v_pk_mul_f32 v[80:81], v[94:95], v[138:139] op_sel_hi:[1,0]
	v_pk_mul_f32 v[82:83], v[100:101], v[138:139] op_sel_hi:[1,0]
	v_cvt_pk_bf16_f32 v72, v72, v73
	v_cvt_pk_bf16_f32 v73, v74, v75
	v_lshl_add_u64 v[74:75], v[24:25], 0, s[24:25]
	v_pk_fma_f32 v[82:83], v[44:45], v[82:83], v[12:13]
	v_pk_fma_f32 v[80:81], v[46:47], v[80:81], v[10:11]
	v_pk_mul_f32 v[84:85], v[98:99], v[138:139] op_sel_hi:[1,0]
	v_pk_mul_f32 v[86:87], v[102:103], v[138:139] op_sel_hi:[1,0]
	global_store_dwordx2 v[74:75], v[72:73], off sc0 sc1
	v_cvt_pk_bf16_f32 v72, v76, v77
	v_cvt_pk_bf16_f32 v73, v78, v79
	v_pk_fma_f32 v[86:87], v[52:53], v[86:87], v[16:17]
	v_pk_fma_f32 v[84:85], v[54:55], v[84:85], v[14:15]
	global_store_dwordx2 v[74:75], v[72:73], off offset:512 sc0 sc1
	v_cvt_pk_bf16_f32 v72, v80, v81
	v_cvt_pk_bf16_f32 v73, v82, v83
	global_store_dwordx2 v[74:75], v[72:73], off offset:1024 sc0 sc1
	v_cvt_pk_bf16_f32 v72, v84, v85
	v_cvt_pk_bf16_f32 v73, v86, v87
	global_store_dwordx2 v[74:75], v[72:73], off offset:1536 sc0 sc1
	v_pk_mul_f32 v[72:73], v[104:105], v[140:141] op_sel_hi:[1,0]
	v_pk_mul_f32 v[74:75], v[108:109], v[140:141] op_sel_hi:[1,0]
	v_pk_fma_f32 v[72:73], v[36:37], v[72:73], v[2:3]
	v_pk_fma_f32 v[74:75], v[34:35], v[74:75], v[4:5]
	v_pk_mul_f32 v[76:77], v[106:107], v[140:141] op_sel_hi:[1,0]
	v_pk_mul_f32 v[78:79], v[112:113], v[140:141] op_sel_hi:[1,0]
	v_rsq_f32_e32 v142, v137
	v_pk_fma_f32 v[78:79], v[40:41], v[78:79], v[8:9]
	v_pk_fma_f32 v[76:77], v[42:43], v[76:77], v[6:7]
	v_pk_mul_f32 v[80:81], v[110:111], v[140:141] op_sel_hi:[1,0]
	v_pk_mul_f32 v[82:83], v[116:117], v[140:141] op_sel_hi:[1,0]
	v_cvt_pk_bf16_f32 v72, v72, v73
	v_cvt_pk_bf16_f32 v73, v74, v75
; #define LAS __attribute__((address_space(3)))
; __device__ __forceinline__ unsigned pkb(float lo, float hi) { f32x2 v = {lo, hi}; bf16x2_t b = __builtin_convertvector(v, bf16x2_t); return __builtin_bit_cast(unsigned, b); }
; template <int R, bool RT = false>
; __device__ __forceinline__ void norm_phase(const NormArgs& a, LAS unsigned char* lds, bool ctx_rows, const float* ctx_src, const float* ctx_shift, const float* ctx_scale) {
;     ...
;             for (int q = 0; q < R; ++q) { const int row = row0 + rr + q;
;                 if (a.src16) { const f16* xr = a.src16 + (size_t)row * DM;
; #pragma unroll
;                     for (int j = 0; j < 4; ++j) { const f16x4 t = *(const f16x4*)(xr + 4 * lane + 256 * j); v[q][j] = (f32x4){(float)t[0], (float)t[1], (float)t[2], (float)t[3]};
;                         if constexpr (RT) { if (j == 0) *(LAS u32x2*)(hs + (rr + q) * 528 + 8 * lane) = __builtin_bit_cast(u32x2, t);
;                             else xp[rr / 4][q][j - 1] = __builtin_bit_cast(u32x2, t); } } }
;     ...
;             for (int q = 0; q < R; ++q) { const int row = row0 + rr + q;
; #pragma unroll
;                 for (int j = 0; j < 4; ++j) v[q][j] = (v[q][j] * rstd[q]) * A[j] + Sh[j];
;                 if (a.fout) {
; #pragma unroll
;                     for (int j = 0; j < 4; ++j) *(f32x4*)(a.fout + (size_t)row * DM + 4 * lane + 256 * j) = v[q][j];
;                 }
;                 if (a.hout) {
; #pragma unroll
;                     for (int j = 0; j < 4; ++j) { u32x2 w; if (a.hbf) { w.x = pkb(v[q][j][0], v[q][j][1]); w.y = pkb(v[q][j][2], v[q][j][3]); } else { w.x = pkh(v[q][j][0], v[q][j][1]); w.y = pkh(v[q][j][2], v[q][j][3]); } *(u32x2*)(a.hout + (size_t)row * DM + 4 * lane + 256 * j) = w; }
;                 }
	v_lshl_add_u64 v[74:75], v[24:25], 0, s[26:27]
	v_pk_fma_f32 v[82:83], v[44:45], v[82:83], v[12:13]
	v_pk_fma_f32 v[80:81], v[46:47], v[80:81], v[10:11]
	v_pk_mul_f32 v[84:85], v[114:115], v[140:141] op_sel_hi:[1,0]
	v_pk_mul_f32 v[86:87], v[118:119], v[140:141] op_sel_hi:[1,0]
	global_store_dwordx2 v[74:75], v[72:73], off sc0 sc1
	v_cvt_pk_bf16_f32 v72, v76, v77
	v_cvt_pk_bf16_f32 v73, v78, v79
	v_pk_fma_f32 v[86:87], v[52:53], v[86:87], v[16:17]
	v_pk_fma_f32 v[84:85], v[54:55], v[84:85], v[14:15]
	global_store_dwordx2 v[74:75], v[72:73], off offset:512 sc0 sc1
	v_cvt_pk_bf16_f32 v72, v80, v81
	v_cvt_pk_bf16_f32 v73, v82, v83
	global_store_dwordx2 v[74:75], v[72:73], off offset:1024 sc0 sc1
	v_cvt_pk_bf16_f32 v72, v84, v85
	v_cvt_pk_bf16_f32 v73, v86, v87
	global_store_dwordx2 v[74:75], v[72:73], off offset:1536 sc0 sc1
	v_pk_mul_f32 v[72:73], v[120:121], v[142:143] op_sel_hi:[1,0]
	v_pk_mul_f32 v[74:75], v[122:123], v[142:143] op_sel_hi:[1,0]
	v_pk_fma_f32 v[72:73], v[36:37], v[72:73], v[2:3]
	v_pk_fma_f32 v[74:75], v[34:35], v[74:75], v[4:5]
	v_pk_mul_f32 v[76:77], v[124:125], v[142:143] op_sel_hi:[1,0]
	v_pk_mul_f32 v[78:79], v[128:129], v[142:143] op_sel_hi:[1,0]
	v_pk_fma_f32 v[76:77], v[42:43], v[76:77], v[6:7]
	v_pk_fma_f32 v[78:79], v[40:41], v[78:79], v[8:9]
	v_pk_mul_f32 v[80:81], v[126:127], v[142:143] op_sel_hi:[1,0]
	v_pk_mul_f32 v[82:83], v[132:133], v[142:143] op_sel_hi:[1,0]
	v_cvt_pk_bf16_f32 v72, v72, v73
	v_cvt_pk_bf16_f32 v73, v74, v75
	v_lshl_add_u64 v[74:75], v[24:25], 0, s[28:29]
	v_pk_fma_f32 v[82:83], v[44:45], v[82:83], v[12:13]
	v_pk_fma_f32 v[80:81], v[46:47], v[80:81], v[10:11]
	v_pk_mul_f32 v[84:85], v[130:131], v[142:143] op_sel_hi:[1,0]
	v_pk_mul_f32 v[86:87], v[134:135], v[142:143] op_sel_hi:[1,0]
	global_store_dwordx2 v[74:75], v[72:73], off sc0 sc1
	v_cvt_pk_bf16_f32 v72, v76, v77
	v_cvt_pk_bf16_f32 v73, v78, v79
	v_pk_fma_f32 v[86:87], v[52:53], v[86:87], v[16:17]
	v_pk_fma_f32 v[84:85], v[54:55], v[84:85], v[14:15]
	global_store_dwordx2 v[74:75], v[72:73], off offset:512 sc0 sc1
	v_cvt_pk_bf16_f32 v72, v80, v81
	v_cvt_pk_bf16_f32 v73, v82, v83
	s_add_i32 s2, s14, 4
	s_add_i32 s24, s14, 5
	global_store_dwordx2 v[74:75], v[72:73], off offset:1024 sc0 sc1
	v_cvt_pk_bf16_f32 v72, v84, v85
	v_cvt_pk_bf16_f32 v73, v86, v87
	s_ashr_i32 s3, s2, 31
	s_ashr_i32 s25, s24, 31
	global_store_dwordx2 v[74:75], v[72:73], off offset:1536 sc0 sc1
	s_lshl_b64 s[2:3], s[2:3], 11
	s_lshl_b64 s[24:25], s[24:25], 11
	v_lshl_add_u64 v[72:73], v[22:23], 0, s[2:3]
	v_lshl_add_u64 v[84:85], v[22:23], 0, s[24:25]
	global_load_dwordx2 v[78:79], v[72:73], off nt
	global_load_dwordx2 v[76:77], v[72:73], off offset:512 nt
	global_load_dwordx2 v[74:75], v[72:73], off offset:1024 nt
	global_load_dwordx2 v[80:81], v[84:85], off nt
	s_add_i32 s28, s14, 7
	s_add_i32 s26, s14, 6
	s_ashr_i32 s29, s28, 31
	s_ashr_i32 s27, s26, 31
	s_lshl_b64 s[28:29], s[28:29], 11
	s_lshl_b64 s[26:27], s[26:27], 11
	v_lshl_add_u64 v[154:155], v[22:23], 0, s[28:29]
	global_load_dwordx2 v[82:83], v[84:85], off offset:512 nt
	global_load_dwordx2 v[92:93], v[154:155], off nt
	global_load_dwordx2 v[94:95], v[154:155], off offset:512 nt
	v_cndmask_b32_e64 v165, 0, v142, s[4:5]
	global_load_dwordx2 v[72:73], v[72:73], off offset:1536 nt
	s_waitcnt vmcnt(7)
	v_cvt_f32_f16_e32 v96, v78
	v_cvt_f32_f16_sdwa v97, v78 dst_sel:DWORD dst_unused:UNUSED_PAD src0_sel:WORD_1
	v_cvt_f32_f16_e32 v100, v79
	v_cvt_f32_f16_sdwa v101, v79 dst_sel:DWORD dst_unused:UNUSED_PAD src0_sel:WORD_1
	s_waitcnt vmcnt(4)
	v_cvt_f32_f16_e32 v112, v80
	v_cvt_f32_f16_sdwa v113, v80 dst_sel:DWORD dst_unused:UNUSED_PAD src0_sel:WORD_1
	v_cvt_f32_f16_e32 v114, v81
	v_cvt_f32_f16_sdwa v115, v81 dst_sel:DWORD dst_unused:UNUSED_PAD src0_sel:WORD_1
	ds_write2_b64 v225, v[78:79], v[80:81] offset0:8 offset1:74
	global_load_dwordx2 v[80:81], v[84:85], off offset:1024 nt
	global_load_dwordx2 v[78:79], v[84:85], off offset:1536 nt
	v_lshl_add_u64 v[84:85], v[22:23], 0, s[26:27]
	global_load_dwordx2 v[90:91], v[84:85], off nt
	global_load_dwordx2 v[88:89], v[84:85], off offset:512 nt
	global_load_dwordx2 v[86:87], v[84:85], off offset:1024 nt
	s_waitcnt vmcnt(7)
	v_cvt_f32_f16_e32 v144, v92
	global_load_dwordx2 v[84:85], v[84:85], off offset:1536 nt
	v_cvt_f32_f16_sdwa v145, v92 dst_sel:DWORD dst_unused:UNUSED_PAD src0_sel:WORD_1
	v_cvt_f32_f16_e32 v146, v93
	v_cvt_f32_f16_sdwa v147, v93 dst_sel:DWORD dst_unused:UNUSED_PAD src0_sel:WORD_1
	v_cvt_f32_f16_e32 v98, v76
	v_cvt_f32_f16_sdwa v99, v76 dst_sel:DWORD dst_unused:UNUSED_PAD src0_sel:WORD_1
	v_cvt_f32_f16_e32 v104, v77
	v_cvt_f32_f16_sdwa v105, v77 dst_sel:DWORD dst_unused:UNUSED_PAD src0_sel:WORD_1
	v_cvt_f32_f16_e32 v102, v74
	v_cvt_f32_f16_sdwa v103, v74 dst_sel:DWORD dst_unused:UNUSED_PAD src0_sel:WORD_1
	v_cvt_f32_f16_e32 v108, v75
	v_cvt_f32_f16_sdwa v109, v75 dst_sel:DWORD dst_unused:UNUSED_PAD src0_sel:WORD_1
	v_pk_mul_f32 v[170:171], v[98:99], v[98:99]
	v_pk_mul_f32 v[172:173], v[104:105], v[104:105]
	s_waitcnt vmcnt(6)
; #define LAS __attribute__((address_space(3)))
; template <int R, bool RT = false>
; __device__ __forceinline__ void norm_phase(const NormArgs& a, LAS unsigned char* lds, bool ctx_rows, const float* ctx_src, const float* ctx_shift, const float* ctx_scale) {
;     ...
;             for (int q = 0; q < R; ++q) { const int row = row0 + rr + q;
;                 if (a.src16) { const f16* xr = a.src16 + (size_t)row * DM;
; #pragma unroll
;                     for (int j = 0; j < 4; ++j) { const f16x4 t = *(const f16x4*)(xr + 4 * lane + 256 * j); v[q][j] = (f32x4){(float)t[0], (float)t[1], (float)t[2], (float)t[3]};
;                         if constexpr (RT) { if (j == 0) *(LAS u32x2*)(hs + (rr + q) * 528 + 8 * lane) = __builtin_bit_cast(u32x2, t);
;                             else xp[rr / 4][q][j - 1] = __builtin_bit_cast(u32x2, t); } } }
;     ...
;             for (int q = 0; q < R; ++q) { float ss = 0.f;
; #pragma unroll
;                 for (int j = 0; j < 4; ++j) ss += (v[q][j][0] * v[q][j][0] + v[q][j][1] * v[q][j][1]) + (v[q][j][2] * v[q][j][2] + v[q][j][3] * v[q][j][3]);
;                 rstd[q] = __builtin_amdgcn_rsqf(wave_sum(ss) * (1.f / DM) + EPS);
;                 if constexpr (RT) rsel[q] = ((lane >> 4) == rr / 4) ? rstd[q] : rsel[q]; }
	v_cvt_f32_f16_e32 v106, v72
	v_cvt_f32_f16_sdwa v107, v72 dst_sel:DWORD dst_unused:UNUSED_PAD src0_sel:WORD_1
	v_cvt_f32_f16_e32 v110, v73
	v_cvt_f32_f16_sdwa v111, v73 dst_sel:DWORD dst_unused:UNUSED_PAD src0_sel:WORD_1
	v_pk_mul_f32 v[166:167], v[96:97], v[96:97]
	v_pk_mul_f32 v[168:169], v[100:101], v[100:101]
	v_add_f32_e32 v160, v172, v173
	v_add_f32_e32 v162, v170, v171
	v_add_f32_e32 v160, v162, v160
	v_add_f32_e32 v162, v168, v169
	v_add_f32_e32 v166, v166, v167
	v_pk_mul_f32 v[174:175], v[102:103], v[102:103]
	v_pk_mul_f32 v[176:177], v[108:109], v[108:109]
	v_add_f32_e32 v162, v166, v162
	v_add_f32_e32 v160, v162, v160
	v_add_f32_e32 v162, v176, v177
	v_add_f32_e32 v166, v174, v175
	v_pk_mul_f32 v[178:179], v[106:107], v[106:107]
	v_pk_mul_f32 v[180:181], v[110:111], v[110:111]
	v_add_f32_e32 v162, v166, v162
	v_add_f32_e32 v160, v160, v162
	v_add_f32_e32 v162, v180, v181
	v_add_f32_e32 v166, v178, v179
	v_add_f32_e32 v162, v166, v162
	v_add_f32_e32 v160, v160, v162
	v_mov_b32_e32 v162, 0
	v_cvt_f32_f16_e32 v116, v82
	v_add_f32_dpp v160, v160, v160 quad_perm:[1,0,3,2] row_mask:0xf bank_mask:0xf bound_ctrl:1
	v_cvt_f32_f16_sdwa v117, v82 dst_sel:DWORD dst_unused:UNUSED_PAD src0_sel:WORD_1
	v_cvt_f32_f16_e32 v120, v83
	v_add_f32_dpp v160, v160, v160 quad_perm:[2,3,0,1] row_mask:0xf bank_mask:0xf bound_ctrl:1
	v_cvt_f32_f16_sdwa v121, v83 dst_sel:DWORD dst_unused:UNUSED_PAD src0_sel:WORD_1
	v_pk_mul_f32 v[170:171], v[116:117], v[116:117]
	v_add_f32_dpp v160, v160, v160 row_half_mirror row_mask:0xf bank_mask:0xf bound_ctrl:1
	v_pk_mul_f32 v[166:167], v[112:113], v[112:113]
	v_pk_mul_f32 v[172:173], v[120:121], v[120:121]
	v_add_f32_dpp v160, v160, v160 row_mirror row_mask:0xf bank_mask:0xf bound_ctrl:1
	v_pk_mul_f32 v[168:169], v[114:115], v[114:115]
	v_add_f32_e32 v166, v166, v167
	v_mov_b32_dpp v162, v160 row_bcast:15 row_mask:0xa bank_mask:0xf
	v_add_f32_e32 v160, v160, v162
	v_mov_b32_e32 v162, 0
	s_waitcnt vmcnt(5)
	v_cvt_f32_f16_e32 v118, v80
	v_mov_b32_dpp v162, v160 row_bcast:31 row_mask:0xc bank_mask:0xf
	v_add_f32_e32 v160, v160, v162
	s_waitcnt vmcnt(3)
	ds_write2_b64 v225, v[90:91], v[92:93] offset0:140 offset1:206
	global_load_dwordx2 v[92:93], v[154:155], off offset:1024 nt
	v_cvt_f32_f16_e32 v128, v90
	v_cvt_f32_f16_sdwa v129, v90 dst_sel:DWORD dst_unused:UNUSED_PAD src0_sel:WORD_1
	v_cvt_f32_f16_e32 v132, v91
	v_cvt_f32_f16_sdwa v133, v91 dst_sel:DWORD dst_unused:UNUSED_PAD src0_sel:WORD_1
	global_load_dwordx2 v[90:91], v[154:155], off offset:1536 nt
	v_readlane_b32 s0, v160, 63
	v_cvt_f32_f16_sdwa v119, v80 dst_sel:DWORD dst_unused:UNUSED_PAD src0_sel:WORD_1
	v_cvt_f32_f16_e32 v124, v81
	v_fma_f32 v160, s0, v214, v213
	v_rsq_f32_e32 v160, v160
	v_cvt_f32_f16_sdwa v125, v81 dst_sel:DWORD dst_unused:UNUSED_PAD src0_sel:WORD_1
	v_cvt_f32_f16_e32 v122, v78
	v_cvt_f32_f16_sdwa v123, v78 dst_sel:DWORD dst_unused:UNUSED_PAD src0_sel:WORD_1
	v_cvt_f32_f16_e32 v126, v79
	v_cvt_f32_f16_sdwa v127, v79 dst_sel:DWORD dst_unused:UNUSED_PAD src0_sel:WORD_1
	v_cndmask_b32_e64 v186, v161, v160, s[6:7]
	v_add_f32_e32 v161, v172, v173
	v_add_f32_e32 v162, v170, v171
	v_add_f32_e32 v161, v162, v161
	v_add_f32_e32 v162, v168, v169
	v_pk_mul_f32 v[174:175], v[118:119], v[118:119]
	v_pk_mul_f32 v[176:177], v[124:125], v[124:125]
	v_add_f32_e32 v162, v166, v162
	v_add_f32_e32 v161, v162, v161
	v_add_f32_e32 v162, v176, v177
	v_add_f32_e32 v166, v174, v175
	v_pk_mul_f32 v[178:179], v[122:123], v[122:123]
	v_pk_mul_f32 v[180:181], v[126:127], v[126:127]
	v_add_f32_e32 v162, v166, v162
	v_add_f32_e32 v161, v161, v162
	v_add_f32_e32 v162, v180, v181
	v_add_f32_e32 v166, v178, v179
	v_add_f32_e32 v162, v166, v162
	v_add_f32_e32 v161, v161, v162
	v_mov_b32_e32 v162, 0
	s_waitcnt vmcnt(4)
	v_cvt_f32_f16_e32 v130, v88
	v_add_f32_dpp v161, v161, v161 quad_perm:[1,0,3,2] row_mask:0xf bank_mask:0xf bound_ctrl:1
	v_cvt_f32_f16_sdwa v131, v88 dst_sel:DWORD dst_unused:UNUSED_PAD src0_sel:WORD_1
	v_cvt_f32_f16_e32 v136, v89
	v_add_f32_dpp v161, v161, v161 quad_perm:[2,3,0,1] row_mask:0xf bank_mask:0xf bound_ctrl:1
	v_cvt_f32_f16_sdwa v137, v89 dst_sel:DWORD dst_unused:UNUSED_PAD src0_sel:WORD_1
	s_waitcnt vmcnt(3)
	v_cvt_f32_f16_e32 v134, v86
	v_add_f32_dpp v161, v161, v161 row_half_mirror row_mask:0xf bank_mask:0xf bound_ctrl:1
	v_cvt_f32_f16_sdwa v135, v86 dst_sel:DWORD dst_unused:UNUSED_PAD src0_sel:WORD_1
	v_cvt_f32_f16_e32 v140, v87
	v_add_f32_dpp v161, v161, v161 row_mirror row_mask:0xf bank_mask:0xf bound_ctrl:1
	v_cvt_f32_f16_sdwa v141, v87 dst_sel:DWORD dst_unused:UNUSED_PAD src0_sel:WORD_1
	v_pk_mul_f32 v[170:171], v[130:131], v[130:131]
	v_mov_b32_dpp v162, v161 row_bcast:15 row_mask:0xa bank_mask:0xf
	v_add_f32_e32 v161, v161, v162
	v_mov_b32_e32 v162, 0
	v_pk_mul_f32 v[172:173], v[136:137], v[136:137]
	s_waitcnt vmcnt(2)
; __device__ __forceinline__ unsigned pkb(float lo, float hi) { f32x2 v = {lo, hi}; bf16x2_t b = __builtin_convertvector(v, bf16x2_t); return __builtin_bit_cast(unsigned, b); }
; template <int R, bool RT = false>
; __device__ __forceinline__ void norm_phase(const NormArgs& a, LAS unsigned char* lds, bool ctx_rows, const float* ctx_src, const float* ctx_shift, const float* ctx_scale) {
;     ...
;             for (int q = 0; q < R; ++q) { float ss = 0.f;
; #pragma unroll
;                 for (int j = 0; j < 4; ++j) ss += (v[q][j][0] * v[q][j][0] + v[q][j][1] * v[q][j][1]) + (v[q][j][2] * v[q][j][2] + v[q][j][3] * v[q][j][3]);
;                 rstd[q] = __builtin_amdgcn_rsqf(wave_sum(ss) * (1.f / DM) + EPS);
;                 if constexpr (RT) rsel[q] = ((lane >> 4) == rr / 4) ? rstd[q] : rsel[q]; }
; #pragma unroll
;             for (int q = 0; q < R; ++q) { const int row = row0 + rr + q;
; #pragma unroll
;                 for (int j = 0; j < 4; ++j) v[q][j] = (v[q][j] * rstd[q]) * A[j] + Sh[j];
;                 if (a.fout) {
; #pragma unroll
;                     for (int j = 0; j < 4; ++j) *(f32x4*)(a.fout + (size_t)row * DM + 4 * lane + 256 * j) = v[q][j];
;                 }
;                 if (a.hout) {
; #pragma unroll
;                     for (int j = 0; j < 4; ++j) { u32x2 w; if (a.hbf) { w.x = pkb(v[q][j][0], v[q][j][1]); w.y = pkb(v[q][j][2], v[q][j][3]); } else { w.x = pkh(v[q][j][0], v[q][j][1]); w.y = pkh(v[q][j][2], v[q][j][3]); } *(u32x2*)(a.hout + (size_t)row * DM + 4 * lane + 256 * j) = w; }
;                 }
	v_cvt_f32_f16_e32 v138, v84
	v_mov_b32_dpp v162, v161 row_bcast:31 row_mask:0xc bank_mask:0xf
	v_add_f32_e32 v161, v161, v162
	v_cvt_f32_f16_sdwa v139, v84 dst_sel:DWORD dst_unused:UNUSED_PAD src0_sel:WORD_1
	v_readlane_b32 s0, v161, 63
	v_cvt_f32_f16_e32 v142, v85
	v_cvt_f32_f16_sdwa v143, v85 dst_sel:DWORD dst_unused:UNUSED_PAD src0_sel:WORD_1
	v_fma_f32 v161, s0, v214, v213
	v_rsq_f32_e32 v162, v161
	v_pk_mul_f32 v[166:167], v[128:129], v[128:129]
	v_pk_mul_f32 v[168:169], v[132:133], v[132:133]
	v_add_f32_e32 v161, v172, v173
	v_cndmask_b32_e64 v187, v163, v162, s[6:7]
	v_add_f32_e32 v163, v170, v171
	v_add_f32_e32 v161, v163, v161
	v_add_f32_e32 v163, v168, v169
	v_add_f32_e32 v166, v166, v167
	v_pk_mul_f32 v[174:175], v[134:135], v[134:135]
	v_pk_mul_f32 v[176:177], v[140:141], v[140:141]
	v_add_f32_e32 v163, v166, v163
	v_add_f32_e32 v161, v163, v161
	v_add_f32_e32 v163, v176, v177
	v_add_f32_e32 v166, v174, v175
	v_pk_mul_f32 v[178:179], v[138:139], v[138:139]
	v_pk_mul_f32 v[180:181], v[142:143], v[142:143]
	v_add_f32_e32 v163, v166, v163
	v_add_f32_e32 v161, v161, v163
	v_add_f32_e32 v163, v180, v181
	v_add_f32_e32 v166, v178, v179
	v_add_f32_e32 v163, v166, v163
	v_add_f32_e32 v161, v161, v163
	v_mov_b32_e32 v163, 0
	v_cvt_f32_f16_e32 v148, v94
	v_add_f32_dpp v161, v161, v161 quad_perm:[1,0,3,2] row_mask:0xf bank_mask:0xf bound_ctrl:1
	v_cvt_f32_f16_sdwa v149, v94 dst_sel:DWORD dst_unused:UNUSED_PAD src0_sel:WORD_1
	v_cvt_f32_f16_e32 v152, v95
	v_add_f32_dpp v161, v161, v161 quad_perm:[2,3,0,1] row_mask:0xf bank_mask:0xf bound_ctrl:1
	v_cvt_f32_f16_sdwa v153, v95 dst_sel:DWORD dst_unused:UNUSED_PAD src0_sel:WORD_1
	s_waitcnt vmcnt(1)
	v_cvt_f32_f16_e32 v150, v92
	v_add_f32_dpp v161, v161, v161 row_half_mirror row_mask:0xf bank_mask:0xf bound_ctrl:1
	v_cvt_f32_f16_sdwa v151, v92 dst_sel:DWORD dst_unused:UNUSED_PAD src0_sel:WORD_1
	v_cvt_f32_f16_e32 v156, v93
	v_add_f32_dpp v161, v161, v161 row_mirror row_mask:0xf bank_mask:0xf bound_ctrl:1
	v_cvt_f32_f16_sdwa v157, v93 dst_sel:DWORD dst_unused:UNUSED_PAD src0_sel:WORD_1
	v_pk_mul_f32 v[168:169], v[144:145], v[144:145]
	v_mov_b32_dpp v163, v161 row_bcast:15 row_mask:0xa bank_mask:0xf
	v_add_f32_e32 v161, v161, v163
	v_mov_b32_e32 v163, 0
	v_pk_mul_f32 v[170:171], v[146:147], v[146:147]
	s_waitcnt vmcnt(0)
	v_cvt_f32_f16_e32 v154, v90
	v_mov_b32_dpp v163, v161 row_bcast:31 row_mask:0xc bank_mask:0xf
	v_add_f32_e32 v161, v161, v163
	v_cvt_f32_f16_sdwa v155, v90 dst_sel:DWORD dst_unused:UNUSED_PAD src0_sel:WORD_1
	v_readlane_b32 s0, v161, 63
	v_cvt_f32_f16_e32 v158, v91
	v_cvt_f32_f16_sdwa v159, v91 dst_sel:DWORD dst_unused:UNUSED_PAD src0_sel:WORD_1
	v_fma_f32 v161, s0, v214, v213
	v_rsq_f32_e32 v166, v161
	v_pk_mul_f32 v[172:173], v[148:149], v[148:149]
	v_pk_mul_f32 v[174:175], v[152:153], v[152:153]
	v_add_f32_e32 v161, v170, v171
	v_add_f32_e32 v163, v168, v169
	v_cndmask_b32_e64 v189, v164, v166, s[6:7]
	v_add_f32_e32 v161, v163, v161
	v_add_f32_e32 v163, v174, v175
	v_add_f32_e32 v164, v172, v173
	v_pk_mul_f32 v[176:177], v[150:151], v[150:151]
	v_pk_mul_f32 v[178:179], v[156:157], v[156:157]
	v_add_f32_e32 v163, v164, v163
	v_add_f32_e32 v161, v161, v163
	v_add_f32_e32 v163, v178, v179
	v_add_f32_e32 v164, v176, v177
	v_pk_mul_f32 v[180:181], v[154:155], v[154:155]
	v_pk_mul_f32 v[182:183], v[158:159], v[158:159]
	v_add_f32_e32 v163, v164, v163
	v_add_f32_e32 v161, v161, v163
	v_add_f32_e32 v163, v182, v183
	v_add_f32_e32 v164, v180, v181
	v_add_f32_e32 v163, v164, v163
	v_add_f32_e32 v161, v161, v163
	v_mov_b32_e32 v163, 0
	s_nop 0
	v_add_f32_dpp v161, v161, v161 quad_perm:[1,0,3,2] row_mask:0xf bank_mask:0xf bound_ctrl:1
	s_nop 1
	v_add_f32_dpp v161, v161, v161 quad_perm:[2,3,0,1] row_mask:0xf bank_mask:0xf bound_ctrl:1
	s_nop 1
	v_add_f32_dpp v161, v161, v161 row_half_mirror row_mask:0xf bank_mask:0xf bound_ctrl:1
	s_nop 1
	v_add_f32_dpp v161, v161, v161 row_mirror row_mask:0xf bank_mask:0xf bound_ctrl:1
	s_nop 1
	v_mov_b32_dpp v163, v161 row_bcast:15 row_mask:0xa bank_mask:0xf
	v_add_f32_e32 v161, v161, v163
	v_mov_b32_e32 v163, 0
	s_nop 1
	v_mov_b32_dpp v163, v161 row_bcast:31 row_mask:0xc bank_mask:0xf
	v_add_f32_e32 v161, v161, v163
	s_nop 0
	v_readlane_b32 s0, v161, 63
	s_nop 1
	v_fma_f32 v161, s0, v214, v213
	v_pk_mul_f32 v[96:97], v[96:97], v[160:161] op_sel_hi:[1,0]
	v_pk_mul_f32 v[100:101], v[100:101], v[160:161] op_sel_hi:[1,0]
	v_pk_fma_f32 v[96:97], v[36:37], v[96:97], v[2:3]
	v_pk_fma_f32 v[100:101], v[34:35], v[100:101], v[4:5]
	v_pk_mul_f32 v[98:99], v[98:99], v[160:161] op_sel_hi:[1,0]
	v_pk_mul_f32 v[104:105], v[104:105], v[160:161] op_sel_hi:[1,0]
	v_pk_fma_f32 v[98:99], v[42:43], v[98:99], v[6:7]
	v_pk_fma_f32 v[104:105], v[40:41], v[104:105], v[8:9]
	v_pk_mul_f32 v[102:103], v[102:103], v[160:161] op_sel_hi:[1,0]
	v_pk_mul_f32 v[108:109], v[108:109], v[160:161] op_sel_hi:[1,0]
	v_cvt_pk_bf16_f32 v96, v96, v97
	v_cvt_pk_bf16_f32 v97, v100, v101
	v_lshl_add_u64 v[100:101], v[24:25], 0, s[2:3]
	v_pk_fma_f32 v[108:109], v[44:45], v[108:109], v[12:13]
	v_pk_fma_f32 v[102:103], v[46:47], v[102:103], v[10:11]
	v_pk_mul_f32 v[106:107], v[106:107], v[160:161] op_sel_hi:[1,0]
	v_pk_mul_f32 v[110:111], v[110:111], v[160:161] op_sel_hi:[1,0]
	global_store_dwordx2 v[100:101], v[96:97], off sc0 sc1
	v_cvt_pk_bf16_f32 v96, v98, v99
	v_cvt_pk_bf16_f32 v97, v104, v105
	v_pk_fma_f32 v[110:111], v[52:53], v[110:111], v[16:17]
	v_pk_fma_f32 v[106:107], v[54:55], v[106:107], v[14:15]
	global_store_dwordx2 v[100:101], v[96:97], off offset:512 sc0 sc1
	v_cvt_pk_bf16_f32 v96, v102, v103
	v_cvt_pk_bf16_f32 v97, v108, v109
	global_store_dwordx2 v[100:101], v[96:97], off offset:1024 sc0 sc1
; #define LAS __attribute__((address_space(3)))
; template <int R, bool RT = false>
; __device__ __forceinline__ void norm_phase(const NormArgs& a, LAS unsigned char* lds, bool ctx_rows, const float* ctx_src, const float* ctx_shift, const float* ctx_scale) {
;     ...
;             for (int q = 0; q < R; ++q) { const int row = row0 + rr + q;
;                 if (a.src16) { const f16* xr = a.src16 + (size_t)row * DM;
; #pragma unroll
;                     for (int j = 0; j < 4; ++j) { const f16x4 t = *(const f16x4*)(xr + 4 * lane + 256 * j); v[q][j] = (f32x4){(float)t[0], (float)t[1], (float)t[2], (float)t[3]};
;                         if constexpr (RT) { if (j == 0) *(LAS u32x2*)(hs + (rr + q) * 528 + 8 * lane) = __builtin_bit_cast(u32x2, t);
;                             else xp[rr / 4][q][j - 1] = __builtin_bit_cast(u32x2, t); } } }
;                 else { const float* xr = a.src + (size_t)row * DM;
; #pragma unroll
;                     for (int j = 0; j < 4; ++j) v[q][j] = *(const f32x4*)(xr + 4 * lane + 256 * j); } }
;             if (a.y2) {
;                 unsigned long long mask[R]; int ee[R][4]; float wgt[R][4]; f16x4 ld[R][4][4];
;                 int cnt[R];
; #pragma unroll
;                 for (int q = 0; q < R; ++q) { mask[q] = __ballot(sl[q] >= 0); cnt[q] = __builtin_popcountll(mask[q]);
; #pragma unroll
;                     for (int i = 0; i < 4; ++i) { if (mask[q]) { ee[q][i] = __builtin_ctzll(mask[q]); mask[q] &= mask[q] - 1; wgt[q][i] = 1.f; } else { ee[q][i] = i ? ee[q][0] : 0; wgt[q][i] = 0.f; } }
; #pragma unroll
;                     for (int i = 0; i < 4; ++i) {
;                         if (i < cnt[q]) { int slot = __shfl(sl[q], ee[q][i]); slot = slot < 0 ? 0 : slot; const f16* yr = a.y2 + ((size_t)ee[q][i] * EROWS + b * CAP + slot) * DM + 4 * lane;
; #pragma unroll
;                             for (int j = 0; j < 4; ++j) ld[q][i][j] = *(const f16x4*)(yr + 256 * j); } } }
; #pragma unroll
;                 for (int q = 0; q < R; ++q) { const int row = row0 + rr + q;
;                     f32x4 cs[4];
; #pragma unroll
;                     for (int j = 0; j < 4; ++j) cs[j] = (f32x4){0.f, 0.f, 0.f, 0.f};
; #pragma unroll
;                     for (int i = 0; i < 4; ++i) if (i < cnt[q]) {
; #pragma unroll
	v_cvt_pk_bf16_f32 v96, v106, v107
	v_cvt_pk_bf16_f32 v97, v110, v111
	global_store_dwordx2 v[100:101], v[96:97], off offset:1536 sc0 sc1
	v_pk_mul_f32 v[96:97], v[112:113], v[162:163] op_sel_hi:[1,0]
	v_pk_mul_f32 v[98:99], v[114:115], v[162:163] op_sel_hi:[1,0]
	v_pk_fma_f32 v[96:97], v[36:37], v[96:97], v[2:3]
	v_pk_fma_f32 v[98:99], v[34:35], v[98:99], v[4:5]
	v_pk_mul_f32 v[100:101], v[116:117], v[162:163] op_sel_hi:[1,0]
	v_pk_mul_f32 v[102:103], v[120:121], v[162:163] op_sel_hi:[1,0]
	v_pk_fma_f32 v[100:101], v[42:43], v[100:101], v[6:7]
	v_pk_fma_f32 v[102:103], v[40:41], v[102:103], v[8:9]
	v_pk_mul_f32 v[104:105], v[118:119], v[162:163] op_sel_hi:[1,0]
	v_pk_mul_f32 v[106:107], v[124:125], v[162:163] op_sel_hi:[1,0]
	v_cvt_pk_bf16_f32 v96, v96, v97
	v_cvt_pk_bf16_f32 v97, v98, v99
	v_lshl_add_u64 v[98:99], v[24:25], 0, s[24:25]
	v_pk_fma_f32 v[106:107], v[44:45], v[106:107], v[12:13]
	v_pk_fma_f32 v[104:105], v[46:47], v[104:105], v[10:11]
	v_pk_mul_f32 v[108:109], v[122:123], v[162:163] op_sel_hi:[1,0]
	v_pk_mul_f32 v[110:111], v[126:127], v[162:163] op_sel_hi:[1,0]
	global_store_dwordx2 v[98:99], v[96:97], off sc0 sc1
	v_cvt_pk_bf16_f32 v96, v100, v101
	v_cvt_pk_bf16_f32 v97, v102, v103
	v_pk_fma_f32 v[110:111], v[52:53], v[110:111], v[16:17]
	v_pk_fma_f32 v[108:109], v[54:55], v[108:109], v[14:15]
	global_store_dwordx2 v[98:99], v[96:97], off offset:512 sc0 sc1
	v_cvt_pk_bf16_f32 v96, v104, v105
	v_cvt_pk_bf16_f32 v97, v106, v107
	global_store_dwordx2 v[98:99], v[96:97], off offset:1024 sc0 sc1
	v_cvt_pk_bf16_f32 v96, v108, v109
	v_cvt_pk_bf16_f32 v97, v110, v111
	global_store_dwordx2 v[98:99], v[96:97], off offset:1536 sc0 sc1
	v_pk_mul_f32 v[96:97], v[128:129], v[166:167] op_sel_hi:[1,0]
	v_pk_mul_f32 v[98:99], v[132:133], v[166:167] op_sel_hi:[1,0]
	v_pk_fma_f32 v[96:97], v[36:37], v[96:97], v[2:3]
	v_pk_fma_f32 v[98:99], v[34:35], v[98:99], v[4:5]
	v_pk_mul_f32 v[100:101], v[130:131], v[166:167] op_sel_hi:[1,0]
	v_pk_mul_f32 v[102:103], v[136:137], v[166:167] op_sel_hi:[1,0]
	v_rsq_f32_e32 v164, v161
	v_pk_fma_f32 v[102:103], v[40:41], v[102:103], v[8:9]
	v_pk_fma_f32 v[100:101], v[42:43], v[100:101], v[6:7]
	v_pk_mul_f32 v[104:105], v[134:135], v[166:167] op_sel_hi:[1,0]
	v_pk_mul_f32 v[106:107], v[140:141], v[166:167] op_sel_hi:[1,0]
	v_cvt_pk_bf16_f32 v96, v96, v97
	v_cvt_pk_bf16_f32 v97, v98, v99
	v_lshl_add_u64 v[98:99], v[24:25], 0, s[26:27]
	v_pk_fma_f32 v[106:107], v[44:45], v[106:107], v[12:13]
	v_pk_fma_f32 v[104:105], v[46:47], v[104:105], v[10:11]
	v_pk_mul_f32 v[108:109], v[138:139], v[166:167] op_sel_hi:[1,0]
	v_pk_mul_f32 v[110:111], v[142:143], v[166:167] op_sel_hi:[1,0]
	global_store_dwordx2 v[98:99], v[96:97], off sc0 sc1
	v_cvt_pk_bf16_f32 v96, v100, v101
	v_cvt_pk_bf16_f32 v97, v102, v103
	v_pk_fma_f32 v[110:111], v[52:53], v[110:111], v[16:17]
	v_pk_fma_f32 v[108:109], v[54:55], v[108:109], v[14:15]
	global_store_dwordx2 v[98:99], v[96:97], off offset:512 sc0 sc1
	v_cvt_pk_bf16_f32 v96, v104, v105
	v_cvt_pk_bf16_f32 v97, v106, v107
	global_store_dwordx2 v[98:99], v[96:97], off offset:1024 sc0 sc1
	v_cvt_pk_bf16_f32 v96, v108, v109
	v_cvt_pk_bf16_f32 v97, v110, v111
	global_store_dwordx2 v[98:99], v[96:97], off offset:1536 sc0 sc1
	v_pk_mul_f32 v[96:97], v[144:145], v[164:165] op_sel_hi:[1,0]
	v_pk_mul_f32 v[98:99], v[146:147], v[164:165] op_sel_hi:[1,0]
	v_pk_fma_f32 v[96:97], v[36:37], v[96:97], v[2:3]
	v_pk_fma_f32 v[98:99], v[34:35], v[98:99], v[4:5]
	v_pk_mul_f32 v[100:101], v[148:149], v[164:165] op_sel_hi:[1,0]
	v_pk_mul_f32 v[102:103], v[152:153], v[164:165] op_sel_hi:[1,0]
	v_pk_fma_f32 v[100:101], v[42:43], v[100:101], v[6:7]
	v_pk_fma_f32 v[102:103], v[40:41], v[102:103], v[8:9]
	v_pk_mul_f32 v[104:105], v[150:151], v[164:165] op_sel_hi:[1,0]
	v_pk_mul_f32 v[106:107], v[156:157], v[164:165] op_sel_hi:[1,0]
	v_cvt_pk_bf16_f32 v96, v96, v97
	v_cvt_pk_bf16_f32 v97, v98, v99
	v_lshl_add_u64 v[98:99], v[24:25], 0, s[28:29]
	s_add_i32 s2, s14, 8
	v_pk_fma_f32 v[106:107], v[44:45], v[106:107], v[12:13]
	v_pk_fma_f32 v[104:105], v[46:47], v[104:105], v[10:11]
	v_pk_mul_f32 v[108:109], v[154:155], v[164:165] op_sel_hi:[1,0]
	v_pk_mul_f32 v[110:111], v[158:159], v[164:165] op_sel_hi:[1,0]
	global_store_dwordx2 v[98:99], v[96:97], off sc0 sc1
	v_cvt_pk_bf16_f32 v96, v100, v101
	v_cvt_pk_bf16_f32 v97, v102, v103
	s_ashr_i32 s3, s2, 31
	v_pk_fma_f32 v[110:111], v[52:53], v[110:111], v[16:17]
	v_pk_fma_f32 v[108:109], v[54:55], v[108:109], v[14:15]
	global_store_dwordx2 v[98:99], v[96:97], off offset:512 sc0 sc1
	v_cvt_pk_bf16_f32 v96, v104, v105
	v_cvt_pk_bf16_f32 v97, v106, v107
	s_lshl_b64 s[24:25], s[2:3], 11
	s_add_i32 s2, s14, 9
	global_store_dwordx2 v[98:99], v[96:97], off offset:1024 sc0 sc1
	v_cvt_pk_bf16_f32 v96, v108, v109
	v_cvt_pk_bf16_f32 v97, v110, v111
	s_ashr_i32 s3, s2, 31
	global_store_dwordx2 v[98:99], v[96:97], off offset:1536 sc0 sc1
	s_lshl_b64 s[26:27], s[2:3], 11
	v_lshl_add_u64 v[96:97], v[22:23], 0, s[24:25]
	v_lshl_add_u64 v[108:109], v[22:23], 0, s[26:27]
	global_load_dwordx2 v[102:103], v[96:97], off nt
	global_load_dwordx2 v[100:101], v[96:97], off offset:512 nt
	global_load_dwordx2 v[98:99], v[96:97], off offset:1024 nt
	global_load_dwordx2 v[104:105], v[108:109], off nt
	s_add_i32 s2, s14, 10
	s_ashr_i32 s3, s2, 31
	s_lshl_b64 s[28:29], s[2:3], 11
	s_add_i32 s2, s14, 11
	s_ashr_i32 s3, s2, 31
	s_lshl_b64 s[30:31], s[2:3], 11
	v_lshl_add_u64 v[178:179], v[22:23], 0, s[30:31]
	global_load_dwordx2 v[106:107], v[108:109], off offset:512 nt
	global_load_dwordx2 v[116:117], v[178:179], off nt
	global_load_dwordx2 v[118:119], v[178:179], off offset:512 nt
	v_cndmask_b32_e64 v185, v165, v164, s[6:7]
	global_load_dwordx2 v[96:97], v[96:97], off offset:1536 nt
	s_add_i32 s2, s14, 12
	s_ashr_i32 s3, s2, 31
	s_waitcnt vmcnt(7)
; #define LAS __attribute__((address_space(3)))
; template <int R, bool RT = false>
; __device__ __forceinline__ void norm_phase(const NormArgs& a, LAS unsigned char* lds, bool ctx_rows, const float* ctx_src, const float* ctx_shift, const float* ctx_scale) {
;     ...
;             for (int q = 0; q < R; ++q) { const int row = row0 + rr + q;
;                 if (a.src16) { const f16* xr = a.src16 + (size_t)row * DM;
; #pragma unroll
;                     for (int j = 0; j < 4; ++j) { const f16x4 t = *(const f16x4*)(xr + 4 * lane + 256 * j); v[q][j] = (f32x4){(float)t[0], (float)t[1], (float)t[2], (float)t[3]};
;                         if constexpr (RT) { if (j == 0) *(LAS u32x2*)(hs + (rr + q) * 528 + 8 * lane) = __builtin_bit_cast(u32x2, t);
;                             else xp[rr / 4][q][j - 1] = __builtin_bit_cast(u32x2, t); } } }
;                 else { const float* xr = a.src + (size_t)row * DM;
; #pragma unroll
;                     for (int j = 0; j < 4; ++j) v[q][j] = *(const f32x4*)(xr + 4 * lane + 256 * j); } }
;             if (a.y2) {
;                 unsigned long long mask[R]; int ee[R][4]; float wgt[R][4]; f16x4 ld[R][4][4];
;                 int cnt[R];
; #pragma unroll
;                 for (int q = 0; q < R; ++q) { mask[q] = __ballot(sl[q] >= 0); cnt[q] = __builtin_popcountll(mask[q]);
; #pragma unroll
;                     for (int i = 0; i < 4; ++i) { if (mask[q]) { ee[q][i] = __builtin_ctzll(mask[q]); mask[q] &= mask[q] - 1; wgt[q][i] = 1.f; } else { ee[q][i] = i ? ee[q][0] : 0; wgt[q][i] = 0.f; } }
; #pragma unroll
;                     for (int i = 0; i < 4; ++i) {
;                         if (i < cnt[q]) { int slot = __shfl(sl[q], ee[q][i]); slot = slot < 0 ? 0 : slot; const f16* yr = a.y2 + ((size_t)ee[q][i] * EROWS + b * CAP + slot) * DM + 4 * lane;
; #pragma unroll
;                             for (int j = 0; j < 4; ++j) ld[q][i][j] = *(const f16x4*)(yr + 256 * j); } } }
; #pragma unroll
;                 for (int q = 0; q < R; ++q) { const int row = row0 + rr + q;
;                     f32x4 cs[4];
; #pragma unroll
;                     for (int j = 0; j < 4; ++j) cs[j] = (f32x4){0.f, 0.f, 0.f, 0.f};
; #pragma unroll
;                     for (int i = 0; i < 4; ++i) if (i < cnt[q]) {
; #pragma unroll
	v_cvt_f32_f16_e32 v120, v102
	v_cvt_f32_f16_sdwa v121, v102 dst_sel:DWORD dst_unused:UNUSED_PAD src0_sel:WORD_1
	v_cvt_f32_f16_e32 v124, v103
	v_cvt_f32_f16_sdwa v125, v103 dst_sel:DWORD dst_unused:UNUSED_PAD src0_sel:WORD_1
	s_waitcnt vmcnt(4)
	v_cvt_f32_f16_e32 v136, v104
	v_cvt_f32_f16_sdwa v137, v104 dst_sel:DWORD dst_unused:UNUSED_PAD src0_sel:WORD_1
	v_cvt_f32_f16_e32 v138, v105
	v_cvt_f32_f16_sdwa v139, v105 dst_sel:DWORD dst_unused:UNUSED_PAD src0_sel:WORD_1
	ds_write2_b64 v226, v[102:103], v[104:105] offset0:16 offset1:82
	global_load_dwordx2 v[104:105], v[108:109], off offset:1024 nt
	global_load_dwordx2 v[102:103], v[108:109], off offset:1536 nt
	v_lshl_add_u64 v[108:109], v[22:23], 0, s[28:29]
	global_load_dwordx2 v[114:115], v[108:109], off nt
	global_load_dwordx2 v[112:113], v[108:109], off offset:512 nt
	global_load_dwordx2 v[110:111], v[108:109], off offset:1024 nt
	s_waitcnt vmcnt(7)
	v_cvt_f32_f16_e32 v168, v116
	global_load_dwordx2 v[108:109], v[108:109], off offset:1536 nt
	v_cvt_f32_f16_sdwa v169, v116 dst_sel:DWORD dst_unused:UNUSED_PAD src0_sel:WORD_1
	v_cvt_f32_f16_e32 v170, v117
	v_cvt_f32_f16_sdwa v171, v117 dst_sel:DWORD dst_unused:UNUSED_PAD src0_sel:WORD_1
	v_cvt_f32_f16_e32 v122, v100
	v_cvt_f32_f16_sdwa v123, v100 dst_sel:DWORD dst_unused:UNUSED_PAD src0_sel:WORD_1
	v_cvt_f32_f16_e32 v128, v101
	v_cvt_f32_f16_sdwa v129, v101 dst_sel:DWORD dst_unused:UNUSED_PAD src0_sel:WORD_1
	v_cvt_f32_f16_e32 v126, v98
	v_cvt_f32_f16_sdwa v127, v98 dst_sel:DWORD dst_unused:UNUSED_PAD src0_sel:WORD_1
	v_cvt_f32_f16_e32 v132, v99
	v_cvt_f32_f16_sdwa v133, v99 dst_sel:DWORD dst_unused:UNUSED_PAD src0_sel:WORD_1
	v_pk_mul_f32 v[194:195], v[122:123], v[122:123]
	v_pk_mul_f32 v[196:197], v[128:129], v[128:129]
	s_waitcnt vmcnt(6)
	v_cvt_f32_f16_e32 v130, v96
	v_cvt_f32_f16_sdwa v131, v96 dst_sel:DWORD dst_unused:UNUSED_PAD src0_sel:WORD_1
	v_cvt_f32_f16_e32 v134, v97
	v_cvt_f32_f16_sdwa v135, v97 dst_sel:DWORD dst_unused:UNUSED_PAD src0_sel:WORD_1
	v_pk_mul_f32 v[190:191], v[120:121], v[120:121]
	v_pk_mul_f32 v[192:193], v[124:125], v[124:125]
	v_add_f32_e32 v184, v196, v197
	v_add_f32_e32 v188, v194, v195
	v_add_f32_e32 v184, v188, v184
	v_add_f32_e32 v188, v192, v193
	v_add_f32_e32 v190, v190, v191
	v_pk_mul_f32 v[198:199], v[126:127], v[126:127]
	v_pk_mul_f32 v[200:201], v[132:133], v[132:133]
	v_add_f32_e32 v188, v190, v188
	v_add_f32_e32 v184, v188, v184
	v_add_f32_e32 v188, v200, v201
	v_add_f32_e32 v190, v198, v199
	v_pk_mul_f32 v[202:203], v[130:131], v[130:131]
	v_pk_mul_f32 v[204:205], v[134:135], v[134:135]
	v_add_f32_e32 v188, v190, v188
	v_add_f32_e32 v184, v184, v188
	v_add_f32_e32 v188, v204, v205
	v_add_f32_e32 v190, v202, v203
	v_add_f32_e32 v188, v190, v188
	v_add_f32_e32 v184, v184, v188
	v_mov_b32_e32 v188, 0
	v_cvt_f32_f16_e32 v140, v106
	v_add_f32_dpp v184, v184, v184 quad_perm:[1,0,3,2] row_mask:0xf bank_mask:0xf bound_ctrl:1
	v_cvt_f32_f16_sdwa v141, v106 dst_sel:DWORD dst_unused:UNUSED_PAD src0_sel:WORD_1
	v_cvt_f32_f16_e32 v144, v107
	v_add_f32_dpp v184, v184, v184 quad_perm:[2,3,0,1] row_mask:0xf bank_mask:0xf bound_ctrl:1
	v_cvt_f32_f16_sdwa v145, v107 dst_sel:DWORD dst_unused:UNUSED_PAD src0_sel:WORD_1
	v_pk_mul_f32 v[194:195], v[140:141], v[140:141]
	v_add_f32_dpp v184, v184, v184 row_half_mirror row_mask:0xf bank_mask:0xf bound_ctrl:1
	v_pk_mul_f32 v[190:191], v[136:137], v[136:137]
	v_pk_mul_f32 v[196:197], v[144:145], v[144:145]
	v_add_f32_dpp v184, v184, v184 row_mirror row_mask:0xf bank_mask:0xf bound_ctrl:1
	v_pk_mul_f32 v[192:193], v[138:139], v[138:139]
	v_add_f32_e32 v190, v190, v191
	v_mov_b32_dpp v188, v184 row_bcast:15 row_mask:0xa bank_mask:0xf
	v_add_f32_e32 v184, v184, v188
	v_mov_b32_e32 v188, 0
	s_waitcnt vmcnt(5)
	v_cvt_f32_f16_e32 v142, v104
	v_mov_b32_dpp v188, v184 row_bcast:31 row_mask:0xc bank_mask:0xf
	v_add_f32_e32 v184, v184, v188
	s_waitcnt vmcnt(3)
	ds_write2_b64 v226, v[114:115], v[116:117] offset0:148 offset1:214
	global_load_dwordx2 v[116:117], v[178:179], off offset:1024 nt
	v_cvt_f32_f16_e32 v152, v114
	v_cvt_f32_f16_sdwa v153, v114 dst_sel:DWORD dst_unused:UNUSED_PAD src0_sel:WORD_1
	v_cvt_f32_f16_e32 v156, v115
	v_cvt_f32_f16_sdwa v157, v115 dst_sel:DWORD dst_unused:UNUSED_PAD src0_sel:WORD_1
	global_load_dwordx2 v[114:115], v[178:179], off offset:1536 nt
	v_readlane_b32 s0, v184, 63
	v_cvt_f32_f16_sdwa v143, v104 dst_sel:DWORD dst_unused:UNUSED_PAD src0_sel:WORD_1
	v_cvt_f32_f16_e32 v148, v105
	v_fma_f32 v184, s0, v214, v213
	v_rsq_f32_e32 v184, v184
	v_cvt_f32_f16_sdwa v149, v105 dst_sel:DWORD dst_unused:UNUSED_PAD src0_sel:WORD_1
	v_cvt_f32_f16_e32 v146, v102
	v_cvt_f32_f16_sdwa v147, v102 dst_sel:DWORD dst_unused:UNUSED_PAD src0_sel:WORD_1
	v_cvt_f32_f16_e32 v150, v103
	v_cvt_f32_f16_sdwa v151, v103 dst_sel:DWORD dst_unused:UNUSED_PAD src0_sel:WORD_1
	v_cndmask_b32_e64 v210, v186, v184, s[8:9]
	v_add_f32_e32 v186, v196, v197
	v_add_f32_e32 v188, v194, v195
	v_add_f32_e32 v186, v188, v186
	v_add_f32_e32 v188, v192, v193
	v_pk_mul_f32 v[198:199], v[142:143], v[142:143]
	v_pk_mul_f32 v[200:201], v[148:149], v[148:149]
	v_add_f32_e32 v188, v190, v188
	v_add_f32_e32 v186, v188, v186
	v_add_f32_e32 v188, v200, v201
	v_add_f32_e32 v190, v198, v199
	v_pk_mul_f32 v[202:203], v[146:147], v[146:147]
	v_pk_mul_f32 v[204:205], v[150:151], v[150:151]
	v_add_f32_e32 v188, v190, v188
	v_add_f32_e32 v186, v186, v188
	v_add_f32_e32 v188, v204, v205
	v_add_f32_e32 v190, v202, v203
	v_add_f32_e32 v188, v190, v188
	v_add_f32_e32 v186, v186, v188
	v_mov_b32_e32 v188, 0
	s_waitcnt vmcnt(4)
; template <int R, bool RT = false>
; __device__ __forceinline__ void norm_phase(const NormArgs& a, LAS unsigned char* lds, bool ctx_rows, const float* ctx_src, const float* ctx_shift, const float* ctx_scale) {
;     ...
;             float rstd[R];
; #pragma unroll
;             for (int q = 0; q < R; ++q) { float ss = 0.f;
; #pragma unroll
;                 for (int j = 0; j < 4; ++j) ss += (v[q][j][0] * v[q][j][0] + v[q][j][1] * v[q][j][1]) + (v[q][j][2] * v[q][j][2] + v[q][j][3] * v[q][j][3]);
;                 rstd[q] = __builtin_amdgcn_rsqf(wave_sum(ss) * (1.f / DM) + EPS);
;                 if constexpr (RT) rsel[q] = ((lane >> 4) == rr / 4) ? rstd[q] : rsel[q]; }
; #pragma unroll
;             for (int q = 0; q < R; ++q) { const int row = row0 + rr + q;
; #pragma unroll
;                 for (int j = 0; j < 4; ++j) v[q][j] = (v[q][j] * rstd[q]) * A[j] + Sh[j];
	v_cvt_f32_f16_e32 v154, v112
	v_add_f32_dpp v186, v186, v186 quad_perm:[1,0,3,2] row_mask:0xf bank_mask:0xf bound_ctrl:1
	v_cvt_f32_f16_sdwa v155, v112 dst_sel:DWORD dst_unused:UNUSED_PAD src0_sel:WORD_1
	v_cvt_f32_f16_e32 v160, v113
	v_add_f32_dpp v186, v186, v186 quad_perm:[2,3,0,1] row_mask:0xf bank_mask:0xf bound_ctrl:1
	v_cvt_f32_f16_sdwa v161, v113 dst_sel:DWORD dst_unused:UNUSED_PAD src0_sel:WORD_1
	s_waitcnt vmcnt(3)
	v_cvt_f32_f16_e32 v158, v110
	v_add_f32_dpp v186, v186, v186 row_half_mirror row_mask:0xf bank_mask:0xf bound_ctrl:1
	v_cvt_f32_f16_sdwa v159, v110 dst_sel:DWORD dst_unused:UNUSED_PAD src0_sel:WORD_1
	v_cvt_f32_f16_e32 v164, v111
	v_add_f32_dpp v186, v186, v186 row_mirror row_mask:0xf bank_mask:0xf bound_ctrl:1
	v_cvt_f32_f16_sdwa v165, v111 dst_sel:DWORD dst_unused:UNUSED_PAD src0_sel:WORD_1
	v_pk_mul_f32 v[194:195], v[154:155], v[154:155]
	v_mov_b32_dpp v188, v186 row_bcast:15 row_mask:0xa bank_mask:0xf
	v_add_f32_e32 v186, v186, v188
	v_mov_b32_e32 v188, 0
	v_pk_mul_f32 v[196:197], v[160:161], v[160:161]
	s_waitcnt vmcnt(2)
	v_cvt_f32_f16_e32 v162, v108
	v_mov_b32_dpp v188, v186 row_bcast:31 row_mask:0xc bank_mask:0xf
	v_add_f32_e32 v186, v186, v188
	v_cvt_f32_f16_sdwa v163, v108 dst_sel:DWORD dst_unused:UNUSED_PAD src0_sel:WORD_1
	v_readlane_b32 s0, v186, 63
	v_cvt_f32_f16_e32 v166, v109
	v_cvt_f32_f16_sdwa v167, v109 dst_sel:DWORD dst_unused:UNUSED_PAD src0_sel:WORD_1
	v_fma_f32 v186, s0, v214, v213
	v_rsq_f32_e32 v186, v186
	v_pk_mul_f32 v[190:191], v[152:153], v[152:153]
	v_pk_mul_f32 v[192:193], v[156:157], v[156:157]
	v_add_f32_e32 v188, v194, v195
	v_cndmask_b32_e64 v212, v187, v186, s[8:9]
	v_add_f32_e32 v187, v196, v197
	v_add_f32_e32 v187, v188, v187
	v_add_f32_e32 v188, v192, v193
	v_add_f32_e32 v190, v190, v191
	v_pk_mul_f32 v[198:199], v[158:159], v[158:159]
	v_pk_mul_f32 v[200:201], v[164:165], v[164:165]
	v_add_f32_e32 v188, v190, v188
	v_add_f32_e32 v187, v188, v187
	v_add_f32_e32 v188, v200, v201
	v_add_f32_e32 v190, v198, v199
	v_pk_mul_f32 v[202:203], v[162:163], v[162:163]
	v_pk_mul_f32 v[204:205], v[166:167], v[166:167]
	v_add_f32_e32 v188, v190, v188
	v_add_f32_e32 v187, v187, v188
	v_add_f32_e32 v188, v204, v205
	v_add_f32_e32 v190, v202, v203
	v_add_f32_e32 v188, v190, v188
	v_add_f32_e32 v187, v187, v188
	v_mov_b32_e32 v188, 0
	v_cvt_f32_f16_e32 v172, v118
	v_add_f32_dpp v187, v187, v187 quad_perm:[1,0,3,2] row_mask:0xf bank_mask:0xf bound_ctrl:1
	v_cvt_f32_f16_sdwa v173, v118 dst_sel:DWORD dst_unused:UNUSED_PAD src0_sel:WORD_1
	v_cvt_f32_f16_e32 v176, v119
	v_add_f32_dpp v187, v187, v187 quad_perm:[2,3,0,1] row_mask:0xf bank_mask:0xf bound_ctrl:1
	v_cvt_f32_f16_sdwa v177, v119 dst_sel:DWORD dst_unused:UNUSED_PAD src0_sel:WORD_1
	s_waitcnt vmcnt(1)
	v_cvt_f32_f16_e32 v174, v116
	v_add_f32_dpp v187, v187, v187 row_half_mirror row_mask:0xf bank_mask:0xf bound_ctrl:1
	v_cvt_f32_f16_sdwa v175, v116 dst_sel:DWORD dst_unused:UNUSED_PAD src0_sel:WORD_1
	v_cvt_f32_f16_e32 v180, v117
	v_add_f32_dpp v187, v187, v187 row_mirror row_mask:0xf bank_mask:0xf bound_ctrl:1
	v_cvt_f32_f16_sdwa v181, v117 dst_sel:DWORD dst_unused:UNUSED_PAD src0_sel:WORD_1
	v_pk_mul_f32 v[190:191], v[168:169], v[168:169]
	v_mov_b32_dpp v188, v187 row_bcast:15 row_mask:0xa bank_mask:0xf
	v_add_f32_e32 v187, v187, v188
	v_mov_b32_e32 v188, 0
	v_pk_mul_f32 v[192:193], v[170:171], v[170:171]
	s_waitcnt vmcnt(0)
	v_cvt_f32_f16_e32 v178, v114
	v_mov_b32_dpp v188, v187 row_bcast:31 row_mask:0xc bank_mask:0xf
	v_add_f32_e32 v187, v187, v188
	v_cvt_f32_f16_sdwa v179, v114 dst_sel:DWORD dst_unused:UNUSED_PAD src0_sel:WORD_1
	v_readlane_b32 s0, v187, 63
	v_cvt_f32_f16_e32 v182, v115
	v_cvt_f32_f16_sdwa v183, v115 dst_sel:DWORD dst_unused:UNUSED_PAD src0_sel:WORD_1
	v_fma_f32 v187, s0, v214, v213
	v_rsq_f32_e32 v188, v187
	v_pk_mul_f32 v[194:195], v[172:173], v[172:173]
	v_pk_mul_f32 v[196:197], v[176:177], v[176:177]
	v_add_f32_e32 v187, v192, v193
	v_cndmask_b32_e64 v230, v189, v188, s[8:9]
	v_add_f32_e32 v189, v190, v191
	v_add_f32_e32 v187, v189, v187
	v_add_f32_e32 v189, v196, v197
	v_add_f32_e32 v190, v194, v195
	v_pk_mul_f32 v[198:199], v[174:175], v[174:175]
	v_pk_mul_f32 v[200:201], v[180:181], v[180:181]
	v_add_f32_e32 v189, v190, v189
	v_add_f32_e32 v187, v187, v189
	v_add_f32_e32 v189, v200, v201
	v_add_f32_e32 v190, v198, v199
	v_pk_mul_f32 v[202:203], v[178:179], v[178:179]
	v_pk_mul_f32 v[204:205], v[182:183], v[182:183]
	v_add_f32_e32 v189, v190, v189
	v_add_f32_e32 v187, v187, v189
	v_add_f32_e32 v189, v204, v205
	v_add_f32_e32 v190, v202, v203
	v_add_f32_e32 v189, v190, v189
	v_add_f32_e32 v187, v187, v189
	v_mov_b32_e32 v189, 0
	v_pk_mul_f32 v[120:121], v[120:121], v[184:185] op_sel_hi:[1,0]
	v_add_f32_dpp v187, v187, v187 quad_perm:[1,0,3,2] row_mask:0xf bank_mask:0xf bound_ctrl:1
	v_pk_mul_f32 v[124:125], v[124:125], v[184:185] op_sel_hi:[1,0]
	v_pk_fma_f32 v[120:121], v[36:37], v[120:121], v[2:3]
	v_add_f32_dpp v187, v187, v187 quad_perm:[2,3,0,1] row_mask:0xf bank_mask:0xf bound_ctrl:1
	v_pk_fma_f32 v[124:125], v[34:35], v[124:125], v[4:5]
	v_pk_mul_f32 v[122:123], v[122:123], v[184:185] op_sel_hi:[1,0]
	v_add_f32_dpp v187, v187, v187 row_half_mirror row_mask:0xf bank_mask:0xf bound_ctrl:1
	v_pk_mul_f32 v[128:129], v[128:129], v[184:185] op_sel_hi:[1,0]
	v_pk_fma_f32 v[122:123], v[42:43], v[122:123], v[6:7]
	v_add_f32_dpp v187, v187, v187 row_mirror row_mask:0xf bank_mask:0xf bound_ctrl:1
	v_pk_fma_f32 v[128:129], v[40:41], v[128:129], v[8:9]
	v_pk_mul_f32 v[126:127], v[126:127], v[184:185] op_sel_hi:[1,0]
	v_mov_b32_dpp v189, v187 row_bcast:15 row_mask:0xa bank_mask:0xf
	v_add_f32_e32 v187, v187, v189
; __device__ __forceinline__ unsigned pkb(float lo, float hi) { f32x2 v = {lo, hi}; bf16x2_t b = __builtin_convertvector(v, bf16x2_t); return __builtin_bit_cast(unsigned, b); }
; template <int R, bool RT = false>
; __device__ __forceinline__ void norm_phase(const NormArgs& a, LAS unsigned char* lds, bool ctx_rows, const float* ctx_src, const float* ctx_shift, const float* ctx_scale) {
;     ...
; #pragma unroll
;             for (int q = 0; q < R; ++q) { const int row = row0 + rr + q;
; #pragma unroll
;                 for (int j = 0; j < 4; ++j) v[q][j] = (v[q][j] * rstd[q]) * A[j] + Sh[j];
;                 if (a.fout) {
; #pragma unroll
;                     for (int j = 0; j < 4; ++j) *(f32x4*)(a.fout + (size_t)row * DM + 4 * lane + 256 * j) = v[q][j];
;                 }
;                 if (a.hout) {
; #pragma unroll
;                     for (int j = 0; j < 4; ++j) { u32x2 w; if (a.hbf) { w.x = pkb(v[q][j][0], v[q][j][1]); w.y = pkb(v[q][j][2], v[q][j][3]); } else { w.x = pkh(v[q][j][0], v[q][j][1]); w.y = pkh(v[q][j][2], v[q][j][3]); } *(u32x2*)(a.hout + (size_t)row * DM + 4 * lane + 256 * j) = w; }
;                 }
	v_mov_b32_e32 v189, 0
	v_pk_mul_f32 v[132:133], v[132:133], v[184:185] op_sel_hi:[1,0]
	v_cvt_pk_bf16_f32 v120, v120, v121
	v_mov_b32_dpp v189, v187 row_bcast:31 row_mask:0xc bank_mask:0xf
	v_cvt_pk_bf16_f32 v121, v124, v125
	v_lshl_add_u64 v[124:125], v[24:25], 0, s[24:25]
	v_add_f32_e32 v187, v187, v189
	v_pk_fma_f32 v[132:133], v[44:45], v[132:133], v[12:13]
	v_pk_fma_f32 v[126:127], v[46:47], v[126:127], v[10:11]
	v_pk_mul_f32 v[130:131], v[130:131], v[184:185] op_sel_hi:[1,0]
	v_pk_mul_f32 v[134:135], v[134:135], v[184:185] op_sel_hi:[1,0]
	global_store_dwordx2 v[124:125], v[120:121], off sc0 sc1
	v_cvt_pk_bf16_f32 v120, v122, v123
	v_cvt_pk_bf16_f32 v121, v128, v129
	v_readlane_b32 s0, v187, 63
	v_pk_fma_f32 v[134:135], v[52:53], v[134:135], v[16:17]
	v_pk_fma_f32 v[130:131], v[54:55], v[130:131], v[14:15]
	global_store_dwordx2 v[124:125], v[120:121], off offset:512 sc0 sc1
	v_cvt_pk_bf16_f32 v120, v126, v127
	v_cvt_pk_bf16_f32 v121, v132, v133
	v_fma_f32 v187, s0, v214, v213
	global_store_dwordx2 v[124:125], v[120:121], off offset:1024 sc0 sc1
	v_cvt_pk_bf16_f32 v120, v130, v131
	v_cvt_pk_bf16_f32 v121, v134, v135
	global_store_dwordx2 v[124:125], v[120:121], off offset:1536 sc0 sc1
	v_pk_mul_f32 v[120:121], v[136:137], v[186:187] op_sel_hi:[1,0]
	v_pk_mul_f32 v[122:123], v[138:139], v[186:187] op_sel_hi:[1,0]
	v_pk_fma_f32 v[120:121], v[36:37], v[120:121], v[2:3]
	v_pk_fma_f32 v[122:123], v[34:35], v[122:123], v[4:5]
	v_pk_mul_f32 v[124:125], v[140:141], v[186:187] op_sel_hi:[1,0]
	v_pk_mul_f32 v[126:127], v[144:145], v[186:187] op_sel_hi:[1,0]
	v_pk_fma_f32 v[124:125], v[42:43], v[124:125], v[6:7]
	v_pk_fma_f32 v[126:127], v[40:41], v[126:127], v[8:9]
	v_pk_mul_f32 v[128:129], v[142:143], v[186:187] op_sel_hi:[1,0]
	v_pk_mul_f32 v[130:131], v[148:149], v[186:187] op_sel_hi:[1,0]
	v_cvt_pk_bf16_f32 v120, v120, v121
	v_cvt_pk_bf16_f32 v121, v122, v123
	v_lshl_add_u64 v[122:123], v[24:25], 0, s[26:27]
	v_pk_fma_f32 v[130:131], v[44:45], v[130:131], v[12:13]
	v_pk_fma_f32 v[128:129], v[46:47], v[128:129], v[10:11]
	v_pk_mul_f32 v[132:133], v[146:147], v[186:187] op_sel_hi:[1,0]
	v_pk_mul_f32 v[134:135], v[150:151], v[186:187] op_sel_hi:[1,0]
	global_store_dwordx2 v[122:123], v[120:121], off sc0 sc1
	v_cvt_pk_bf16_f32 v120, v124, v125
	v_cvt_pk_bf16_f32 v121, v126, v127
	v_pk_fma_f32 v[134:135], v[52:53], v[134:135], v[16:17]
	v_pk_fma_f32 v[132:133], v[54:55], v[132:133], v[14:15]
	global_store_dwordx2 v[122:123], v[120:121], off offset:512 sc0 sc1
	v_cvt_pk_bf16_f32 v120, v128, v129
	v_cvt_pk_bf16_f32 v121, v130, v131
	global_store_dwordx2 v[122:123], v[120:121], off offset:1024 sc0 sc1
	v_cvt_pk_bf16_f32 v120, v132, v133
	v_cvt_pk_bf16_f32 v121, v134, v135
	global_store_dwordx2 v[122:123], v[120:121], off offset:1536 sc0 sc1
	v_pk_mul_f32 v[120:121], v[152:153], v[188:189] op_sel_hi:[1,0]
	v_pk_mul_f32 v[122:123], v[156:157], v[188:189] op_sel_hi:[1,0]
	v_pk_fma_f32 v[120:121], v[36:37], v[120:121], v[2:3]
	v_pk_fma_f32 v[122:123], v[34:35], v[122:123], v[4:5]
	v_pk_mul_f32 v[124:125], v[154:155], v[188:189] op_sel_hi:[1,0]
	v_pk_mul_f32 v[126:127], v[160:161], v[188:189] op_sel_hi:[1,0]
	v_rsq_f32_e32 v190, v187
	v_pk_fma_f32 v[126:127], v[40:41], v[126:127], v[8:9]
	v_pk_fma_f32 v[124:125], v[42:43], v[124:125], v[6:7]
	v_pk_mul_f32 v[128:129], v[158:159], v[188:189] op_sel_hi:[1,0]
	v_pk_mul_f32 v[130:131], v[164:165], v[188:189] op_sel_hi:[1,0]
	v_cvt_pk_bf16_f32 v120, v120, v121
	v_cvt_pk_bf16_f32 v121, v122, v123
	v_lshl_add_u64 v[122:123], v[24:25], 0, s[28:29]
	v_pk_fma_f32 v[130:131], v[44:45], v[130:131], v[12:13]
	v_pk_fma_f32 v[128:129], v[46:47], v[128:129], v[10:11]
	v_pk_mul_f32 v[132:133], v[162:163], v[188:189] op_sel_hi:[1,0]
	v_pk_mul_f32 v[134:135], v[166:167], v[188:189] op_sel_hi:[1,0]
	global_store_dwordx2 v[122:123], v[120:121], off sc0 sc1
	v_cvt_pk_bf16_f32 v120, v124, v125
	v_cvt_pk_bf16_f32 v121, v126, v127
	v_pk_fma_f32 v[134:135], v[52:53], v[134:135], v[16:17]
	v_pk_fma_f32 v[132:133], v[54:55], v[132:133], v[14:15]
	global_store_dwordx2 v[122:123], v[120:121], off offset:512 sc0 sc1
	v_cvt_pk_bf16_f32 v120, v128, v129
	v_cvt_pk_bf16_f32 v121, v130, v131
	global_store_dwordx2 v[122:123], v[120:121], off offset:1024 sc0 sc1
	v_cvt_pk_bf16_f32 v120, v132, v133
	v_cvt_pk_bf16_f32 v121, v134, v135
	global_store_dwordx2 v[122:123], v[120:121], off offset:1536 sc0 sc1
	v_pk_mul_f32 v[120:121], v[168:169], v[190:191] op_sel_hi:[1,0]
	v_pk_mul_f32 v[122:123], v[170:171], v[190:191] op_sel_hi:[1,0]
	v_pk_fma_f32 v[120:121], v[36:37], v[120:121], v[2:3]
	v_pk_fma_f32 v[122:123], v[34:35], v[122:123], v[4:5]
	v_pk_mul_f32 v[124:125], v[172:173], v[190:191] op_sel_hi:[1,0]
	v_pk_mul_f32 v[126:127], v[176:177], v[190:191] op_sel_hi:[1,0]
	v_pk_fma_f32 v[124:125], v[42:43], v[124:125], v[6:7]
	v_pk_fma_f32 v[126:127], v[40:41], v[126:127], v[8:9]
	v_pk_mul_f32 v[128:129], v[174:175], v[190:191] op_sel_hi:[1,0]
	v_pk_mul_f32 v[130:131], v[180:181], v[190:191] op_sel_hi:[1,0]
	v_cvt_pk_bf16_f32 v120, v120, v121
	v_cvt_pk_bf16_f32 v121, v122, v123
	v_lshl_add_u64 v[122:123], v[24:25], 0, s[30:31]
	v_pk_fma_f32 v[130:131], v[44:45], v[130:131], v[12:13]
	v_pk_fma_f32 v[128:129], v[46:47], v[128:129], v[10:11]
	v_pk_mul_f32 v[132:133], v[178:179], v[190:191] op_sel_hi:[1,0]
	v_pk_mul_f32 v[134:135], v[182:183], v[190:191] op_sel_hi:[1,0]
	global_store_dwordx2 v[122:123], v[120:121], off sc0 sc1
	v_cvt_pk_bf16_f32 v120, v124, v125
	v_cvt_pk_bf16_f32 v121, v126, v127
	v_pk_fma_f32 v[134:135], v[52:53], v[134:135], v[16:17]
	v_pk_fma_f32 v[132:133], v[54:55], v[132:133], v[14:15]
	global_store_dwordx2 v[122:123], v[120:121], off offset:512 sc0 sc1
	v_cvt_pk_bf16_f32 v120, v128, v129
	v_cvt_pk_bf16_f32 v121, v130, v131
	s_lshl_b64 s[24:25], s[2:3], 11
	s_add_i32 s2, s14, 13
	global_store_dwordx2 v[122:123], v[120:121], off offset:1024 sc0 sc1
	v_cvt_pk_bf16_f32 v120, v132, v133
	v_cvt_pk_bf16_f32 v121, v134, v135
	s_ashr_i32 s3, s2, 31
	global_store_dwordx2 v[122:123], v[120:121], off offset:1536 sc0 sc1
	s_lshl_b64 s[26:27], s[2:3], 11
	v_lshl_add_u64 v[120:121], v[22:23], 0, s[24:25]
	v_lshl_add_u64 v[132:133], v[22:23], 0, s[26:27]
	global_load_dwordx2 v[126:127], v[120:121], off nt
	global_load_dwordx2 v[124:125], v[120:121], off offset:512 nt
	global_load_dwordx2 v[122:123], v[120:121], off offset:1024 nt
	global_load_dwordx2 v[128:129], v[132:133], off nt
	s_add_i32 s2, s14, 14
	s_ashr_i32 s3, s2, 31
	s_lshl_b64 s[28:29], s[2:3], 11
	s_add_i32 s2, s14, 15
	s_ashr_i32 s3, s2, 31
	s_lshl_b64 s[30:31], s[2:3], 11
	v_lshl_add_u64 v[204:205], v[22:23], 0, s[30:31]
	global_load_dwordx2 v[130:131], v[132:133], off offset:512 nt
	global_load_dwordx2 v[188:189], v[204:205], off nt
	v_cndmask_b32_e64 v231, v185, v190, s[8:9]
	global_load_dwordx2 v[120:121], v[120:121], off offset:1536 nt
	s_waitcnt vmcnt(6)
; #define LAS __attribute__((address_space(3)))
; template <int R, bool RT = false>
; __device__ __forceinline__ void norm_phase(const NormArgs& a, LAS unsigned char* lds, bool ctx_rows, const float* ctx_src, const float* ctx_shift, const float* ctx_scale) {
;     ...
;             for (int q = 0; q < R; ++q) { const int row = row0 + rr + q;
;                 if (a.src16) { const f16* xr = a.src16 + (size_t)row * DM;
; #pragma unroll
;                     for (int j = 0; j < 4; ++j) { const f16x4 t = *(const f16x4*)(xr + 4 * lane + 256 * j); v[q][j] = (f32x4){(float)t[0], (float)t[1], (float)t[2], (float)t[3]};
;                         if constexpr (RT) { if (j == 0) *(LAS u32x2*)(hs + (rr + q) * 528 + 8 * lane) = __builtin_bit_cast(u32x2, t);
;                             else xp[rr / 4][q][j - 1] = __builtin_bit_cast(u32x2, t); } } }
;                 else { const float* xr = a.src + (size_t)row * DM;
; #pragma unroll
;                     for (int j = 0; j < 4; ++j) v[q][j] = *(const f32x4*)(xr + 4 * lane + 256 * j); } }
;             if (a.y2) {
;                 unsigned long long mask[R]; int ee[R][4]; float wgt[R][4]; f16x4 ld[R][4][4];
;                 int cnt[R];
; #pragma unroll
;                 for (int q = 0; q < R; ++q) { mask[q] = __ballot(sl[q] >= 0); cnt[q] = __builtin_popcountll(mask[q]);
; #pragma unroll
;                     for (int i = 0; i < 4; ++i) { if (mask[q]) { ee[q][i] = __builtin_ctzll(mask[q]); mask[q] &= mask[q] - 1; wgt[q][i] = 1.f; } else { ee[q][i] = i ? ee[q][0] : 0; wgt[q][i] = 0.f; } }
; #pragma unroll
;                     for (int i = 0; i < 4; ++i) {
;                         if (i < cnt[q]) { int slot = __shfl(sl[q], ee[q][i]); slot = slot < 0 ? 0 : slot; const f16* yr = a.y2 + ((size_t)ee[q][i] * EROWS + b * CAP + slot) * DM + 4 * lane;
; #pragma unroll
;                             for (int j = 0; j < 4; ++j) ld[q][i][j] = *(const f16x4*)(yr + 256 * j); } } }
; #pragma unroll
;                 for (int q = 0; q < R; ++q) { const int row = row0 + rr + q;
;                     f32x4 cs[4];
; #pragma unroll
;                     for (int j = 0; j < 4; ++j) cs[j] = (f32x4){0.f, 0.f, 0.f, 0.f};
; #pragma unroll
;                     for (int i = 0; i < 4; ++i) if (i < cnt[q]) {
; #pragma unroll
	v_cvt_f32_f16_e32 v134, v126
	v_cvt_f32_f16_sdwa v135, v126 dst_sel:DWORD dst_unused:UNUSED_PAD src0_sel:WORD_1
	v_cvt_f32_f16_e32 v138, v127
	v_cvt_f32_f16_sdwa v139, v127 dst_sel:DWORD dst_unused:UNUSED_PAD src0_sel:WORD_1
	s_waitcnt vmcnt(3)
	v_cvt_f32_f16_e32 v154, v128
	v_cvt_f32_f16_sdwa v155, v128 dst_sel:DWORD dst_unused:UNUSED_PAD src0_sel:WORD_1
	v_cvt_f32_f16_e32 v156, v129
	v_cvt_f32_f16_sdwa v157, v129 dst_sel:DWORD dst_unused:UNUSED_PAD src0_sel:WORD_1
	ds_write2_b64 v227, v[126:127], v[128:129] offset0:24 offset1:90
	global_load_dwordx2 v[128:129], v[132:133], off offset:1024 nt
	global_load_dwordx2 v[126:127], v[132:133], off offset:1536 nt
	v_lshl_add_u64 v[132:133], v[22:23], 0, s[28:29]
	global_load_dwordx2 v[186:187], v[132:133], off nt
	global_load_dwordx2 v[152:153], v[132:133], off offset:512 nt
	global_load_dwordx2 v[150:151], v[132:133], off offset:1024 nt
	s_waitcnt vmcnt(6)
	v_cvt_f32_f16_e32 v192, v188
	global_load_dwordx2 v[132:133], v[132:133], off offset:1536 nt
	v_cvt_f32_f16_sdwa v193, v188 dst_sel:DWORD dst_unused:UNUSED_PAD src0_sel:WORD_1
	v_cvt_f32_f16_e32 v194, v189
	v_cvt_f32_f16_sdwa v195, v189 dst_sel:DWORD dst_unused:UNUSED_PAD src0_sel:WORD_1
	global_load_dwordx2 v[190:191], v[204:205], off offset:1024 nt
	v_cvt_f32_f16_e32 v136, v124
	v_cvt_f32_f16_sdwa v137, v124 dst_sel:DWORD dst_unused:UNUSED_PAD src0_sel:WORD_1
	v_cvt_f32_f16_e32 v142, v125
	v_cvt_f32_f16_sdwa v143, v125 dst_sel:DWORD dst_unused:UNUSED_PAD src0_sel:WORD_1
	v_cvt_f32_f16_e32 v140, v122
	v_cvt_f32_f16_sdwa v141, v122 dst_sel:DWORD dst_unused:UNUSED_PAD src0_sel:WORD_1
	v_cvt_f32_f16_e32 v146, v123
	v_cvt_f32_f16_sdwa v147, v123 dst_sel:DWORD dst_unused:UNUSED_PAD src0_sel:WORD_1
	s_waitcnt vmcnt(7)
	v_cvt_f32_f16_e32 v144, v120
	v_cvt_f32_f16_sdwa v145, v120 dst_sel:DWORD dst_unused:UNUSED_PAD src0_sel:WORD_1
	v_cvt_f32_f16_e32 v148, v121
	v_cvt_f32_f16_sdwa v149, v121 dst_sel:DWORD dst_unused:UNUSED_PAD src0_sel:WORD_1
	v_pk_mul_f32 v[232:233], v[134:135], v[134:135]
	v_pk_mul_f32 v[234:235], v[138:139], v[138:139]
	v_pk_mul_f32 v[236:237], v[136:137], v[136:137]
	v_pk_mul_f32 v[238:239], v[142:143], v[142:143]
	v_add_f32_e32 v236, v236, v237
	v_add_f32_e32 v208, v238, v239
	v_add_f32_e32 v234, v234, v235
	v_add_f32_e32 v232, v232, v233
	v_pk_mul_f32 v[240:241], v[140:141], v[140:141]
	v_pk_mul_f32 v[242:243], v[146:147], v[146:147]
	v_add_f32_e32 v208, v236, v208
	v_add_f32_e32 v232, v232, v234
	v_add_f32_e32 v208, v232, v208
	v_add_f32_e32 v232, v242, v243
	v_add_f32_e32 v233, v240, v241
	v_pk_mul_f32 v[244:245], v[144:145], v[144:145]
	v_pk_mul_f32 v[246:247], v[148:149], v[148:149]
	v_add_f32_e32 v232, v233, v232
	v_add_f32_e32 v208, v208, v232
	v_add_f32_e32 v232, v246, v247
	v_add_f32_e32 v233, v244, v245
	v_add_f32_e32 v232, v233, v232
	v_add_f32_e32 v208, v208, v232
	v_mov_b32_e32 v232, 0
	v_cvt_f32_f16_e32 v158, v130
	v_add_f32_dpp v208, v208, v208 quad_perm:[1,0,3,2] row_mask:0xf bank_mask:0xf bound_ctrl:1
	v_cvt_f32_f16_sdwa v159, v130 dst_sel:DWORD dst_unused:UNUSED_PAD src0_sel:WORD_1
	v_cvt_f32_f16_e32 v162, v131
	v_add_f32_dpp v208, v208, v208 quad_perm:[2,3,0,1] row_mask:0xf bank_mask:0xf bound_ctrl:1
	v_cvt_f32_f16_sdwa v163, v131 dst_sel:DWORD dst_unused:UNUSED_PAD src0_sel:WORD_1
	v_pk_mul_f32 v[238:239], v[158:159], v[158:159]
	v_add_f32_dpp v208, v208, v208 row_half_mirror row_mask:0xf bank_mask:0xf bound_ctrl:1
	v_pk_mul_f32 v[234:235], v[154:155], v[154:155]
	v_pk_mul_f32 v[240:241], v[162:163], v[162:163]
	v_add_f32_dpp v208, v208, v208 row_mirror row_mask:0xf bank_mask:0xf bound_ctrl:1
	v_pk_mul_f32 v[236:237], v[156:157], v[156:157]
	v_add_f32_e32 v234, v234, v235
	v_mov_b32_dpp v232, v208 row_bcast:15 row_mask:0xa bank_mask:0xf
	v_add_f32_e32 v208, v208, v232
	v_mov_b32_e32 v232, 0
	s_waitcnt vmcnt(6)
	v_cvt_f32_f16_e32 v160, v128
	v_mov_b32_dpp v232, v208 row_bcast:31 row_mask:0xc bank_mask:0xf
	v_add_f32_e32 v208, v208, v232
	s_waitcnt vmcnt(4)
	ds_write2_b64 v227, v[186:187], v[188:189] offset0:156 offset1:222
	global_load_dwordx2 v[188:189], v[204:205], off offset:512 nt
	v_cvt_f32_f16_e32 v170, v186
	v_cvt_f32_f16_sdwa v171, v186 dst_sel:DWORD dst_unused:UNUSED_PAD src0_sel:WORD_1
	v_cvt_f32_f16_e32 v174, v187
	v_cvt_f32_f16_sdwa v175, v187 dst_sel:DWORD dst_unused:UNUSED_PAD src0_sel:WORD_1
	global_load_dwordx2 v[186:187], v[204:205], off offset:1536 nt
	v_readlane_b32 s0, v208, 63
	v_cvt_f32_f16_sdwa v161, v128 dst_sel:DWORD dst_unused:UNUSED_PAD src0_sel:WORD_1
	v_cvt_f32_f16_e32 v166, v129
	v_fma_f32 v208, s0, v214, v213
	v_rsq_f32_e32 v208, v208
	v_cvt_f32_f16_sdwa v167, v129 dst_sel:DWORD dst_unused:UNUSED_PAD src0_sel:WORD_1
	v_cvt_f32_f16_e32 v164, v126
	v_cvt_f32_f16_sdwa v165, v126 dst_sel:DWORD dst_unused:UNUSED_PAD src0_sel:WORD_1
	v_cvt_f32_f16_e32 v168, v127
	v_cvt_f32_f16_sdwa v169, v127 dst_sel:DWORD dst_unused:UNUSED_PAD src0_sel:WORD_1
	v_cndmask_b32_e64 v233, v210, v208, s[10:11]
	v_add_f32_e32 v210, v240, v241
	v_add_f32_e32 v232, v238, v239
	v_add_f32_e32 v210, v232, v210
	v_add_f32_e32 v232, v236, v237
	v_pk_mul_f32 v[242:243], v[160:161], v[160:161]
	v_pk_mul_f32 v[244:245], v[166:167], v[166:167]
	v_add_f32_e32 v232, v234, v232
	v_add_f32_e32 v210, v232, v210
	v_add_f32_e32 v232, v244, v245
	v_add_f32_e32 v234, v242, v243
	v_pk_mul_f32 v[246:247], v[164:165], v[164:165]
	v_pk_mul_f32 v[248:249], v[168:169], v[168:169]
	v_add_f32_e32 v232, v234, v232
	v_add_f32_e32 v210, v210, v232
	v_add_f32_e32 v232, v248, v249
	v_add_f32_e32 v234, v246, v247
	v_add_f32_e32 v232, v234, v232
	v_add_f32_e32 v210, v210, v232
	v_mov_b32_e32 v232, 0
	s_waitcnt vmcnt(5)
; __device__ __forceinline__ unsigned pkb(float lo, float hi) { f32x2 v = {lo, hi}; bf16x2_t b = __builtin_convertvector(v, bf16x2_t); return __builtin_bit_cast(unsigned, b); }
; template <int R, bool RT = false>
; __device__ __forceinline__ void norm_phase(const NormArgs& a, LAS unsigned char* lds, bool ctx_rows, const float* ctx_src, const float* ctx_shift, const float* ctx_scale) {
;     ...
;             float rstd[R];
; #pragma unroll
;             for (int q = 0; q < R; ++q) { float ss = 0.f;
; #pragma unroll
;                 for (int j = 0; j < 4; ++j) ss += (v[q][j][0] * v[q][j][0] + v[q][j][1] * v[q][j][1]) + (v[q][j][2] * v[q][j][2] + v[q][j][3] * v[q][j][3]);
;                 rstd[q] = __builtin_amdgcn_rsqf(wave_sum(ss) * (1.f / DM) + EPS);
;                 if constexpr (RT) rsel[q] = ((lane >> 4) == rr / 4) ? rstd[q] : rsel[q]; }
; #pragma unroll
;             for (int q = 0; q < R; ++q) { const int row = row0 + rr + q;
; #pragma unroll
;                 for (int j = 0; j < 4; ++j) v[q][j] = (v[q][j] * rstd[q]) * A[j] + Sh[j];
;                 if (a.fout) {
; #pragma unroll
;                     for (int j = 0; j < 4; ++j) *(f32x4*)(a.fout + (size_t)row * DM + 4 * lane + 256 * j) = v[q][j];
;                 }
;                 if (a.hout) {
; #pragma unroll
;                     for (int j = 0; j < 4; ++j) { u32x2 w; if (a.hbf) { w.x = pkb(v[q][j][0], v[q][j][1]); w.y = pkb(v[q][j][2], v[q][j][3]); } else { w.x = pkh(v[q][j][0], v[q][j][1]); w.y = pkh(v[q][j][2], v[q][j][3]); } *(u32x2*)(a.hout + (size_t)row * DM + 4 * lane + 256 * j) = w; }
;                 }
	v_cvt_f32_f16_e32 v172, v152
	v_add_f32_dpp v210, v210, v210 quad_perm:[1,0,3,2] row_mask:0xf bank_mask:0xf bound_ctrl:1
	v_cvt_f32_f16_sdwa v173, v152 dst_sel:DWORD dst_unused:UNUSED_PAD src0_sel:WORD_1
	v_cvt_f32_f16_e32 v178, v153
	v_add_f32_dpp v210, v210, v210 quad_perm:[2,3,0,1] row_mask:0xf bank_mask:0xf bound_ctrl:1
	v_cvt_f32_f16_sdwa v179, v153 dst_sel:DWORD dst_unused:UNUSED_PAD src0_sel:WORD_1
	s_waitcnt vmcnt(4)
	v_cvt_f32_f16_e32 v176, v150
	v_add_f32_dpp v210, v210, v210 row_half_mirror row_mask:0xf bank_mask:0xf bound_ctrl:1
	v_cvt_f32_f16_sdwa v177, v150 dst_sel:DWORD dst_unused:UNUSED_PAD src0_sel:WORD_1
	v_cvt_f32_f16_e32 v182, v151
	v_add_f32_dpp v210, v210, v210 row_mirror row_mask:0xf bank_mask:0xf bound_ctrl:1
	v_cvt_f32_f16_sdwa v183, v151 dst_sel:DWORD dst_unused:UNUSED_PAD src0_sel:WORD_1
	s_waitcnt vmcnt(3)
	v_cvt_f32_f16_e32 v180, v132
	v_mov_b32_dpp v232, v210 row_bcast:15 row_mask:0xa bank_mask:0xf
	v_add_f32_e32 v210, v210, v232
	v_mov_b32_e32 v232, 0
	v_cvt_f32_f16_sdwa v181, v132 dst_sel:DWORD dst_unused:UNUSED_PAD src0_sel:WORD_1
	v_cvt_f32_f16_e32 v184, v133
	v_mov_b32_dpp v232, v210 row_bcast:31 row_mask:0xc bank_mask:0xf
	v_add_f32_e32 v210, v210, v232
	v_cvt_f32_f16_sdwa v185, v133 dst_sel:DWORD dst_unused:UNUSED_PAD src0_sel:WORD_1
	v_readlane_b32 s0, v210, 63
	v_pk_mul_f32 v[234:235], v[170:171], v[170:171]
	v_pk_mul_f32 v[236:237], v[174:175], v[174:175]
	v_fma_f32 v210, s0, v214, v213
	v_rsq_f32_e32 v210, v210
	v_pk_mul_f32 v[238:239], v[172:173], v[172:173]
	v_pk_mul_f32 v[240:241], v[178:179], v[178:179]
	v_add_f32_e32 v238, v238, v239
	v_cndmask_b32_e64 v232, v212, v210, s[10:11]
	v_add_f32_e32 v212, v240, v241
	v_add_f32_e32 v236, v236, v237
	v_add_f32_e32 v234, v234, v235
	v_pk_mul_f32 v[242:243], v[176:177], v[176:177]
	v_pk_mul_f32 v[244:245], v[182:183], v[182:183]
	v_add_f32_e32 v212, v238, v212
	v_add_f32_e32 v234, v234, v236
	v_add_f32_e32 v212, v234, v212
	v_add_f32_e32 v234, v244, v245
	v_add_f32_e32 v235, v242, v243
	v_pk_mul_f32 v[246:247], v[180:181], v[180:181]
	v_pk_mul_f32 v[248:249], v[184:185], v[184:185]
	v_add_f32_e32 v234, v235, v234
	v_add_f32_e32 v212, v212, v234
	v_add_f32_e32 v234, v248, v249
	v_add_f32_e32 v235, v246, v247
	v_add_f32_e32 v234, v235, v234
	v_add_f32_e32 v212, v212, v234
	v_mov_b32_e32 v234, 0
	s_waitcnt vmcnt(1)
	v_cvt_f32_f16_e32 v196, v188
	v_add_f32_dpp v212, v212, v212 quad_perm:[1,0,3,2] row_mask:0xf bank_mask:0xf bound_ctrl:1
	v_cvt_f32_f16_sdwa v197, v188 dst_sel:DWORD dst_unused:UNUSED_PAD src0_sel:WORD_1
	v_cvt_f32_f16_e32 v198, v189
	v_add_f32_dpp v212, v212, v212 quad_perm:[2,3,0,1] row_mask:0xf bank_mask:0xf bound_ctrl:1
	v_cvt_f32_f16_sdwa v199, v189 dst_sel:DWORD dst_unused:UNUSED_PAD src0_sel:WORD_1
	v_cvt_f32_f16_e32 v200, v190
	v_add_f32_dpp v212, v212, v212 row_half_mirror row_mask:0xf bank_mask:0xf bound_ctrl:1
	v_cvt_f32_f16_sdwa v201, v190 dst_sel:DWORD dst_unused:UNUSED_PAD src0_sel:WORD_1
	v_cvt_f32_f16_e32 v202, v191
	v_add_f32_dpp v212, v212, v212 row_mirror row_mask:0xf bank_mask:0xf bound_ctrl:1
	v_cvt_f32_f16_sdwa v203, v191 dst_sel:DWORD dst_unused:UNUSED_PAD src0_sel:WORD_1
	v_pk_mul_f32 v[236:237], v[194:195], v[194:195]
	v_mov_b32_dpp v234, v212 row_bcast:15 row_mask:0xa bank_mask:0xf
	v_add_f32_e32 v212, v212, v234
	v_mov_b32_e32 v234, 0
	s_waitcnt vmcnt(0)
	v_cvt_f32_f16_e32 v204, v186
	v_cvt_f32_f16_sdwa v205, v186 dst_sel:DWORD dst_unused:UNUSED_PAD src0_sel:WORD_1
	v_mov_b32_dpp v234, v212 row_bcast:31 row_mask:0xc bank_mask:0xf
	v_add_f32_e32 v212, v212, v234
	v_pk_mul_f32 v[234:235], v[192:193], v[192:193]
	v_cvt_f32_f16_e32 v206, v187
	v_cvt_f32_f16_sdwa v207, v187 dst_sel:DWORD dst_unused:UNUSED_PAD src0_sel:WORD_1
	v_pk_mul_f32 v[238:239], v[196:197], v[196:197]
	v_pk_mul_f32 v[240:241], v[198:199], v[198:199]
	v_add_f32_e32 v236, v236, v237
	v_add_f32_e32 v234, v234, v235
	v_add_f32_e32 v234, v234, v236
	v_add_f32_e32 v235, v240, v241
	v_add_f32_e32 v236, v238, v239
	v_pk_mul_f32 v[242:243], v[200:201], v[200:201]
	v_pk_mul_f32 v[244:245], v[202:203], v[202:203]
	v_add_f32_e32 v235, v236, v235
	v_add_f32_e32 v234, v234, v235
	v_add_f32_e32 v235, v244, v245
	v_add_f32_e32 v236, v242, v243
	v_pk_mul_f32 v[246:247], v[204:205], v[204:205]
	v_pk_mul_f32 v[248:249], v[206:207], v[206:207]
	v_add_f32_e32 v235, v236, v235
	v_pk_mul_f32 v[134:135], v[134:135], v[208:209] op_sel_hi:[1,0]
	v_pk_mul_f32 v[138:139], v[138:139], v[208:209] op_sel_hi:[1,0]
	v_add_f32_e32 v234, v234, v235
	v_add_f32_e32 v235, v248, v249
	v_add_f32_e32 v236, v246, v247
	v_pk_fma_f32 v[138:139], v[34:35], v[138:139], v[4:5]
	v_pk_fma_f32 v[134:135], v[36:37], v[134:135], v[2:3]
	v_pk_mul_f32 v[136:137], v[136:137], v[208:209] op_sel_hi:[1,0]
	v_pk_mul_f32 v[142:143], v[142:143], v[208:209] op_sel_hi:[1,0]
	v_add_f32_e32 v235, v236, v235
	v_pk_fma_f32 v[142:143], v[40:41], v[142:143], v[8:9]
	v_pk_fma_f32 v[136:137], v[42:43], v[136:137], v[6:7]
	v_pk_mul_f32 v[140:141], v[140:141], v[208:209] op_sel_hi:[1,0]
	v_pk_mul_f32 v[146:147], v[146:147], v[208:209] op_sel_hi:[1,0]
	v_cvt_pk_bf16_f32 v134, v134, v135
	v_cvt_pk_bf16_f32 v135, v138, v139
	v_lshl_add_u64 v[138:139], v[24:25], 0, s[24:25]
	v_add_f32_e32 v234, v234, v235
	v_pk_fma_f32 v[146:147], v[44:45], v[146:147], v[12:13]
	v_pk_fma_f32 v[140:141], v[46:47], v[140:141], v[10:11]
	v_pk_mul_f32 v[144:145], v[144:145], v[208:209] op_sel_hi:[1,0]
	v_pk_mul_f32 v[148:149], v[148:149], v[208:209] op_sel_hi:[1,0]
	global_store_dwordx2 v[138:139], v[134:135], off sc0 sc1
	v_cvt_pk_bf16_f32 v134, v136, v137
	v_cvt_pk_bf16_f32 v135, v142, v143
	v_add_f32_dpp v234, v234, v234 quad_perm:[1,0,3,2] row_mask:0xf bank_mask:0xf bound_ctrl:1
; #define LAS __attribute__((address_space(3)))
; __device__ __forceinline__ unsigned pkb(float lo, float hi) { f32x2 v = {lo, hi}; bf16x2_t b = __builtin_convertvector(v, bf16x2_t); return __builtin_bit_cast(unsigned, b); }
; template <int R, bool RT = false>
; __device__ __forceinline__ void norm_phase(const NormArgs& a, LAS unsigned char* lds, bool ctx_rows, const float* ctx_src, const float* ctx_shift, const float* ctx_scale) {
;     ...
; #pragma unroll
;             for (int q = 0; q < R; ++q) { const int row = row0 + rr + q;
; #pragma unroll
;                 for (int j = 0; j < 4; ++j) v[q][j] = (v[q][j] * rstd[q]) * A[j] + Sh[j];
;                 if (a.fout) {
; #pragma unroll
;                     for (int j = 0; j < 4; ++j) *(f32x4*)(a.fout + (size_t)row * DM + 4 * lane + 256 * j) = v[q][j];
;                 }
;                 if (a.hout) {
; #pragma unroll
;                     for (int j = 0; j < 4; ++j) { u32x2 w; if (a.hbf) { w.x = pkb(v[q][j][0], v[q][j][1]); w.y = pkb(v[q][j][2], v[q][j][3]); } else { w.x = pkh(v[q][j][0], v[q][j][1]); w.y = pkh(v[q][j][2], v[q][j][3]); } *(u32x2*)(a.hout + (size_t)row * DM + 4 * lane + 256 * j) = w; }
;                 }
;     ...
;             const LAS unsigned char* ap = hs + i16 * 528 + 16 * c4; const LAS unsigned char* bp = lds + i16 * 2048;
;             const int xa = (c4 ^ i16) << 4;
;             f32x4 acc0 = {0.f, 0.f, 0.f, 0.f}, acc1 = acc0, acc2 = acc0, acc3 = acc0;
; #pragma unroll
;             for (int j = 0; j < 4; ++j) {
; #pragma unroll
;                 for (int g = 0; g < 4; ++g)
; #pragma unroll
;                     for (int q = 0; q < 4; ++q) { const int row = 4 * g + q; if (j > 0) *(LAS u32x2*)(hs + row * 528 + 8 * lane) = xp[g][q][j > 0 ? j - 1 : 0]; }
; #pragma unroll
;                 for (int s8 = 0; s8 < 8; ++s8) {
;                     if ((s8 & 3) == 0) asm volatile("" ::: "memory");
;                     const f16x8 Af = *(const LAS f16x8*)(ap + 64 * s8);
;                     const f16x8 Bh = *(const LAS f16x8*)(bp + ((512 * j + 64 * s8) ^ xa)), Bl = *(const LAS f16x8*)(bp + 32768 + ((512 * j + 64 * s8) ^ xa));
	v_pk_fma_f32 v[148:149], v[52:53], v[148:149], v[16:17]
	v_pk_fma_f32 v[144:145], v[54:55], v[144:145], v[14:15]
	global_store_dwordx2 v[138:139], v[134:135], off offset:512 sc0 sc1
	v_cvt_pk_bf16_f32 v134, v140, v141
	v_cvt_pk_bf16_f32 v135, v146, v147
	v_add_f32_dpp v234, v234, v234 quad_perm:[2,3,0,1] row_mask:0xf bank_mask:0xf bound_ctrl:1
	global_store_dwordx2 v[138:139], v[134:135], off offset:1024 sc0 sc1
	v_cvt_pk_bf16_f32 v134, v144, v145
	v_cvt_pk_bf16_f32 v135, v148, v149
	v_readlane_b32 s0, v212, 63
	v_add_f32_dpp v234, v234, v234 row_half_mirror row_mask:0xf bank_mask:0xf bound_ctrl:1
	global_store_dwordx2 v[138:139], v[134:135], off offset:1536 sc0 sc1
	v_pk_mul_f32 v[134:135], v[154:155], v[210:211] op_sel_hi:[1,0]
	v_pk_mul_f32 v[136:137], v[156:157], v[210:211] op_sel_hi:[1,0]
	v_fma_f32 v212, s0, v214, v213
	v_add_f32_dpp v234, v234, v234 row_mirror row_mask:0xf bank_mask:0xf bound_ctrl:1
	v_mov_b32_e32 v235, 0
	v_pk_fma_f32 v[136:137], v[34:35], v[136:137], v[4:5]
	v_pk_fma_f32 v[134:135], v[36:37], v[134:135], v[2:3]
	v_pk_mul_f32 v[138:139], v[158:159], v[210:211] op_sel_hi:[1,0]
	v_pk_mul_f32 v[140:141], v[162:163], v[210:211] op_sel_hi:[1,0]
	v_rsq_f32_e32 v212, v212
	v_mov_b32_dpp v235, v234 row_bcast:15 row_mask:0xa bank_mask:0xf
	v_pk_fma_f32 v[140:141], v[40:41], v[140:141], v[8:9]
	v_pk_fma_f32 v[138:139], v[42:43], v[138:139], v[6:7]
	v_pk_mul_f32 v[142:143], v[160:161], v[210:211] op_sel_hi:[1,0]
	v_pk_mul_f32 v[144:145], v[166:167], v[210:211] op_sel_hi:[1,0]
	v_cvt_pk_bf16_f32 v134, v134, v135
	v_cvt_pk_bf16_f32 v135, v136, v137
	v_lshl_add_u64 v[136:137], v[24:25], 0, s[26:27]
	v_add_f32_e32 v234, v234, v235
	v_mov_b32_e32 v235, 0
	v_pk_fma_f32 v[144:145], v[44:45], v[144:145], v[12:13]
	v_pk_fma_f32 v[142:143], v[46:47], v[142:143], v[10:11]
	v_pk_mul_f32 v[146:147], v[164:165], v[210:211] op_sel_hi:[1,0]
	v_pk_mul_f32 v[148:149], v[168:169], v[210:211] op_sel_hi:[1,0]
	global_store_dwordx2 v[136:137], v[134:135], off sc0 sc1
	v_cvt_pk_bf16_f32 v134, v138, v139
	v_cvt_pk_bf16_f32 v135, v140, v141
	v_mov_b32_dpp v235, v234 row_bcast:31 row_mask:0xc bank_mask:0xf
	v_pk_fma_f32 v[148:149], v[52:53], v[148:149], v[16:17]
	v_pk_fma_f32 v[146:147], v[54:55], v[146:147], v[14:15]
	global_store_dwordx2 v[136:137], v[134:135], off offset:512 sc0 sc1
	v_cvt_pk_bf16_f32 v134, v142, v143
	v_cvt_pk_bf16_f32 v135, v144, v145
	v_add_f32_e32 v234, v234, v235
	global_store_dwordx2 v[136:137], v[134:135], off offset:1024 sc0 sc1
	v_cvt_pk_bf16_f32 v134, v146, v147
	v_cvt_pk_bf16_f32 v135, v148, v149
	v_readlane_b32 s0, v234, 63
	global_store_dwordx2 v[136:137], v[134:135], off offset:1536 sc0 sc1
	v_pk_mul_f32 v[134:135], v[170:171], v[212:213] op_sel_hi:[1,0]
	v_pk_mul_f32 v[136:137], v[174:175], v[212:213] op_sel_hi:[1,0]
	v_fma_f32 v234, s0, v214, v213
	v_pk_fma_f32 v[136:137], v[34:35], v[136:137], v[4:5]
	v_pk_fma_f32 v[134:135], v[36:37], v[134:135], v[2:3]
	v_pk_mul_f32 v[138:139], v[172:173], v[212:213] op_sel_hi:[1,0]
	v_pk_mul_f32 v[140:141], v[178:179], v[212:213] op_sel_hi:[1,0]
	v_rsq_f32_e32 v234, v234
	v_pk_fma_f32 v[140:141], v[40:41], v[140:141], v[8:9]
	v_pk_fma_f32 v[138:139], v[42:43], v[138:139], v[6:7]
	v_pk_mul_f32 v[142:143], v[176:177], v[212:213] op_sel_hi:[1,0]
	v_pk_mul_f32 v[144:145], v[182:183], v[212:213] op_sel_hi:[1,0]
	v_cvt_pk_bf16_f32 v134, v134, v135
	v_cvt_pk_bf16_f32 v135, v136, v137
	v_lshl_add_u64 v[136:137], v[24:25], 0, s[28:29]
	v_pk_fma_f32 v[144:145], v[44:45], v[144:145], v[12:13]
	v_pk_fma_f32 v[142:143], v[46:47], v[142:143], v[10:11]
	v_pk_mul_f32 v[146:147], v[180:181], v[212:213] op_sel_hi:[1,0]
	v_pk_mul_f32 v[148:149], v[184:185], v[212:213] op_sel_hi:[1,0]
	global_store_dwordx2 v[136:137], v[134:135], off sc0 sc1
	v_cvt_pk_bf16_f32 v134, v138, v139
	v_cvt_pk_bf16_f32 v135, v140, v141
	v_pk_fma_f32 v[148:149], v[52:53], v[148:149], v[16:17]
	v_pk_fma_f32 v[146:147], v[54:55], v[146:147], v[14:15]
	global_store_dwordx2 v[136:137], v[134:135], off offset:512 sc0 sc1
	v_cvt_pk_bf16_f32 v134, v142, v143
	v_cvt_pk_bf16_f32 v135, v144, v145
	global_store_dwordx2 v[136:137], v[134:135], off offset:1024 sc0 sc1
	v_cvt_pk_bf16_f32 v134, v146, v147
	v_cvt_pk_bf16_f32 v135, v148, v149
	global_store_dwordx2 v[136:137], v[134:135], off offset:1536 sc0 sc1
	v_pk_mul_f32 v[134:135], v[192:193], v[234:235] op_sel_hi:[1,0]
	v_pk_mul_f32 v[136:137], v[194:195], v[234:235] op_sel_hi:[1,0]
	v_pk_fma_f32 v[2:3], v[36:37], v[134:135], v[2:3]
	v_pk_fma_f32 v[4:5], v[34:35], v[136:137], v[4:5]
	v_pk_mul_f32 v[34:35], v[196:197], v[234:235] op_sel_hi:[1,0]
	v_pk_mul_f32 v[36:37], v[198:199], v[234:235] op_sel_hi:[1,0]
	v_pk_fma_f32 v[6:7], v[42:43], v[34:35], v[6:7]
	v_pk_fma_f32 v[8:9], v[40:41], v[36:37], v[8:9]
	v_pk_mul_f32 v[34:35], v[200:201], v[234:235] op_sel_hi:[1,0]
	v_pk_mul_f32 v[36:37], v[202:203], v[234:235] op_sel_hi:[1,0]
	v_cvt_pk_bf16_f32 v2, v2, v3
	v_cvt_pk_bf16_f32 v3, v4, v5
	v_lshl_add_u64 v[4:5], v[24:25], 0, s[30:31]
	v_pk_fma_f32 v[12:13], v[44:45], v[36:37], v[12:13]
	v_pk_fma_f32 v[10:11], v[46:47], v[34:35], v[10:11]
	v_pk_mul_f32 v[34:35], v[204:205], v[234:235] op_sel_hi:[1,0]
	v_pk_mul_f32 v[36:37], v[206:207], v[234:235] op_sel_hi:[1,0]
	global_store_dwordx2 v[4:5], v[2:3], off sc0 sc1
	v_cvt_pk_bf16_f32 v2, v6, v7
	v_cvt_pk_bf16_f32 v3, v8, v9
	v_pk_fma_f32 v[16:17], v[52:53], v[36:37], v[16:17]
	v_pk_fma_f32 v[14:15], v[54:55], v[34:35], v[14:15]
	global_store_dwordx2 v[4:5], v[2:3], off offset:512 sc0 sc1
	v_cvt_pk_bf16_f32 v2, v10, v11
	v_cvt_pk_bf16_f32 v3, v12, v13
	global_store_dwordx2 v[4:5], v[2:3], off offset:1024 sc0 sc1
	v_cvt_pk_bf16_f32 v2, v14, v15
	v_cvt_pk_bf16_f32 v3, v16, v17
	global_store_dwordx2 v[4:5], v[2:3], off offset:1536 sc0 sc1
	ds_read_b128 v[2:5], v215 offset:32768
	ds_read_b128 v[6:9], v215
	ds_read_b128 v[10:13], v216
	s_waitcnt lgkmcnt(0)
; #define LAS __attribute__((address_space(3)))
; template <int R, bool RT = false>
; __device__ __forceinline__ void norm_phase(const NormArgs& a, LAS unsigned char* lds, bool ctx_rows, const float* ctx_src, const float* ctx_shift, const float* ctx_scale) {
;     ...
; #pragma unroll
;             for (int j = 0; j < 4; ++j) {
; #pragma unroll
;                 for (int g = 0; g < 4; ++g)
; #pragma unroll
;                     for (int q = 0; q < 4; ++q) { const int row = 4 * g + q; if (j > 0) *(LAS u32x2*)(hs + row * 528 + 8 * lane) = xp[g][q][j > 0 ? j - 1 : 0]; }
; #pragma unroll
;                 for (int s8 = 0; s8 < 8; ++s8) {
;                     if ((s8 & 3) == 0) asm volatile("" ::: "memory");
;                     const f16x8 Af = *(const LAS f16x8*)(ap + 64 * s8);
;                     const f16x8 Bh = *(const LAS f16x8*)(bp + ((512 * j + 64 * s8) ^ xa)), Bl = *(const LAS f16x8*)(bp + 32768 + ((512 * j + 64 * s8) ^ xa));
;                     if (s8 & 1) { acc1 = __builtin_amdgcn_mfma_f32_16x16x32_f16(Af, Bh, acc1, 0, 0, 0); acc3 = __builtin_amdgcn_mfma_f32_16x16x32_f16(Af, Bl, acc3, 0, 0, 0); }
;                     else        { acc0 = __builtin_amdgcn_mfma_f32_16x16x32_f16(Af, Bh, acc0, 0, 0, 0); acc2 = __builtin_amdgcn_mfma_f32_16x16x32_f16(Af, Bl, acc2, 0, 0, 0); } }
;             }
	v_mfma_f32_16x16x32_f16 v[6:9], v[10:13], v[6:9], 0
	v_cndmask_b32_e64 v230, v230, v212, s[10:11]
	v_cndmask_b32_e64 v231, v231, v234, s[10:11]
	s_and_b32 s0, s14, 0x7f0
	v_mfma_f32_16x16x32_f16 v[2:5], v[10:13], v[2:5], 0
	ds_read_b128 v[10:13], v216 offset:64
	ds_read_b128 v[14:17], v217 offset:32768
	ds_read_b128 v[34:37], v217
	s_lshl_b32 s0, s0, 2
	s_add_i32 s14, s14, 0x8000
	s_waitcnt lgkmcnt(0)
	v_mfma_f32_16x16x32_f16 v[34:37], v[10:13], v[34:37], 0
	v_mfma_f32_16x16x32_f16 v[10:13], v[10:13], v[14:17], 0
	ds_read_b128 v[14:17], v216 offset:128
	ds_read_b128 v[40:43], v218 offset:32768
	ds_read_b128 v[44:47], v218
	s_waitcnt lgkmcnt(0)
	v_mfma_f32_16x16x32_f16 v[6:9], v[14:17], v[44:47], v[6:9]
	v_mfma_f32_16x16x32_f16 v[2:5], v[14:17], v[40:43], v[2:5]
	ds_read_b128 v[14:17], v216 offset:192
	ds_read_b128 v[40:43], v219 offset:32768
	ds_read_b128 v[44:47], v219
	s_waitcnt lgkmcnt(0)
	v_mfma_f32_16x16x32_f16 v[34:37], v[14:17], v[44:47], v[34:37]
	v_mfma_f32_16x16x32_f16 v[10:13], v[14:17], v[40:43], v[10:13]
	ds_read_b128 v[14:17], v215 offset:33024
	ds_read_b128 v[40:43], v215 offset:256
	ds_read_b128 v[44:47], v216 offset:256
	s_waitcnt lgkmcnt(0)
	v_mfma_f32_16x16x32_f16 v[6:9], v[44:47], v[40:43], v[6:9]
	v_mfma_f32_16x16x32_f16 v[2:5], v[44:47], v[14:17], v[2:5]
	ds_read_b128 v[14:17], v216 offset:320
	ds_read_b128 v[40:43], v217 offset:33024
	ds_read_b128 v[44:47], v217 offset:256
	s_waitcnt lgkmcnt(0)
	v_mfma_f32_16x16x32_f16 v[34:37], v[14:17], v[44:47], v[34:37]
	v_mfma_f32_16x16x32_f16 v[10:13], v[14:17], v[40:43], v[10:13]
	ds_read_b128 v[14:17], v216 offset:384
	ds_read_b128 v[40:43], v218 offset:33024
	ds_read_b128 v[44:47], v218 offset:256
	s_waitcnt lgkmcnt(0)
	v_mfma_f32_16x16x32_f16 v[6:9], v[14:17], v[44:47], v[6:9]
	v_mfma_f32_16x16x32_f16 v[2:5], v[14:17], v[40:43], v[2:5]
	ds_read_b128 v[14:17], v216 offset:448
	ds_read_b128 v[40:43], v219 offset:33024
	ds_read_b128 v[44:47], v219 offset:256
	ds_write2_b64 v211, v[48:49], v[58:59] offset1:66
	ds_write2_b64 v211, v[64:65], v[70:71] offset0:132 offset1:198
	ds_write2_b64 v225, v[76:77], v[82:83] offset0:8 offset1:74
	ds_write2_b64 v225, v[88:89], v[94:95] offset0:140 offset1:206
	ds_write2_b64 v226, v[100:101], v[106:107] offset0:16 offset1:82
	ds_write2_b64 v226, v[112:113], v[118:119] offset0:148 offset1:214
	ds_write2_b64 v227, v[124:125], v[130:131] offset0:24 offset1:90
	ds_write2_b64 v227, v[152:153], v[188:189] offset0:156 offset1:222
	s_waitcnt lgkmcnt(8)
	v_mfma_f32_16x16x32_f16 v[34:37], v[14:17], v[44:47], v[34:37]
	v_mfma_f32_16x16x32_f16 v[10:13], v[14:17], v[40:43], v[10:13]
	ds_read_b128 v[14:17], v215 offset:33280
	ds_read_b128 v[40:43], v215 offset:512
	ds_read_b128 v[44:47], v216
	s_waitcnt lgkmcnt(0)
	v_mfma_f32_16x16x32_f16 v[6:9], v[44:47], v[40:43], v[6:9]
	v_mfma_f32_16x16x32_f16 v[2:5], v[44:47], v[14:17], v[2:5]
	ds_read_b128 v[14:17], v216 offset:64
	ds_read_b128 v[40:43], v217 offset:33280
	ds_read_b128 v[44:47], v217 offset:512
	s_waitcnt lgkmcnt(0)
	v_mfma_f32_16x16x32_f16 v[34:37], v[14:17], v[44:47], v[34:37]
	v_mfma_f32_16x16x32_f16 v[10:13], v[14:17], v[40:43], v[10:13]
	ds_read_b128 v[14:17], v216 offset:128
	ds_read_b128 v[40:43], v218 offset:33280
	ds_read_b128 v[44:47], v218 offset:512
	s_waitcnt lgkmcnt(0)
	v_mfma_f32_16x16x32_f16 v[6:9], v[14:17], v[44:47], v[6:9]
	v_mfma_f32_16x16x32_f16 v[2:5], v[14:17], v[40:43], v[2:5]
	ds_read_b128 v[14:17], v216 offset:192
	ds_read_b128 v[40:43], v219 offset:33280
	ds_read_b128 v[44:47], v219 offset:512
	s_waitcnt lgkmcnt(0)
	v_mfma_f32_16x16x32_f16 v[34:37], v[14:17], v[44:47], v[34:37]
	v_mfma_f32_16x16x32_f16 v[10:13], v[14:17], v[40:43], v[10:13]
	ds_read_b128 v[14:17], v215 offset:33536
	ds_read_b128 v[40:43], v215 offset:768
	ds_read_b128 v[44:47], v216 offset:256
	s_waitcnt lgkmcnt(0)
	v_mfma_f32_16x16x32_f16 v[6:9], v[44:47], v[40:43], v[6:9]
	v_mfma_f32_16x16x32_f16 v[2:5], v[44:47], v[14:17], v[2:5]
	ds_read_b128 v[14:17], v216 offset:320
	ds_read_b128 v[40:43], v217 offset:33536
	ds_read_b128 v[44:47], v217 offset:768
	s_waitcnt lgkmcnt(0)
	v_mfma_f32_16x16x32_f16 v[34:37], v[14:17], v[44:47], v[34:37]
	v_mfma_f32_16x16x32_f16 v[10:13], v[14:17], v[40:43], v[10:13]
	ds_read_b128 v[14:17], v216 offset:384
	ds_read_b128 v[40:43], v218 offset:33536
	ds_read_b128 v[44:47], v218 offset:768
	s_waitcnt lgkmcnt(0)
	v_mfma_f32_16x16x32_f16 v[6:9], v[14:17], v[44:47], v[6:9]
	v_mfma_f32_16x16x32_f16 v[2:5], v[14:17], v[40:43], v[2:5]
	ds_read_b128 v[14:17], v216 offset:448
	ds_read_b128 v[40:43], v219 offset:33536
	ds_read_b128 v[44:47], v219 offset:768
	ds_write2_b64 v211, v[38:39], v[56:57] offset1:66
	ds_write2_b64 v211, v[62:63], v[68:69] offset0:132 offset1:198
	ds_write2_b64 v225, v[74:75], v[80:81] offset0:8 offset1:74
	ds_write2_b64 v225, v[86:87], v[92:93] offset0:140 offset1:206
	ds_write2_b64 v226, v[98:99], v[104:105] offset0:16 offset1:82
	ds_write2_b64 v226, v[110:111], v[116:117] offset0:148 offset1:214
	ds_write2_b64 v227, v[122:123], v[128:129] offset0:24 offset1:90
	ds_write2_b64 v227, v[150:151], v[190:191] offset0:156 offset1:222
	s_waitcnt lgkmcnt(8)
	v_mfma_f32_16x16x32_f16 v[34:37], v[14:17], v[44:47], v[34:37]
	v_mfma_f32_16x16x32_f16 v[10:13], v[14:17], v[40:43], v[10:13]
	ds_read_b128 v[14:17], v215 offset:33792
	ds_read_b128 v[38:41], v215 offset:1024
	ds_read_b128 v[42:45], v216
	s_waitcnt lgkmcnt(0)
	v_mfma_f32_16x16x32_f16 v[6:9], v[42:45], v[38:41], v[6:9]
	v_mfma_f32_16x16x32_f16 v[2:5], v[42:45], v[14:17], v[2:5]
	ds_read_b128 v[14:17], v216 offset:64
	ds_read_b128 v[38:41], v217 offset:33792
	ds_read_b128 v[42:45], v217 offset:1024
	s_waitcnt lgkmcnt(0)
; #define LAS __attribute__((address_space(3)))
; template <int R, bool RT = false>
; __device__ __forceinline__ void norm_phase(const NormArgs& a, LAS unsigned char* lds, bool ctx_rows, const float* ctx_src, const float* ctx_shift, const float* ctx_scale) {
;     ...
;                     const f16x8 Af = *(const LAS f16x8*)(ap + 64 * s8);
;                     const f16x8 Bh = *(const LAS f16x8*)(bp + ((512 * j + 64 * s8) ^ xa)), Bl = *(const LAS f16x8*)(bp + 32768 + ((512 * j + 64 * s8) ^ xa));
;                     if (s8 & 1) { acc1 = __builtin_amdgcn_mfma_f32_16x16x32_f16(Af, Bh, acc1, 0, 0, 0); acc3 = __builtin_amdgcn_mfma_f32_16x16x32_f16(Af, Bl, acc3, 0, 0, 0); }
;                     else        { acc0 = __builtin_amdgcn_mfma_f32_16x16x32_f16(Af, Bh, acc0, 0, 0, 0); acc2 = __builtin_amdgcn_mfma_f32_16x16x32_f16(Af, Bl, acc2, 0, 0, 0); } }
;             }
;             const f32x4 d4 = (acc0 + acc1) + (acc2 + acc3);
;             f32x4 o4;
; #pragma unroll
;             for (int r = 0; r < 4; ++r) { const float lgt = rsel[r] * d4[r] + ce; float mx = lgt;
; #pragma unroll
;                 for (int o = 1; o < 16; o <<= 1) mx = fmaxf(mx, __shfl_xor(mx, o));
;                 const float ex = expf(lgt - mx); float sm = ex;
; #pragma unroll
;                 for (int o = 1; o < 16; o <<= 1) sm += __shfl_xor(sm, o);
;                 o4[r] = ex / sm; }
;             *(f32x4*)(a.aff + ((size_t)b * NE + i16) * SEQ + (row0 & (SEQ - 1)) + 4 * c4) = o4;
	v_mfma_f32_16x16x32_f16 v[34:37], v[14:17], v[42:45], v[34:37]
	v_mfma_f32_16x16x32_f16 v[10:13], v[14:17], v[38:41], v[10:13]
	ds_read_b128 v[14:17], v216 offset:128
	ds_read_b128 v[38:41], v218 offset:33792
	ds_read_b128 v[42:45], v218 offset:1024
	s_waitcnt lgkmcnt(0)
	v_mfma_f32_16x16x32_f16 v[6:9], v[14:17], v[42:45], v[6:9]
	v_mfma_f32_16x16x32_f16 v[2:5], v[14:17], v[38:41], v[2:5]
	ds_read_b128 v[14:17], v216 offset:192
	ds_read_b128 v[38:41], v219 offset:33792
	ds_read_b128 v[42:45], v219 offset:1024
	s_waitcnt lgkmcnt(0)
	v_mfma_f32_16x16x32_f16 v[34:37], v[14:17], v[42:45], v[34:37]
	v_mfma_f32_16x16x32_f16 v[10:13], v[14:17], v[38:41], v[10:13]
	ds_read_b128 v[14:17], v215 offset:34048
	ds_read_b128 v[38:41], v215 offset:1280
	ds_read_b128 v[42:45], v216 offset:256
	s_waitcnt lgkmcnt(0)
	v_mfma_f32_16x16x32_f16 v[6:9], v[42:45], v[38:41], v[6:9]
	v_mfma_f32_16x16x32_f16 v[2:5], v[42:45], v[14:17], v[2:5]
	ds_read_b128 v[14:17], v216 offset:320
	ds_read_b128 v[38:41], v217 offset:34048
	ds_read_b128 v[42:45], v217 offset:1280
	s_waitcnt lgkmcnt(0)
	v_mfma_f32_16x16x32_f16 v[34:37], v[14:17], v[42:45], v[34:37]
	v_mfma_f32_16x16x32_f16 v[10:13], v[14:17], v[38:41], v[10:13]
	ds_read_b128 v[14:17], v216 offset:384
	ds_read_b128 v[38:41], v218 offset:34048
	ds_read_b128 v[42:45], v218 offset:1280
	s_waitcnt lgkmcnt(0)
	v_mfma_f32_16x16x32_f16 v[6:9], v[14:17], v[42:45], v[6:9]
	v_mfma_f32_16x16x32_f16 v[2:5], v[14:17], v[38:41], v[2:5]
	ds_read_b128 v[14:17], v216 offset:448
	ds_read_b128 v[38:41], v219 offset:34048
	ds_read_b128 v[42:45], v219 offset:1280
	ds_write2_b64 v211, v[32:33], v[50:51] offset1:66
	ds_write2_b64 v211, v[60:61], v[66:67] offset0:132 offset1:198
	ds_write2_b64 v225, v[72:73], v[78:79] offset0:8 offset1:74
	ds_write2_b64 v225, v[84:85], v[90:91] offset0:140 offset1:206
	ds_write2_b64 v226, v[96:97], v[102:103] offset0:16 offset1:82
	ds_write2_b64 v226, v[108:109], v[114:115] offset0:148 offset1:214
	ds_write2_b64 v227, v[120:121], v[126:127] offset0:24 offset1:90
	ds_write2_b64 v227, v[132:133], v[186:187] offset0:156 offset1:222
	s_waitcnt lgkmcnt(8)
	v_mfma_f32_16x16x32_f16 v[34:37], v[14:17], v[42:45], v[34:37]
	v_mfma_f32_16x16x32_f16 v[10:13], v[14:17], v[38:41], v[10:13]
	ds_read_b128 v[14:17], v215 offset:34304
	ds_read_b128 v[38:41], v215 offset:1536
	ds_read_b128 v[42:45], v216
	s_waitcnt lgkmcnt(0)
	v_mfma_f32_16x16x32_f16 v[6:9], v[42:45], v[38:41], v[6:9]
	v_mfma_f32_16x16x32_f16 v[2:5], v[42:45], v[14:17], v[2:5]
	ds_read_b128 v[14:17], v216 offset:64
	ds_read_b128 v[38:41], v217 offset:34304
	ds_read_b128 v[42:45], v217 offset:1536
	s_waitcnt lgkmcnt(0)
	v_mfma_f32_16x16x32_f16 v[32:35], v[14:17], v[42:45], v[34:37]
	v_mfma_f32_16x16x32_f16 v[10:13], v[14:17], v[38:41], v[10:13]
	ds_read_b128 v[14:17], v216 offset:128
	s_nop 0
	ds_read_b128 v[36:39], v218 offset:34304
	ds_read_b128 v[40:43], v218 offset:1536
	s_waitcnt lgkmcnt(0)
	v_mfma_f32_16x16x32_f16 v[6:9], v[14:17], v[40:43], v[6:9]
	v_mfma_f32_16x16x32_f16 v[2:5], v[14:17], v[36:39], v[2:5]
	ds_read_b128 v[14:17], v216 offset:192
	ds_read_b128 v[36:39], v219 offset:34304
	ds_read_b128 v[40:43], v219 offset:1536
	s_waitcnt lgkmcnt(0)
	v_mfma_f32_16x16x32_f16 v[32:35], v[14:17], v[40:43], v[32:35]
	v_mfma_f32_16x16x32_f16 v[10:13], v[14:17], v[36:39], v[10:13]
	ds_read_b128 v[14:17], v215 offset:34560
	ds_read_b128 v[36:39], v215 offset:1792
	ds_read_b128 v[40:43], v216 offset:256
	s_waitcnt lgkmcnt(0)
	v_mfma_f32_16x16x32_f16 v[6:9], v[40:43], v[36:39], v[6:9]
	v_mfma_f32_16x16x32_f16 v[2:5], v[40:43], v[14:17], v[2:5]
	ds_read_b128 v[14:17], v216 offset:320
	ds_read_b128 v[36:39], v217 offset:34560
	ds_read_b128 v[40:43], v217 offset:1792
	s_waitcnt lgkmcnt(0)
	v_mfma_f32_16x16x32_f16 v[32:35], v[14:17], v[40:43], v[32:35]
	v_mfma_f32_16x16x32_f16 v[10:13], v[14:17], v[36:39], v[10:13]
	ds_read_b128 v[14:17], v216 offset:384
	ds_read_b128 v[36:39], v218 offset:34560
	ds_read_b128 v[40:43], v218 offset:1792
	s_waitcnt lgkmcnt(0)
	v_mfma_f32_16x16x32_f16 v[6:9], v[14:17], v[40:43], v[6:9]
	v_mfma_f32_16x16x32_f16 v[2:5], v[14:17], v[36:39], v[2:5]
	ds_read_b128 v[14:17], v216 offset:448
	ds_read_b128 v[36:39], v219 offset:34560
	ds_read_b128 v[40:43], v219 offset:1792
	s_waitcnt lgkmcnt(0)
	v_mfma_f32_16x16x32_f16 v[32:35], v[14:17], v[40:43], v[32:35]
	v_mfma_f32_16x16x32_f16 v[10:13], v[14:17], v[36:39], v[10:13]
	s_nop 6
	v_add_f32_e64 v8, v8, v34
	v_add_f32_e64 v9, v9, v35
	v_pk_add_f32 v[6:7], v[6:7], v[32:33]
	v_pk_add_f32 v[4:5], v[4:5], v[12:13]
	v_pk_add_f32 v[10:11], v[2:3], v[10:11]
	v_pk_add_f32 v[2:3], v[8:9], v[4:5]
	v_pk_add_f32 v[4:5], v[6:7], v[10:11]
	v_cndmask_b32_e32 v6, v220, v222, vcc
	v_fma_f32 v4, v233, v4, v1
	v_lshlrev_b32_e32 v12, 2, v6
	ds_bpermute_b32 v6, v12, v4
	v_cmp_lt_i32_e32 vcc, v223, v221
	v_fma_f32 v2, v230, v2, v1
	ds_bpermute_b32 v10, v12, v2
	v_cndmask_b32_e32 v7, v220, v223, vcc
	s_waitcnt lgkmcnt(1)
	v_max_f32_e32 v6, v6, v6
	v_max_f32_e32 v6, v4, v6
	v_lshlrev_b32_e32 v13, 2, v7
	ds_bpermute_b32 v7, v13, v6
	s_waitcnt lgkmcnt(1)
	v_max_f32_e32 v10, v10, v10
	v_cmp_lt_i32_e32 vcc, v224, v221
	v_max_f32_e32 v10, v2, v10
	ds_bpermute_b32 v11, v13, v10
	s_waitcnt lgkmcnt(1)
	v_max_f32_e32 v7, v7, v7
	v_max_f32_e32 v6, v6, v7
	v_cndmask_b32_e32 v7, v220, v224, vcc
	v_lshlrev_b32_e32 v14, 2, v7
	ds_bpermute_b32 v7, v14, v6
	s_waitcnt lgkmcnt(1)
	v_max_f32_e32 v11, v11, v11
	v_max_f32_e32 v10, v10, v11
	v_cmp_lt_i32_e32 vcc, v228, v221
	ds_bpermute_b32 v11, v14, v10
	s_waitcnt lgkmcnt(1)
; template <int R, bool RT = false>
; __device__ __forceinline__ void norm_phase(const NormArgs& a, LAS unsigned char* lds, bool ctx_rows, const float* ctx_src, const float* ctx_shift, const float* ctx_scale) {
;     ...
;             for (int r = 0; r < 4; ++r) { const float lgt = rsel[r] * d4[r] + ce; float mx = lgt;
; #pragma unroll
;                 for (int o = 1; o < 16; o <<= 1) mx = fmaxf(mx, __shfl_xor(mx, o));
;                 const float ex = expf(lgt - mx); float sm = ex;
; #pragma unroll
;                 for (int o = 1; o < 16; o <<= 1) sm += __shfl_xor(sm, o);
;                 o4[r] = ex / sm; }
;             *(f32x4*)(a.aff + ((size_t)b * NE + i16) * SEQ + (row0 & (SEQ - 1)) + 4 * c4) = o4;
	v_max_f32_e32 v7, v7, v7
	v_max_f32_e32 v6, v6, v7
	v_cndmask_b32_e32 v7, v220, v228, vcc
	v_lshlrev_b32_e32 v15, 2, v7
	ds_bpermute_b32 v7, v15, v6
	s_waitcnt lgkmcnt(1)
	v_max_f32_e32 v11, v11, v11
	v_max_f32_e32 v10, v10, v11
	ds_bpermute_b32 v11, v15, v10
	v_fma_f32 v5, v232, v5, v1
	s_waitcnt lgkmcnt(1)
	v_max_f32_e32 v7, v7, v7
	v_max_f32_e32 v6, v6, v7
	v_sub_f32_e32 v4, v4, v6
	v_mul_f32_e32 v6, 0x3fb8aa3b, v4
	v_fma_f32 v7, v4, s35, -v6
	v_rndne_f32_e32 v8, v6
	s_waitcnt lgkmcnt(0)
	v_max_f32_e32 v11, v11, v11
	v_fmac_f32_e32 v7, 0x32a5705f, v4
	v_sub_f32_e32 v6, v6, v8
	v_max_f32_e32 v10, v10, v11
	v_add_f32_e32 v6, v6, v7
	v_sub_f32_e32 v2, v2, v10
	v_exp_f32_e32 v6, v6
	v_cvt_i32_f32_e32 v7, v8
	v_mul_f32_e32 v10, 0x3fb8aa3b, v2
	v_fma_f32 v11, v2, s35, -v10
	v_rndne_f32_e32 v16, v10
	v_fmac_f32_e32 v11, 0x32a5705f, v2
	v_sub_f32_e32 v10, v10, v16
	v_add_f32_e32 v10, v10, v11
	v_ldexp_f32 v6, v6, v7
	ds_bpermute_b32 v7, v12, v5
	v_exp_f32_e32 v10, v10
	v_cvt_i32_f32_e32 v11, v16
	v_fma_f32 v3, v231, v3, v1
	v_cmp_ngt_f32_e32 vcc, s36, v4
	s_waitcnt lgkmcnt(0)
	v_max_f32_e32 v7, v7, v7
	v_ldexp_f32 v10, v10, v11
	ds_bpermute_b32 v11, v12, v3
	v_max_f32_e32 v7, v5, v7
	ds_bpermute_b32 v8, v13, v7
	v_cndmask_b32_e32 v6, 0, v6, vcc
	v_cmp_nlt_f32_e32 vcc, s37, v4
	s_waitcnt lgkmcnt(1)
	v_max_f32_e32 v11, v11, v11
	v_max_f32_e32 v11, v3, v11
	ds_bpermute_b32 v16, v13, v11
	s_waitcnt lgkmcnt(1)
	v_max_f32_e32 v8, v8, v8
	v_max_f32_e32 v7, v7, v8
	ds_bpermute_b32 v8, v14, v7
	v_cndmask_b32_e32 v4, v229, v6, vcc
	s_waitcnt lgkmcnt(1)
	v_max_f32_e32 v16, v16, v16
	v_max_f32_e32 v11, v11, v16
	ds_bpermute_b32 v16, v14, v11
	s_waitcnt lgkmcnt(1)
	v_max_f32_e32 v8, v8, v8
	v_max_f32_e32 v7, v7, v8
	ds_bpermute_b32 v8, v15, v7
	ds_bpermute_b32 v6, v12, v4
	s_waitcnt lgkmcnt(2)
	v_max_f32_e32 v16, v16, v16
	v_max_f32_e32 v11, v11, v16
	ds_bpermute_b32 v16, v15, v11
	s_waitcnt lgkmcnt(2)
	v_max_f32_e32 v8, v8, v8
	v_max_f32_e32 v7, v7, v8
	v_sub_f32_e32 v5, v5, v7
	v_mul_f32_e32 v7, 0x3fb8aa3b, v5
	v_fma_f32 v8, v5, s35, -v7
	v_rndne_f32_e32 v9, v7
	s_waitcnt lgkmcnt(0)
	v_max_f32_e32 v16, v16, v16
	v_fmac_f32_e32 v8, 0x32a5705f, v5
	v_sub_f32_e32 v7, v7, v9
	v_max_f32_e32 v11, v11, v16
	v_add_f32_e32 v7, v7, v8
	v_sub_f32_e32 v3, v3, v11
	v_exp_f32_e32 v7, v7
	v_cvt_i32_f32_e32 v8, v9
	v_mul_f32_e32 v11, 0x3fb8aa3b, v3
	v_fma_f32 v16, v3, s35, -v11
	v_rndne_f32_e32 v17, v11
	v_fmac_f32_e32 v16, 0x32a5705f, v3
	v_sub_f32_e32 v11, v11, v17
	v_add_f32_e32 v11, v11, v16
	v_ldexp_f32 v7, v7, v8
	v_cmp_ngt_f32_e32 vcc, s36, v5
	v_exp_f32_e32 v11, v11
	v_cvt_i32_f32_e32 v16, v17
	v_cndmask_b32_e32 v7, 0, v7, vcc
	v_cmp_nlt_f32_e32 vcc, s37, v5
	v_ldexp_f32 v11, v11, v16
	s_nop 0
	v_cndmask_b32_e32 v5, v229, v7, vcc
	v_cmp_ngt_f32_e32 vcc, s36, v2
	ds_bpermute_b32 v7, v12, v5
	s_waitcnt lgkmcnt(0)
	v_pk_add_f32 v[6:7], v[4:5], v[6:7]
	v_cndmask_b32_e32 v10, 0, v10, vcc
	v_cmp_nlt_f32_e32 vcc, s37, v2
	ds_bpermute_b32 v8, v13, v6
	ds_bpermute_b32 v9, v13, v7
	v_cndmask_b32_e32 v10, v229, v10, vcc
	v_cmp_ngt_f32_e32 vcc, s36, v3
	ds_bpermute_b32 v2, v12, v10
	s_waitcnt lgkmcnt(1)
	v_pk_add_f32 v[6:7], v[6:7], v[8:9]
	v_cndmask_b32_e32 v11, 0, v11, vcc
	v_cmp_nlt_f32_e32 vcc, s37, v3
	ds_bpermute_b32 v8, v14, v6
	ds_bpermute_b32 v9, v14, v7
	v_cndmask_b32_e32 v11, v229, v11, vcc
	ds_bpermute_b32 v3, v12, v11
	s_waitcnt lgkmcnt(1)
	v_pk_add_f32 v[6:7], v[6:7], v[8:9]
	ds_bpermute_b32 v8, v15, v6
	s_waitcnt lgkmcnt(1)
	v_pk_add_f32 v[2:3], v[10:11], v[2:3]
	ds_bpermute_b32 v12, v13, v2
	ds_bpermute_b32 v13, v13, v3
	ds_bpermute_b32 v9, v15, v7
	s_waitcnt lgkmcnt(1)
	v_pk_add_f32 v[2:3], v[2:3], v[12:13]
	ds_bpermute_b32 v12, v14, v2
	ds_bpermute_b32 v13, v14, v3
	s_waitcnt lgkmcnt(0)
	v_pk_add_f32 v[2:3], v[2:3], v[12:13]
	ds_bpermute_b32 v12, v15, v2
	ds_bpermute_b32 v13, v15, v3
	s_waitcnt lgkmcnt(0)
	v_pk_add_f32 v[12:13], v[2:3], v[12:13]
	v_pk_add_f32 v[2:3], v[6:7], v[8:9]
	s_nop 0
	v_div_scale_f32 v6, s[2:3], v3, v3, v5
	v_rcp_f32_e32 v7, v6
	s_nop 0
	v_fma_f32 v8, -v6, v7, 1.0
	v_fmac_f32_e32 v7, v8, v7
	v_div_scale_f32 v8, vcc, v5, v3, v5
	v_mul_f32_e32 v9, v8, v7
	v_fma_f32 v14, -v6, v9, v8
	v_fmac_f32_e32 v9, v14, v7
	v_fma_f32 v6, -v6, v9, v8
	v_div_fmas_f32 v6, v6, v7, v9
	v_div_fixup_f32 v3, v6, v3, v5
	v_div_scale_f32 v5, s[2:3], v2, v2, v4
	v_rcp_f32_e32 v6, v5
	s_nop 0
	v_fma_f32 v7, -v5, v6, 1.0
	v_fmac_f32_e32 v6, v7, v6
	v_div_scale_f32 v7, vcc, v4, v2, v4
	v_mul_f32_e32 v8, v7, v6
	v_fma_f32 v9, -v5, v8, v7
	v_fmac_f32_e32 v8, v9, v6
	v_fma_f32 v5, -v5, v8, v7
	v_div_fmas_f32 v5, v5, v6, v8
	v_div_fixup_f32 v2, v5, v2, v4
	v_div_scale_f32 v4, s[2:3], v13, v13, v11
	v_rcp_f32_e32 v5, v4
	s_nop 0
	v_fma_f32 v6, -v4, v5, 1.0
	v_fmac_f32_e32 v5, v6, v5
	v_div_scale_f32 v6, vcc, v11, v13, v11
	v_mul_f32_e32 v7, v6, v5
	v_fma_f32 v8, -v4, v7, v6
	v_fmac_f32_e32 v7, v8, v5
	v_fma_f32 v4, -v4, v7, v6
	v_div_fmas_f32 v4, v4, v5, v7
	v_div_fixup_f32 v5, v4, v13, v11
	v_div_scale_f32 v4, s[2:3], v12, v12, v10
	v_rcp_f32_e32 v6, v4
	s_lshl_b64 s[2:3], s[22:23], 17
	v_fma_f32 v7, -v4, v6, 1.0
	v_fmac_f32_e32 v6, v7, v6
	v_div_scale_f32 v7, vcc, v10, v12, v10
	v_mul_f32_e32 v8, v7, v6
	v_fma_f32 v9, -v4, v8, v7
	v_fmac_f32_e32 v8, v9, v6
	v_fma_f32 v4, -v4, v8, v7
	v_div_fmas_f32 v4, v4, v6, v8
	v_lshl_add_u64 v[6:7], v[26:27], 0, s[2:3]
	v_lshl_add_u64 v[6:7], v[6:7], 0, s[0:1]
	s_add_i32 s0, s34, 0x800
	v_div_fixup_f32 v4, v4, v12, v10
	v_lshl_add_u64 v[6:7], v[6:7], 0, v[18:19]
	s_cmp_lt_i32 s34, 0
	s_mov_b32 s34, s0
	global_store_dwordx4 v[6:7], v[2:5], off
	s_cbranch_scc1 .LBB0_808

; template <int R, bool RT = false>
; __device__ __forceinline__ void norm_phase(const NormArgs& a, LAS unsigned char* lds, bool ctx_rows, const float* ctx_src, const float* ctx_shift, const float* ctx_scale) {
;     ...
;         for (int rr = 0; rr < 16; rr += R) {
;             if constexpr (RT) asm volatile("" ::: "memory");
;             f32x4 v[R][4];
;             int sl[R];
; #pragma unroll
;             for (int q = 0; q < R; ++q) { sl[q] = -1; if (a.y2) { const int r = rr + q; const int pk = r < 4 ? ipk[0] : (r < 8 ? ipk[1] : (r < 12 ? ipk[2] : ipk[3]));
;                     const int got = __shfl(pk, (lane & 15) + 16 * (r & 3)); sl[q] = lane < 16 ? got : -1; } }
; #pragma unroll
;             for (int q = 0; q < R; ++q) { const int row = row0 + rr + q;
;                 if (a.src16) { const f16* xr = a.src16 + (size_t)row * DM;
; #pragma unroll
;                     for (int j = 0; j < 4; ++j) { const f16x4 t = *(const f16x4*)(xr + 4 * lane + 256 * j); v[q][j] = (f32x4){(float)t[0], (float)t[1], (float)t[2], (float)t[3]};
;                         if constexpr (RT) { if (j == 0) *(LAS u32x2*)(hs + (rr + q) * 528 + 8 * lane) = __builtin_bit_cast(u32x2, t);
;                             else xp[rr / 4][q][j - 1] = __builtin_bit_cast(u32x2, t); } } }
;                 else { const float* xr = a.src + (size_t)row * DM;
; #pragma unroll
;                     for (int j = 0; j < 4; ++j) v[q][j] = *(const f32x4*)(xr + 4 * lane + 256 * j); } }
;             if (a.y2) {
;                 unsigned long long mask[R]; int ee[R][4]; float wgt[R][4]; f16x4 ld[R][4][4];
;                 int cnt[R];
; #pragma unroll
;                 for (int q = 0; q < R; ++q) { mask[q] = __ballot(sl[q] >= 0); cnt[q] = __builtin_popcountll(mask[q]);
; #pragma unroll
;                     for (int i = 0; i < 4; ++i) { if (mask[q]) { ee[q][i] = __builtin_ctzll(mask[q]); mask[q] &= mask[q] - 1; wgt[q][i] = 1.f; } else { ee[q][i] = i ? ee[q][0] : 0; wgt[q][i] = 0.f; } }
; #pragma unroll
;                     for (int i = 0; i < 4; ++i) {
;                         if (i < cnt[q]) { int slot = __shfl(sl[q], ee[q][i]); slot = slot < 0 ? 0 : slot; const f16* yr = a.y2 + ((size_t)ee[q][i] * EROWS + b * CAP + slot) * DM + 4 * lane;
; #pragma unroll
;                             for (int j = 0; j < 4; ++j) ld[q][i][j] = *(const f16x4*)(yr + 256 * j); } } }
; #pragma unroll
.LBB0_831:
	s_or_b32 s20, s30, s29
	s_ashr_i32 s21, s20, 31
	s_lshl_b64 s[0:1], s[20:21], 11
	v_lshl_add_u64 v[18:19], v[100:101], 0, s[0:1]
	global_load_dwordx2 v[20:21], v[18:19], off nt
	global_load_dwordx2 v[24:25], v[18:19], off offset:512 nt
	global_load_dwordx2 v[28:29], v[18:19], off offset:1024 nt
	global_load_dwordx2 v[32:33], v[18:19], off offset:1536 nt
	s_or_b32 s2, s20, 1
	s_ashr_i32 s3, s2, 31
	s_lshl_b64 s[2:3], s[2:3], 11
	v_lshl_add_u64 v[18:19], v[100:101], 0, s[2:3]
	global_load_dwordx2 v[36:37], v[18:19], off nt
	global_load_dwordx2 v[40:41], v[18:19], off offset:512 nt
	global_load_dwordx2 v[44:45], v[18:19], off offset:1024 nt
	global_load_dwordx2 v[48:49], v[18:19], off offset:1536 nt
	s_or_b32 s18, s20, 2
	s_ashr_i32 s19, s18, 31
	s_lshl_b64 s[18:19], s[18:19], 11
	v_lshl_add_u64 v[18:19], v[100:101], 0, s[18:19]
	global_load_dwordx2 v[52:53], v[18:19], off nt
	global_load_dwordx2 v[56:57], v[18:19], off offset:512 nt
	global_load_dwordx2 v[60:61], v[18:19], off offset:1024 nt
	global_load_dwordx2 v[64:65], v[18:19], off offset:1536 nt
	s_or_b32 s20, s20, 3
	s_ashr_i32 s21, s20, 31
	s_lshl_b64 s[20:21], s[20:21], 11
	v_lshl_add_u64 v[18:19], v[100:101], 0, s[20:21]
	global_load_dwordx2 v[68:69], v[18:19], off nt
	global_load_dwordx2 v[72:73], v[18:19], off offset:512 nt
	global_load_dwordx2 v[76:77], v[18:19], off offset:1024 nt
	global_load_dwordx2 v[80:81], v[18:19], off offset:1536 nt
	s_and_b64 vcc, exec, s[4:5]
	s_waitcnt vmcnt(15)
	v_cvt_f32_f16_e32 v18, v20
	v_cvt_f32_f16_sdwa v19, v20 dst_sel:DWORD dst_unused:UNUSED_PAD src0_sel:WORD_1
	v_cvt_f32_f16_e32 v20, v21
	v_cvt_f32_f16_sdwa v21, v21 dst_sel:DWORD dst_unused:UNUSED_PAD src0_sel:WORD_1
	s_waitcnt vmcnt(14)
	v_cvt_f32_f16_e32 v22, v24
	v_cvt_f32_f16_sdwa v23, v24 dst_sel:DWORD dst_unused:UNUSED_PAD src0_sel:WORD_1
	v_cvt_f32_f16_e32 v24, v25
	v_cvt_f32_f16_sdwa v25, v25 dst_sel:DWORD dst_unused:UNUSED_PAD src0_sel:WORD_1
	s_waitcnt vmcnt(13)
	v_cvt_f32_f16_e32 v26, v28
	v_cvt_f32_f16_sdwa v27, v28 dst_sel:DWORD dst_unused:UNUSED_PAD src0_sel:WORD_1
	v_cvt_f32_f16_e32 v28, v29
	v_cvt_f32_f16_sdwa v29, v29 dst_sel:DWORD dst_unused:UNUSED_PAD src0_sel:WORD_1
	s_waitcnt vmcnt(12)
	v_cvt_f32_f16_e32 v30, v32
	v_cvt_f32_f16_sdwa v31, v32 dst_sel:DWORD dst_unused:UNUSED_PAD src0_sel:WORD_1
	v_cvt_f32_f16_e32 v32, v33
	v_cvt_f32_f16_sdwa v33, v33 dst_sel:DWORD dst_unused:UNUSED_PAD src0_sel:WORD_1
	s_waitcnt lgkmcnt(0)
	v_mov_b32_e32 v84, v19
	v_mov_b32_e32 v85, v21
	v_mov_b32_e32 v82, v18
	v_mov_b32_e32 v83, v20
	v_pk_mul_f32 v[84:85], v[84:85], v[84:85]
	v_mov_b32_e32 v86, v23
	v_mov_b32_e32 v87, v25
	v_pk_fma_f32 v[82:83], v[82:83], v[82:83], v[84:85]
	v_mov_b32_e32 v84, v22
	v_mov_b32_e32 v85, v24
	v_pk_mul_f32 v[86:87], v[86:87], v[86:87]
	v_mul_f32_e32 v88, v29, v29
	v_pk_fma_f32 v[84:85], v[84:85], v[84:85], v[86:87]
	v_mul_f32_e32 v86, v27, v27
	s_waitcnt vmcnt(11)
	v_cvt_f32_f16_e32 v34, v36
	v_cvt_f32_f16_sdwa v35, v36 dst_sel:DWORD dst_unused:UNUSED_PAD src0_sel:WORD_1
	v_cvt_f32_f16_e32 v36, v37
	v_cvt_f32_f16_sdwa v37, v37 dst_sel:DWORD dst_unused:UNUSED_PAD src0_sel:WORD_1
	v_pk_add_f32 v[82:83], v[82:83], v[82:83] op_sel:[0,1] op_sel_hi:[1,0]
	v_pk_add_f32 v[84:85], v[84:85], v[84:85] op_sel:[0,1] op_sel_hi:[1,0]
	v_pk_fma_f32 v[86:87], v[26:27], v[26:27], v[86:87] op_sel_hi:[1,1,0]
	v_pk_fma_f32 v[88:89], v[28:29], v[28:29], v[88:89] op_sel_hi:[1,1,0]
	v_pk_mul_f32 v[90:91], v[30:31], v[30:31]
	v_pk_mul_f32 v[92:93], v[32:33], v[32:33]
	s_waitcnt vmcnt(10)
	v_cvt_f32_f16_e32 v38, v40
	v_cvt_f32_f16_sdwa v39, v40 dst_sel:DWORD dst_unused:UNUSED_PAD src0_sel:WORD_1
	v_cvt_f32_f16_e32 v40, v41
	v_cvt_f32_f16_sdwa v41, v41 dst_sel:DWORD dst_unused:UNUSED_PAD src0_sel:WORD_1
	v_mov_b32_e32 v83, v90
	v_mov_b32_e32 v85, v91
	v_mov_b32_e32 v87, v92
	v_mov_b32_e32 v89, v93
	v_pk_add_f32 v[82:83], v[82:83], v[84:85]
	v_pk_add_f32 v[84:85], v[86:87], v[88:89]
	s_waitcnt vmcnt(9)
	v_cvt_f32_f16_e32 v42, v44
	v_cvt_f32_f16_sdwa v43, v44 dst_sel:DWORD dst_unused:UNUSED_PAD src0_sel:WORD_1
	v_cvt_f32_f16_e32 v44, v45
	v_cvt_f32_f16_sdwa v45, v45 dst_sel:DWORD dst_unused:UNUSED_PAD src0_sel:WORD_1
	v_pk_add_f32 v[82:83], v[82:83], v[84:85]
	s_waitcnt vmcnt(8)
	v_cvt_f32_f16_e32 v46, v48
	v_cvt_f32_f16_sdwa v47, v48 dst_sel:DWORD dst_unused:UNUSED_PAD src0_sel:WORD_1
	v_cvt_f32_f16_e32 v48, v49
	v_cvt_f32_f16_sdwa v49, v49 dst_sel:DWORD dst_unused:UNUSED_PAD src0_sel:WORD_1
	v_add_f32_e32 v82, v82, v83
	v_mov_b32_e32 v86, v35
	v_mov_b32_e32 v87, v37
	v_add_f32_dpp v82, v82, v82 quad_perm:[1,0,3,2] row_mask:0xf bank_mask:0xf bound_ctrl:1
	v_mov_b32_e32 v84, v34
	v_mov_b32_e32 v85, v36
	v_pk_mul_f32 v[86:87], v[86:87], v[86:87]
	v_mov_b32_e32 v88, v39
	v_mov_b32_e32 v89, v41
	v_add_f32_dpp v82, v82, v82 quad_perm:[2,3,0,1] row_mask:0xf bank_mask:0xf bound_ctrl:1
	v_pk_fma_f32 v[84:85], v[84:85], v[84:85], v[86:87]
	v_mov_b32_e32 v86, v38
	v_mov_b32_e32 v87, v40
	v_pk_mul_f32 v[88:89], v[88:89], v[88:89]
	v_add_f32_dpp v82, v82, v82 row_half_mirror row_mask:0xf bank_mask:0xf bound_ctrl:1
	v_pk_fma_f32 v[86:87], v[86:87], v[86:87], v[88:89]
	v_mul_f32_e32 v88, v43, v43
	v_mul_f32_e32 v90, v45, v45
	v_add_f32_dpp v82, v82, v82 row_mirror row_mask:0xf bank_mask:0xf bound_ctrl:1
	v_mov_b32_e32 v83, 0
	v_pk_add_f32 v[84:85], v[84:85], v[84:85] op_sel:[0,1] op_sel_hi:[1,0]
	v_pk_add_f32 v[86:87], v[86:87], v[86:87] op_sel:[0,1] op_sel_hi:[1,0]
	v_pk_fma_f32 v[88:89], v[42:43], v[42:43], v[88:89] op_sel_hi:[1,1,0]
	v_pk_fma_f32 v[90:91], v[44:45], v[44:45], v[90:91] op_sel_hi:[1,1,0]
	v_pk_mul_f32 v[92:93], v[46:47], v[46:47]
	v_pk_mul_f32 v[94:95], v[48:49], v[48:49]
	v_mov_b32_dpp v83, v82 row_bcast:15 row_mask:0xa bank_mask:0xf
	v_mov_b32_e32 v85, v92
	v_mov_b32_e32 v87, v93
	v_mov_b32_e32 v89, v94
	v_mov_b32_e32 v91, v95
	v_add_f32_e32 v82, v82, v83
	v_mov_b32_e32 v83, 0
	v_pk_add_f32 v[84:85], v[84:85], v[86:87]
	v_pk_add_f32 v[86:87], v[88:89], v[90:91]
	s_waitcnt vmcnt(7)
; template <int R, bool RT = false>
; __device__ __forceinline__ void norm_phase(const NormArgs& a, LAS unsigned char* lds, bool ctx_rows, const float* ctx_src, const float* ctx_shift, const float* ctx_scale) {
;     ...
;             float rstd[R];
; #pragma unroll
;             for (int q = 0; q < R; ++q) { float ss = 0.f;
; #pragma unroll
;                 for (int j = 0; j < 4; ++j) ss += (v[q][j][0] * v[q][j][0] + v[q][j][1] * v[q][j][1]) + (v[q][j][2] * v[q][j][2] + v[q][j][3] * v[q][j][3]);
;                 rstd[q] = __builtin_amdgcn_rsqf(wave_sum(ss) * (1.f / DM) + EPS);
;                 if constexpr (RT) rsel[q] = ((lane >> 4) == rr / 4) ? rstd[q] : rsel[q]; }
	v_cvt_f32_f16_e32 v50, v52
	v_cvt_f32_f16_sdwa v51, v52 dst_sel:DWORD dst_unused:UNUSED_PAD src0_sel:WORD_1
	v_cvt_f32_f16_e32 v52, v53
	v_cvt_f32_f16_sdwa v53, v53 dst_sel:DWORD dst_unused:UNUSED_PAD src0_sel:WORD_1
	v_mov_b32_dpp v83, v82 row_bcast:31 row_mask:0xc bank_mask:0xf
	v_pk_add_f32 v[84:85], v[84:85], v[86:87]
	s_waitcnt vmcnt(6)
	v_cvt_f32_f16_e32 v54, v56
	v_cvt_f32_f16_sdwa v55, v56 dst_sel:DWORD dst_unused:UNUSED_PAD src0_sel:WORD_1
	v_cvt_f32_f16_e32 v56, v57
	v_cvt_f32_f16_sdwa v57, v57 dst_sel:DWORD dst_unused:UNUSED_PAD src0_sel:WORD_1
	v_add_f32_e32 v82, v82, v83
	v_add_f32_e32 v83, v84, v85
	s_waitcnt vmcnt(5)
	v_cvt_f32_f16_e32 v58, v60
	v_cvt_f32_f16_sdwa v59, v60 dst_sel:DWORD dst_unused:UNUSED_PAD src0_sel:WORD_1
	v_add_f32_dpp v83, v83, v83 quad_perm:[1,0,3,2] row_mask:0xf bank_mask:0xf bound_ctrl:1
	v_cvt_f32_f16_e32 v60, v61
	v_cvt_f32_f16_sdwa v61, v61 dst_sel:DWORD dst_unused:UNUSED_PAD src0_sel:WORD_1
	v_add_f32_dpp v83, v83, v83 quad_perm:[2,3,0,1] row_mask:0xf bank_mask:0xf bound_ctrl:1
	s_waitcnt vmcnt(4)
	v_cvt_f32_f16_e32 v62, v64
	v_cvt_f32_f16_sdwa v63, v64 dst_sel:DWORD dst_unused:UNUSED_PAD src0_sel:WORD_1
	v_cvt_f32_f16_e32 v64, v65
	v_cvt_f32_f16_sdwa v65, v65 dst_sel:DWORD dst_unused:UNUSED_PAD src0_sel:WORD_1
	v_add_f32_dpp v83, v83, v83 row_half_mirror row_mask:0xf bank_mask:0xf bound_ctrl:1
	v_mov_b32_e32 v88, v51
	v_mov_b32_e32 v89, v53
	v_add_f32_dpp v83, v83, v83 row_mirror row_mask:0xf bank_mask:0xf bound_ctrl:1
	v_mov_b32_e32 v84, 0
	v_mov_b32_e32 v86, v50
	v_mov_b32_e32 v87, v52
	v_pk_mul_f32 v[88:89], v[88:89], v[88:89]
	v_mov_b32_e32 v90, v55
	v_mov_b32_e32 v91, v57
	v_mov_b32_dpp v84, v83 row_bcast:15 row_mask:0xa bank_mask:0xf
	v_pk_fma_f32 v[86:87], v[86:87], v[86:87], v[88:89]
	v_mov_b32_e32 v88, v54
	v_mov_b32_e32 v89, v56
	v_pk_mul_f32 v[90:91], v[90:91], v[90:91]
	v_add_f32_e32 v83, v83, v84
	v_mov_b32_e32 v84, 0
	v_pk_fma_f32 v[88:89], v[88:89], v[88:89], v[90:91]
	v_mul_f32_e32 v90, v59, v59
	v_mul_f32_e32 v92, v61, v61
	v_mov_b32_dpp v84, v83 row_bcast:31 row_mask:0xc bank_mask:0xf
	v_pk_add_f32 v[86:87], v[86:87], v[86:87] op_sel:[0,1] op_sel_hi:[1,0]
	v_pk_add_f32 v[88:89], v[88:89], v[88:89] op_sel:[0,1] op_sel_hi:[1,0]
	v_pk_fma_f32 v[90:91], v[58:59], v[58:59], v[90:91] op_sel_hi:[1,1,0]
	v_pk_fma_f32 v[92:93], v[60:61], v[60:61], v[92:93] op_sel_hi:[1,1,0]
	v_pk_mul_f32 v[94:95], v[62:63], v[62:63]
	v_pk_mul_f32 v[96:97], v[64:65], v[64:65]
	v_readlane_b32 s31, v82, 63
	v_add_f32_e32 v83, v83, v84
	v_mov_b32_e32 v87, v94
	v_mov_b32_e32 v89, v95
	v_mov_b32_e32 v91, v96
	v_mov_b32_e32 v93, v97
	v_fma_f32 v82, s31, v130, v129
	v_readlane_b32 s31, v83, 63
	v_pk_add_f32 v[86:87], v[86:87], v[88:89]
	v_pk_add_f32 v[88:89], v[90:91], v[92:93]
	s_waitcnt vmcnt(3)
	v_cvt_f32_f16_e32 v66, v68
	v_cvt_f32_f16_sdwa v67, v68 dst_sel:DWORD dst_unused:UNUSED_PAD src0_sel:WORD_1
	v_cvt_f32_f16_e32 v68, v69
	v_cvt_f32_f16_sdwa v69, v69 dst_sel:DWORD dst_unused:UNUSED_PAD src0_sel:WORD_1
	v_fma_f32 v83, s31, v130, v129
	v_pk_add_f32 v[86:87], v[86:87], v[88:89]
	s_waitcnt vmcnt(2)
	v_cvt_f32_f16_e32 v70, v72
	v_cvt_f32_f16_sdwa v71, v72 dst_sel:DWORD dst_unused:UNUSED_PAD src0_sel:WORD_1
	v_cvt_f32_f16_e32 v72, v73
	v_cvt_f32_f16_sdwa v73, v73 dst_sel:DWORD dst_unused:UNUSED_PAD src0_sel:WORD_1
	v_rsq_f32_e32 v84, v83
	v_add_f32_e32 v83, v86, v87
	s_waitcnt vmcnt(1)
	v_cvt_f32_f16_e32 v74, v76
	v_cvt_f32_f16_sdwa v75, v76 dst_sel:DWORD dst_unused:UNUSED_PAD src0_sel:WORD_1
	v_add_f32_dpp v83, v83, v83 quad_perm:[1,0,3,2] row_mask:0xf bank_mask:0xf bound_ctrl:1
	v_cvt_f32_f16_e32 v76, v77
	v_cvt_f32_f16_sdwa v77, v77 dst_sel:DWORD dst_unused:UNUSED_PAD src0_sel:WORD_1
	v_add_f32_dpp v83, v83, v83 quad_perm:[2,3,0,1] row_mask:0xf bank_mask:0xf bound_ctrl:1
	s_waitcnt vmcnt(0)
	v_cvt_f32_f16_e32 v78, v80
	v_cvt_f32_f16_sdwa v79, v80 dst_sel:DWORD dst_unused:UNUSED_PAD src0_sel:WORD_1
	v_cvt_f32_f16_e32 v80, v81
	v_cvt_f32_f16_sdwa v81, v81 dst_sel:DWORD dst_unused:UNUSED_PAD src0_sel:WORD_1
	v_add_f32_dpp v83, v83, v83 row_half_mirror row_mask:0xf bank_mask:0xf bound_ctrl:1
	v_mov_b32_e32 v90, v67
	v_mov_b32_e32 v91, v69
	v_add_f32_dpp v83, v83, v83 row_mirror row_mask:0xf bank_mask:0xf bound_ctrl:1
	v_mov_b32_e32 v85, 0
	v_mov_b32_e32 v88, v66
	v_mov_b32_e32 v89, v68
	v_pk_mul_f32 v[90:91], v[90:91], v[90:91]
	v_mov_b32_e32 v92, v71
	v_mov_b32_e32 v93, v73
	v_mov_b32_dpp v85, v83 row_bcast:15 row_mask:0xa bank_mask:0xf
	v_pk_fma_f32 v[88:89], v[88:89], v[88:89], v[90:91]
	v_mov_b32_e32 v90, v70
	v_mov_b32_e32 v91, v72
	v_pk_mul_f32 v[92:93], v[92:93], v[92:93]
	v_add_f32_e32 v83, v83, v85
	v_mov_b32_e32 v85, 0
	v_pk_fma_f32 v[90:91], v[90:91], v[90:91], v[92:93]
	v_mul_f32_e32 v92, v75, v75
	v_mul_f32_e32 v94, v77, v77
	v_mov_b32_dpp v85, v83 row_bcast:31 row_mask:0xc bank_mask:0xf
	v_pk_add_f32 v[88:89], v[88:89], v[88:89] op_sel:[0,1] op_sel_hi:[1,0]
	v_pk_add_f32 v[90:91], v[90:91], v[90:91] op_sel:[0,1] op_sel_hi:[1,0]
	v_pk_fma_f32 v[92:93], v[74:75], v[74:75], v[92:93] op_sel_hi:[1,1,0]
	v_pk_fma_f32 v[94:95], v[76:77], v[76:77], v[94:95] op_sel_hi:[1,1,0]
	v_pk_mul_f32 v[96:97], v[78:79], v[78:79]
	v_pk_mul_f32 v[134:135], v[80:81], v[80:81]
	v_add_f32_e32 v83, v83, v85
	v_mov_b32_e32 v89, v96
	v_mov_b32_e32 v91, v97
	v_mov_b32_e32 v93, v134
	v_mov_b32_e32 v95, v135
	v_readlane_b32 s31, v83, 63
	v_pk_add_f32 v[88:89], v[88:89], v[90:91]
	v_pk_add_f32 v[90:91], v[92:93], v[94:95]
	v_fma_f32 v83, s31, v130, v129
	v_pk_add_f32 v[88:89], v[88:89], v[90:91]
	v_rsq_f32_e32 v86, v83
	v_add_f32_e32 v83, v88, v89
	v_mov_b32_e32 v85, 0
	v_rsq_f32_e32 v82, v82
; __device__ __forceinline__ unsigned pkb(float lo, float hi) { f32x2 v = {lo, hi}; bf16x2_t b = __builtin_convertvector(v, bf16x2_t); return __builtin_bit_cast(unsigned, b); }
; template <int R, bool RT = false>
; __device__ __forceinline__ void norm_phase(const NormArgs& a, LAS unsigned char* lds, bool ctx_rows, const float* ctx_src, const float* ctx_shift, const float* ctx_scale) {
;     ...
; #pragma unroll
;             for (int q = 0; q < R; ++q) { const int row = row0 + rr + q;
; #pragma unroll
;                 for (int j = 0; j < 4; ++j) v[q][j] = (v[q][j] * rstd[q]) * A[j] + Sh[j];
;                 if (a.fout) {
; #pragma unroll
;                     for (int j = 0; j < 4; ++j) *(f32x4*)(a.fout + (size_t)row * DM + 4 * lane + 256 * j) = v[q][j];
;                 }
;                 if (a.hout) {
; #pragma unroll
;                     for (int j = 0; j < 4; ++j) { u32x2 w; if (a.hbf) { w.x = pkb(v[q][j][0], v[q][j][1]); w.y = pkb(v[q][j][2], v[q][j][3]); } else { w.x = pkh(v[q][j][0], v[q][j][1]); w.y = pkh(v[q][j][2], v[q][j][3]); } *(u32x2*)(a.hout + (size_t)row * DM + 4 * lane + 256 * j) = w; }
;                 }
	v_add_f32_dpp v83, v83, v83 quad_perm:[1,0,3,2] row_mask:0xf bank_mask:0xf bound_ctrl:1
	v_lshl_add_u64 v[90:91], v[102:103], 0, s[0:1]
	v_pk_mul_f32 v[50:51], v[50:51], v[86:87] op_sel_hi:[1,0]
	v_add_f32_dpp v83, v83, v83 quad_perm:[2,3,0,1] row_mask:0xf bank_mask:0xf bound_ctrl:1
	v_pk_mul_f32 v[52:53], v[52:53], v[86:87] op_sel_hi:[1,0]
	v_pk_fma_f32 v[50:51], v[114:115], v[50:51], v[2:3]
	v_add_f32_dpp v83, v83, v83 row_half_mirror row_mask:0xf bank_mask:0xf bound_ctrl:1
	v_pk_fma_f32 v[52:53], v[112:113], v[52:53], v[4:5]
	v_pk_mul_f32 v[54:55], v[54:55], v[86:87] op_sel_hi:[1,0]
	v_add_f32_dpp v83, v83, v83 row_mirror row_mask:0xf bank_mask:0xf bound_ctrl:1
	v_pk_mul_f32 v[56:57], v[56:57], v[86:87] op_sel_hi:[1,0]
	v_pk_fma_f32 v[54:55], v[118:119], v[54:55], v[6:7]
	v_mov_b32_dpp v85, v83 row_bcast:15 row_mask:0xa bank_mask:0xf
	v_add_f32_e32 v83, v83, v85
	v_mov_b32_e32 v85, 0
	v_pk_fma_f32 v[56:57], v[116:117], v[56:57], v[8:9]
	v_pk_mul_f32 v[58:59], v[58:59], v[86:87] op_sel_hi:[1,0]
	v_mov_b32_dpp v85, v83 row_bcast:31 row_mask:0xc bank_mask:0xf
	v_add_f32_e32 v83, v83, v85
	v_pk_mul_f32 v[34:35], v[34:35], v[84:85] op_sel_hi:[1,0]
	v_readlane_b32 s31, v83, 63
	v_pk_mul_f32 v[36:37], v[36:37], v[84:85] op_sel_hi:[1,0]
	v_pk_fma_f32 v[34:35], v[114:115], v[34:35], v[2:3]
	v_fma_f32 v83, s31, v130, v129
	v_pk_mul_f32 v[18:19], v[18:19], v[82:83] op_sel_hi:[1,0]
	v_pk_mul_f32 v[20:21], v[20:21], v[82:83] op_sel_hi:[1,0]
	v_pk_fma_f32 v[18:19], v[114:115], v[18:19], v[2:3]
	v_pk_fma_f32 v[20:21], v[112:113], v[20:21], v[4:5]
	v_pk_mul_f32 v[22:23], v[22:23], v[82:83] op_sel_hi:[1,0]
	v_pk_mul_f32 v[24:25], v[24:25], v[82:83] op_sel_hi:[1,0]
	v_rsq_f32_e32 v88, v83
	v_pk_fma_f32 v[24:25], v[116:117], v[24:25], v[8:9]
	v_pk_fma_f32 v[22:23], v[118:119], v[22:23], v[6:7]
	v_pk_mul_f32 v[26:27], v[26:27], v[82:83] op_sel_hi:[1,0]
	v_pk_mul_f32 v[28:29], v[28:29], v[82:83] op_sel_hi:[1,0]
	v_pk_mul_f32 v[30:31], v[30:31], v[82:83] op_sel_hi:[1,0]
	v_pk_mul_f32 v[32:33], v[32:33], v[82:83] op_sel_hi:[1,0]
	v_cvt_pk_bf16_f32 v82, v18, v19
	v_cvt_pk_bf16_f32 v83, v20, v21
	v_pk_fma_f32 v[28:29], v[120:121], v[28:29], v[12:13]
	v_pk_fma_f32 v[26:27], v[122:123], v[26:27], v[10:11]
	global_store_dwordx2 v[90:91], v[82:83], off sc0 sc1
	v_cvt_pk_bf16_f32 v82, v22, v23
	v_cvt_pk_bf16_f32 v83, v24, v25
	v_pk_fma_f32 v[32:33], v[124:125], v[32:33], v[16:17]
	v_pk_fma_f32 v[30:31], v[126:127], v[30:31], v[14:15]
	global_store_dwordx2 v[90:91], v[82:83], off offset:512 sc0 sc1
	v_cvt_pk_bf16_f32 v82, v26, v27
	v_cvt_pk_bf16_f32 v83, v28, v29
	global_store_dwordx2 v[90:91], v[82:83], off offset:1024 sc0 sc1
	v_cvt_pk_bf16_f32 v82, v30, v31
	v_cvt_pk_bf16_f32 v83, v32, v33
	v_pk_fma_f32 v[36:37], v[112:113], v[36:37], v[4:5]
	v_pk_mul_f32 v[38:39], v[38:39], v[84:85] op_sel_hi:[1,0]
	v_pk_mul_f32 v[40:41], v[40:41], v[84:85] op_sel_hi:[1,0]
	global_store_dwordx2 v[90:91], v[82:83], off offset:1536 sc0 sc1
	v_pk_fma_f32 v[40:41], v[116:117], v[40:41], v[8:9]
	v_pk_fma_f32 v[38:39], v[118:119], v[38:39], v[6:7]
	v_pk_mul_f32 v[42:43], v[42:43], v[84:85] op_sel_hi:[1,0]
	v_pk_mul_f32 v[44:45], v[44:45], v[84:85] op_sel_hi:[1,0]
	v_pk_mul_f32 v[46:47], v[46:47], v[84:85] op_sel_hi:[1,0]
	v_pk_mul_f32 v[48:49], v[48:49], v[84:85] op_sel_hi:[1,0]
	v_cvt_pk_bf16_f32 v82, v34, v35
	v_cvt_pk_bf16_f32 v83, v36, v37
	v_lshl_add_u64 v[84:85], v[102:103], 0, s[2:3]
	v_pk_fma_f32 v[44:45], v[120:121], v[44:45], v[12:13]
	v_pk_fma_f32 v[42:43], v[122:123], v[42:43], v[10:11]
	global_store_dwordx2 v[84:85], v[82:83], off sc0 sc1
	v_cvt_pk_bf16_f32 v82, v38, v39
	v_cvt_pk_bf16_f32 v83, v40, v41
	v_pk_fma_f32 v[48:49], v[124:125], v[48:49], v[16:17]
	v_pk_fma_f32 v[46:47], v[126:127], v[46:47], v[14:15]
	global_store_dwordx2 v[84:85], v[82:83], off offset:512 sc0 sc1
	v_cvt_pk_bf16_f32 v82, v42, v43
	v_cvt_pk_bf16_f32 v83, v44, v45
	global_store_dwordx2 v[84:85], v[82:83], off offset:1024 sc0 sc1
	v_cvt_pk_bf16_f32 v82, v46, v47
	v_cvt_pk_bf16_f32 v83, v48, v49
	global_store_dwordx2 v[84:85], v[82:83], off offset:1536 sc0 sc1
	v_pk_mul_f32 v[60:61], v[60:61], v[86:87] op_sel_hi:[1,0]
	v_cvt_pk_bf16_f32 v82, v50, v51
	v_cvt_pk_bf16_f32 v83, v52, v53
	v_lshl_add_u64 v[84:85], v[102:103], 0, s[18:19]
	v_pk_fma_f32 v[60:61], v[120:121], v[60:61], v[12:13]
	v_pk_fma_f32 v[58:59], v[122:123], v[58:59], v[10:11]
	v_pk_mul_f32 v[62:63], v[62:63], v[86:87] op_sel_hi:[1,0]
	v_pk_mul_f32 v[64:65], v[64:65], v[86:87] op_sel_hi:[1,0]
	global_store_dwordx2 v[84:85], v[82:83], off sc0 sc1
	v_cvt_pk_bf16_f32 v82, v54, v55
	v_cvt_pk_bf16_f32 v83, v56, v57
	v_pk_fma_f32 v[64:65], v[124:125], v[64:65], v[16:17]
	v_pk_fma_f32 v[62:63], v[126:127], v[62:63], v[14:15]
	global_store_dwordx2 v[84:85], v[82:83], off offset:512 sc0 sc1
	v_cvt_pk_bf16_f32 v82, v58, v59
	v_cvt_pk_bf16_f32 v83, v60, v61
	v_pk_mul_f32 v[66:67], v[66:67], v[88:89] op_sel_hi:[1,0]
	v_pk_mul_f32 v[68:69], v[68:69], v[88:89] op_sel_hi:[1,0]
	global_store_dwordx2 v[84:85], v[82:83], off offset:1024 sc0 sc1
	v_cvt_pk_bf16_f32 v82, v62, v63
	v_cvt_pk_bf16_f32 v83, v64, v65
	v_pk_fma_f32 v[68:69], v[112:113], v[68:69], v[4:5]
	v_pk_fma_f32 v[66:67], v[114:115], v[66:67], v[2:3]
	v_pk_mul_f32 v[70:71], v[70:71], v[88:89] op_sel_hi:[1,0]
	v_pk_mul_f32 v[72:73], v[72:73], v[88:89] op_sel_hi:[1,0]
	global_store_dwordx2 v[84:85], v[82:83], off offset:1536 sc0 sc1
	v_pk_fma_f32 v[72:73], v[116:117], v[72:73], v[8:9]
	v_pk_fma_f32 v[70:71], v[118:119], v[70:71], v[6:7]
	v_pk_mul_f32 v[74:75], v[74:75], v[88:89] op_sel_hi:[1,0]
	v_pk_mul_f32 v[76:77], v[76:77], v[88:89] op_sel_hi:[1,0]
	v_cvt_pk_bf16_f32 v82, v66, v67
	v_cvt_pk_bf16_f32 v83, v68, v69
	v_lshl_add_u64 v[84:85], v[102:103], 0, s[20:21]
	v_pk_fma_f32 v[76:77], v[120:121], v[76:77], v[12:13]
	v_pk_fma_f32 v[74:75], v[122:123], v[74:75], v[10:11]
	v_pk_mul_f32 v[78:79], v[78:79], v[88:89] op_sel_hi:[1,0]
	v_pk_mul_f32 v[80:81], v[80:81], v[88:89] op_sel_hi:[1,0]
	global_store_dwordx2 v[84:85], v[82:83], off sc0 sc1
	v_cvt_pk_bf16_f32 v82, v70, v71
	v_cvt_pk_bf16_f32 v83, v72, v73
	v_pk_fma_f32 v[80:81], v[124:125], v[80:81], v[16:17]
	v_pk_fma_f32 v[78:79], v[126:127], v[78:79], v[14:15]
	global_store_dwordx2 v[84:85], v[82:83], off offset:512 sc0 sc1
	v_cvt_pk_bf16_f32 v82, v74, v75
	v_cvt_pk_bf16_f32 v83, v76, v77
	global_store_dwordx2 v[84:85], v[82:83], off offset:1024 sc0 sc1
	v_cvt_pk_bf16_f32 v82, v78, v79
	v_cvt_pk_bf16_f32 v83, v80, v81
	global_store_dwordx2 v[84:85], v[82:83], off offset:1536 sc0 sc1
	s_cbranch_vccnz .LBB0_830
	s_mov_b64 s[0:1], 0
	s_branch .LBB0_834
